# rstd hoist + tail weight-converters (P1/P3/P13 idle WGs convert next weights; P0 shortened for layers 1-3) + hand-written SwiGLU epilogue
# speedup vs baseline: 1.0103x; 1.0103x over previous
; #define LAS __attribute__((address_space(3)))
; #define IN(k) in_range(lo, hi, (k))
; __global__ void __launch_bounds__(NWAVES * 64, 2) mk_fwd(Args args) {
;     ...
;     for (int l = 0; l < DEPTH; ++l) {
;         const int pb = 1 + l * NPH;
;         if (hi <= pb || lo >= pb + NPH) continue;
;         if (EN(0) && IN(pb + 0)) {
;             PH_LOCALS
;             LAS float* scr = (LAS float*)(lds + RING_OFF + wave * 16640);   static_assert(8 * 16640 <= LDSCTL_OFF, "converter scratch below the LDS control words");
;             constexpr int I_UP = (D / 64) * (NUP / 64), I_DN = (DFF / 64) * (D / 64), I_IN = (D / 64) * (DINP / 64), I_GLU = 16 * 16, I_L = 4 * 16, I_V1 = 16 * 4, I_V2 = 4 * 16,
;                           I_BS5 = 16 * 32, I_BAT = 8 * 32, I_BRW = 16 * 32, I_OUT = 32 * 32;
;             constexpr int NITEMS = 2 * I_UP + 2 * I_DN + I_IN + I_GLU + 3 * I_L + I_V1 + I_V2 + I_BS5 + I_BAT + I_BRW + I_OUT;
;             const int lv = l > 0 ? l - 1 : 0;
;     ...
;             for (int it = gw; it < NITEMS; it += NGW) {
;                 ConvItem ca; CONV_DESC(ca, it);
.LBB0_25:
	s_mul_i32 s6, s58, 15
	s_add_i32 s2, s6, 1
	s_cmp_gt_i32 s77, s2
	s_cselect_b64 s[0:1], -1, 0
	s_add_i32 s3, s6, 16
	s_cmp_lt_i32 s76, s3
	s_cselect_b64 s[4:5], -1, 0
	s_and_b64 s[0:1], s[0:1], s[4:5]
	s_andn2_b64 vcc, exec, s[0:1]
	s_cbranch_vccnz .LBB0_24
	v_writelane_b32 v254, s6, 36
	v_writelane_b32 v254, s3, 37
	s_mov_b32 s3, s2
	s_cmp_gt_i32 s76, s3
	s_cselect_b64 s[0:1], -1, 0
	s_cmp_ge_i32 s3, s77
	s_cselect_b64 s[4:5], -1, 0
	s_or_b64 s[0:1], s[0:1], s[4:5]
	v_writelane_b32 v254, s58, 38
	s_and_b64 vcc, exec, s[0:1]
	s_cbranch_vccnz .LBB0_92
	v_readlane_b32 s0, v254, 8
	v_readlane_b32 s4, v254, 10
	v_readlane_b32 s1, v254, 9
	v_mbcnt_lo_u32_b32 v11, -1, 0
	v_mbcnt_hi_u32_b32 v11, -1, v11
	s_load_dword s6, s[0:1], 0x0
	s_mov_b32 s3, s84
	s_waitcnt lgkmcnt(0)
	s_lshl_b32 s3, s3, 3
	v_readlane_b32 s0, v254, 0
	s_add_i32 s3, s3, s4
	v_readlane_b32 s98, v254, 38
	s_nop 3
	s_cmp_lt_u32 s98, 1
	s_cbranch_scc1 .Lmy_p0_full
	s_add_i32 s3, s3, 16768
.Lmy_p0_full:
	v_readlane_b32 s1, v254, 1
	s_cmpk_gt_i32 s3, 0x69bf
	s_cbranch_scc1 .LBB0_92
	s_load_dwordx2 s[8:9], s[0:1], 0x138
	v_readlane_b32 s14, v254, 38
	s_mulk_i32 s4, 0x4100
	s_add_i32 s7, s4, 0
	v_sub_u32_e64 v0, s14, 1 clamp
	s_lshl_b32 s33, s6, 3
	v_readfirstlane_b32 s4, v0
	s_lshl_b32 s96, s4, 16
	s_waitcnt lgkmcnt(0)
	s_add_u32 s4, s8, 0x22800000
	s_addc_u32 s5, s9, 0
	v_writelane_b32 v254, s4, 39
	s_mov_b32 s15, s97
	v_and_b32_e32 v0, 7, v11
	v_writelane_b32 v254, s5, 40
	s_add_u32 s4, s8, 0x22780000
	s_addc_u32 s5, s9, 0
	v_writelane_b32 v254, s4, 41
	v_ashrrev_i32_e32 v13, 3, v11
	v_lshlrev_b32_e32 v10, 3, v0
	v_writelane_b32 v254, s5, 42
	s_lshl_b32 s4, s14, 18
	s_add_u32 s10, s8, 0x22700000
	s_addc_u32 s11, s9, 0
	v_writelane_b32 v254, s10, 43
	s_mov_b32 s5, s97
	v_mul_u32_u24_e32 v0, 0x820, v0
	v_writelane_b32 v254, s11, 44
	s_mul_i32 s10, s14, 0x18000
	s_mov_b32 s11, s97
	v_writelane_b32 v254, s10, 45
	v_lshlrev_b32_e32 v1, 2, v13
	v_lshl_add_u32 v12, v11, 2, s7
	v_writelane_b32 v254, s11, 46
	s_add_u32 s10, s8, 0x22680000
	s_addc_u32 s11, s9, 0
	v_writelane_b32 v254, s10, 47
	v_add3_u32 v14, s7, v0, v1
	s_mov_b32 s41, s97
	v_writelane_b32 v254, s11, 48
	s_add_u32 s10, s8, 0x22600000
	s_addc_u32 s11, s9, 0
	v_writelane_b32 v254, s10, 49
	s_nop 1
	v_writelane_b32 v254, s11, 50
	s_lshl_b32 s10, s14, 20
	s_mov_b32 s11, s97
	v_writelane_b32 v254, s10, 51
	s_nop 1
	v_writelane_b32 v254, s11, 52
	s_add_u32 s10, s8, 0x22400000
	s_addc_u32 s11, s9, 0
	v_writelane_b32 v254, s10, 53
	s_nop 1
	v_writelane_b32 v254, s11, 54
	s_lshl_b32 s10, s14, 21
	s_mov_b32 s11, s97
	v_writelane_b32 v254, s10, 55
	s_nop 1
	v_writelane_b32 v254, s11, 56
	s_add_u32 s10, s8, 0x22e80000
	s_addc_u32 s11, s9, 0
	v_writelane_b32 v254, s10, 57
	s_nop 1
	v_writelane_b32 v254, s11, 58
	s_add_u32 s10, s8, 0x27b80000
	s_addc_u32 s11, s9, 0
	v_writelane_b32 v254, s10, 59
	s_nop 1
	v_writelane_b32 v254, s11, 60
	s_add_u32 s10, s8, 0x22880000
	s_addc_u32 s11, s9, 0
	v_writelane_b32 v254, s10, 61
	s_nop 1
	v_writelane_b32 v254, s11, 62
	s_lshl_b32 s10, s14, 22
	s_add_u32 s12, s8, 0x23280000
	s_addc_u32 s13, s9, 0
	v_writelane_b32 v254, s12, 63
	s_mov_b32 s11, s97
	s_nop 0
	v_writelane_b32 v255, s13, 0
	s_mul_i32 s12, s14, 0xac0000
	s_mov_b32 s13, s97
	v_writelane_b32 v255, s12, 1
	s_nop 1
	v_writelane_b32 v255, s13, 2
	s_add_u32 s12, s8, 0x26580000
	s_addc_u32 s13, s9, 0
	v_writelane_b32 v255, s12, 3
	s_nop 1
	v_writelane_b32 v255, s13, 4
	s_add_u32 s12, s8, 0x1d200000
	s_addc_u32 s13, s9, 0
	s_lshl_b32 s40, s14, 11
	v_writelane_b32 v255, s12, 5
	s_add_u32 s16, s8, 0x1e800000
	s_addc_u32 s17, s9, 0
	v_writelane_b32 v255, s13, 6
	v_writelane_b32 v255, s16, 7
	s_mul_i32 s12, s14, 0x1de0000
	s_mul_i32 s14, s14, 0x1580000
	v_writelane_b32 v255, s17, 8
	v_writelane_b32 v255, s14, 9
	s_mov_b32 s13, s97
	s_nop 0
	v_writelane_b32 v255, s15, 10
	s_add_u32 s14, s8, 0x23a80000
	s_addc_u32 s15, s9, 0
	v_writelane_b32 v255, s14, 11
	s_add_u32 s8, s8, 0x1a700000
	s_addc_u32 s9, s9, 0
	v_writelane_b32 v255, s15, 12
	v_writelane_b32 v255, s8, 13
	s_lshl_b64 s[4:5], s[4:5], 2
	s_lshl_b32 s7, s3, 4
	v_writelane_b32 v255, s9, 14
	v_writelane_b32 v255, s4, 15
	s_add_i32 s72, s7, 0xc00
	s_lshl_b32 s7, s3, 1
	v_writelane_b32 v255, s5, 16
	s_lshl_b64 s[4:5], s[10:11], 2
	v_writelane_b32 v255, s4, 17
	s_lshl_b32 s66, s3, 6
	s_lshl_b32 s67, s6, 9
	v_writelane_b32 v255, s5, 18
	s_lshl_b64 s[4:5], s[12:13], 2
	v_writelane_b32 v255, s4, 19
	s_lshl_b32 s68, s3, 5
	s_lshl_b32 s69, s6, 8
	v_writelane_b32 v255, s5, 20
	v_writelane_b32 v255, s80, 21
	s_lshl_b32 s70, s3, 2
	s_lshl_b32 s71, s6, 5
	v_writelane_b32 v255, s81, 22
	v_writelane_b32 v255, s82, 23
	s_lshl_b32 s73, s6, 7
	s_add_i32 s74, s7, 0x13500
	s_lshl_b32 s75, s6, 4
	v_writelane_b32 v255, s83, 24
	s_branch .LBB0_31

; __device__ __forceinline__ unsigned cvt_pk_bf16(float lo, float hi) { unsigned r; asm volatile("v_cvt_pk_bf16_f32 %0, %1, %2" : "=v"(r) : "v"(lo), "v"(hi)); return r; }
; __device__ __forceinline__ int fresh_lane() { int l; asm volatile("v_mbcnt_lo_u32_b32 %0, -1, 0\n\tv_mbcnt_hi_u32_b32 %0, -1, %0" : "=v"(l)); return l; }
; __device__ __forceinline__ void store16_wt(__amdgpu_buffer_rsrc_t rsrc, unsigned byte_off, v4u v) { __builtin_amdgcn_raw_buffer_store_b128(v, rsrc, byte_off, 0, 16); }
;     __device__ __forceinline__ void operator()(AccRef acc, const Unit& u, int wr, int wc, int, int) const {
;         const int ln_ = fresh_lane(), fr = ln_ & 15, fq = ln_ >> 4;
;         const int row0 = u.pm * 256 + wr * 64 + fr, col0 = u.pn * 128 + wc * 32 + 8 * fq;
;         const __amdgpu_buffer_rsrc_t rsrc = __builtin_amdgcn_make_buffer_rsrc((void*)H, 0, (int)((size_t)M * DFF * 2), 0x00020000);
;         float rs[8]; rows_rstd(ss, row0, fq, ln_, rs);
; #pragma unroll
;         for (int ai = 0; ai < 2; ++ai)
; #pragma unroll
;             for (int m = 0; m < 4; ++m) {
;                 const int row = row0 + ai * 128 + m * 16;
;                 const float r = rs[ai * 4 + m];
;                 float h[8];
; #pragma unroll
;                 for (int n = 0; n < 2; ++n)
; #pragma unroll
;                     for (int j = 0; j < 4; ++j) { const float a = acc[ai][0][m][n][j] * r, b = acc[ai][1][m][n][j] * r; h[4 * n + j] = a * __builtin_amdgcn_rcpf(1.0f + __expf(-a)) * b; }
;                 v4u w; w.x = cvt_pk_bf16(h[0], h[1]); w.y = cvt_pk_bf16(h[2], h[3]); w.z = cvt_pk_bf16(h[4], h[5]); w.w = cvt_pk_bf16(h[6], h[7]);
;                 store16_wt(rsrc, (unsigned)(((size_t)row * DFF + col0) * 2), w);
.LBB0_138:
	s_lshl_b32 s98, s6, 8
	v_mbcnt_lo_u32_b32 v130, -1, 0
	v_mbcnt_hi_u32_b32 v130, -1, v130
	s_add_i32 s98, s98, s37
	s_lshl_b32 s99, s7, 7
	s_or_b32 s99, s99, s39
	v_and_or_b32 v131, v130, 15, s98
	v_lshrrev_b32_e32 v132, 4, v130
	v_lshl_add_u32 v132, v132, 3, s99
	s_movk_i32 s98, 0x1580
	v_mul_lo_u32 v131, v131, s98
	v_readlane_b32 s20, v254, 15
	v_readlane_b32 s21, v254, 16
	v_readlane_b32 s22, v254, 17
	v_readlane_b32 s23, v254, 18
	v_add_lshl_u32 v131, v132, v131, 1
	v_mul_f32_e32 v126, v242, v126
	v_mul_f32_e32 v127, v242, v127
	v_mul_f32_e32 v128, v242, v128
	v_mul_f32_e32 v129, v242, v129
	v_mul_f32_e32 v118, v242, v118
	v_mul_f32_e32 v119, v242, v119
	v_mul_f32_e32 v120, v242, v120
	v_mul_f32_e32 v121, v242, v121
	v_mul_f32_e32 v122, v242, v122
	v_mul_f32_e32 v123, v242, v123
	v_mul_f32_e32 v124, v242, v124
	v_mul_f32_e32 v125, v242, v125
	v_mul_f32_e32 v114, v242, v114
	v_mul_f32_e32 v115, v242, v115
	v_mul_f32_e32 v116, v242, v116
	v_mul_f32_e32 v117, v242, v117
	v_mul_f32_e32 v140, 0xbfb8aa3b, v126
	v_mul_f32_e32 v141, 0xbfb8aa3b, v127
	v_mul_f32_e32 v142, 0xbfb8aa3b, v128
	v_mul_f32_e32 v143, 0xbfb8aa3b, v129
	v_mul_f32_e32 v144, 0xbfb8aa3b, v118
	v_mul_f32_e32 v145, 0xbfb8aa3b, v119
	v_mul_f32_e32 v146, 0xbfb8aa3b, v120
	v_mul_f32_e32 v147, 0xbfb8aa3b, v121
	v_exp_f32_e32 v140, v140
	v_exp_f32_e32 v141, v141
	v_exp_f32_e32 v142, v142
	v_exp_f32_e32 v143, v143
	v_exp_f32_e32 v144, v144
	v_exp_f32_e32 v145, v145
	v_exp_f32_e32 v146, v146
	v_exp_f32_e32 v147, v147
	v_add_f32_e32 v140, 1.0, v140
	v_add_f32_e32 v141, 1.0, v141
	v_add_f32_e32 v142, 1.0, v142
	v_add_f32_e32 v143, 1.0, v143
	v_add_f32_e32 v144, 1.0, v144
	v_add_f32_e32 v145, 1.0, v145
	v_add_f32_e32 v146, 1.0, v146
	v_add_f32_e32 v147, 1.0, v147
	v_rcp_f32_e32 v140, v140
	v_rcp_f32_e32 v141, v141
	v_rcp_f32_e32 v142, v142
	v_rcp_f32_e32 v143, v143
	v_rcp_f32_e32 v144, v144
	v_rcp_f32_e32 v145, v145
	v_rcp_f32_e32 v146, v146
	v_rcp_f32_e32 v147, v147
	v_mul_f32_e32 v126, v126, v140
	v_mul_f32_e32 v127, v127, v141
	v_mul_f32_e32 v128, v128, v142
	v_mul_f32_e32 v129, v129, v143
	v_mul_f32_e32 v118, v118, v144
	v_mul_f32_e32 v119, v119, v145
	v_mul_f32_e32 v120, v120, v146
	v_mul_f32_e32 v121, v121, v147
	v_mul_f32_e32 v126, v122, v126
	v_mul_f32_e32 v127, v123, v127
	v_mul_f32_e32 v128, v124, v128
	v_mul_f32_e32 v129, v125, v129
	v_mul_f32_e32 v118, v114, v118
	v_mul_f32_e32 v119, v115, v119
	v_mul_f32_e32 v120, v116, v120
	v_mul_f32_e32 v121, v117, v121
	v_cvt_pk_bf16_f32 v148, v126, v127
	v_cvt_pk_bf16_f32 v149, v128, v129
	v_cvt_pk_bf16_f32 v150, v118, v119
	v_cvt_pk_bf16_f32 v151, v120, v121
	v_mov_b32_e32 v133, v131
	buffer_store_dwordx4 v[148:151], v133, s[20:23], 0 offen sc1
	v_mul_f32_e32 v110, v243, v110
	v_mul_f32_e32 v111, v243, v111
	v_mul_f32_e32 v112, v243, v112
	v_mul_f32_e32 v113, v243, v113
	v_mul_f32_e32 v102, v243, v102
	v_mul_f32_e32 v103, v243, v103
	v_mul_f32_e32 v104, v243, v104
	v_mul_f32_e32 v105, v243, v105
	v_mul_f32_e32 v106, v243, v106
	v_mul_f32_e32 v107, v243, v107
	v_mul_f32_e32 v108, v243, v108
	v_mul_f32_e32 v109, v243, v109
	v_mul_f32_e32 v98, v243, v98
	v_mul_f32_e32 v99, v243, v99
	v_mul_f32_e32 v100, v243, v100
	v_mul_f32_e32 v101, v243, v101
	v_mul_f32_e32 v140, 0xbfb8aa3b, v110
	v_mul_f32_e32 v141, 0xbfb8aa3b, v111
	v_mul_f32_e32 v142, 0xbfb8aa3b, v112
	v_mul_f32_e32 v143, 0xbfb8aa3b, v113
	v_mul_f32_e32 v144, 0xbfb8aa3b, v102
	v_mul_f32_e32 v145, 0xbfb8aa3b, v103
	v_mul_f32_e32 v146, 0xbfb8aa3b, v104
	v_mul_f32_e32 v147, 0xbfb8aa3b, v105
	v_exp_f32_e32 v140, v140
	v_exp_f32_e32 v141, v141
	v_exp_f32_e32 v142, v142
	v_exp_f32_e32 v143, v143
	v_exp_f32_e32 v144, v144
	v_exp_f32_e32 v145, v145
	v_exp_f32_e32 v146, v146
	v_exp_f32_e32 v147, v147
	v_add_f32_e32 v140, 1.0, v140
	v_add_f32_e32 v141, 1.0, v141
	v_add_f32_e32 v142, 1.0, v142
	v_add_f32_e32 v143, 1.0, v143
	v_add_f32_e32 v144, 1.0, v144
	v_add_f32_e32 v145, 1.0, v145
	v_add_f32_e32 v146, 1.0, v146
	v_add_f32_e32 v147, 1.0, v147
	v_rcp_f32_e32 v140, v140
	v_rcp_f32_e32 v141, v141
	v_rcp_f32_e32 v142, v142
	v_rcp_f32_e32 v143, v143
	v_rcp_f32_e32 v144, v144
	v_rcp_f32_e32 v145, v145
	v_rcp_f32_e32 v146, v146
	v_rcp_f32_e32 v147, v147
	v_mul_f32_e32 v110, v110, v140
	v_mul_f32_e32 v111, v111, v141
	v_mul_f32_e32 v112, v112, v142
	v_mul_f32_e32 v113, v113, v143
	v_mul_f32_e32 v102, v102, v144
	v_mul_f32_e32 v103, v103, v145
	v_mul_f32_e32 v104, v104, v146
	v_mul_f32_e32 v105, v105, v147
	v_mul_f32_e32 v110, v106, v110
	v_mul_f32_e32 v111, v107, v111
	v_mul_f32_e32 v112, v108, v112
	v_mul_f32_e32 v113, v109, v113
	v_mul_f32_e32 v102, v98, v102
	v_mul_f32_e32 v103, v99, v103
	v_mul_f32_e32 v104, v100, v104
	v_mul_f32_e32 v105, v101, v105
	v_cvt_pk_bf16_f32 v152, v110, v111
	v_cvt_pk_bf16_f32 v153, v112, v113
	v_cvt_pk_bf16_f32 v154, v102, v103
	v_cvt_pk_bf16_f32 v155, v104, v105
	v_add_u32_e32 v133, 0x2b000, v131
	buffer_store_dwordx4 v[152:155], v133, s[20:23], 0 offen sc1
	v_mul_f32_e32 v94, v244, v94
	v_mul_f32_e32 v95, v244, v95
	v_mul_f32_e32 v96, v244, v96
	v_mul_f32_e32 v97, v244, v97
	v_mul_f32_e32 v86, v244, v86
	v_mul_f32_e32 v87, v244, v87
	v_mul_f32_e32 v88, v244, v88
	v_mul_f32_e32 v89, v244, v89
	v_mul_f32_e32 v90, v244, v90
	v_mul_f32_e32 v91, v244, v91
	v_mul_f32_e32 v92, v244, v92
	v_mul_f32_e32 v93, v244, v93
	v_mul_f32_e32 v82, v244, v82
	v_mul_f32_e32 v83, v244, v83
	v_mul_f32_e32 v84, v244, v84
	v_mul_f32_e32 v85, v244, v85
	v_mul_f32_e32 v140, 0xbfb8aa3b, v94
	v_mul_f32_e32 v141, 0xbfb8aa3b, v95
	v_mul_f32_e32 v142, 0xbfb8aa3b, v96
	v_mul_f32_e32 v143, 0xbfb8aa3b, v97
	v_mul_f32_e32 v144, 0xbfb8aa3b, v86
	v_mul_f32_e32 v145, 0xbfb8aa3b, v87
; __device__ __forceinline__ unsigned cvt_pk_bf16(float lo, float hi) { unsigned r; asm volatile("v_cvt_pk_bf16_f32 %0, %1, %2" : "=v"(r) : "v"(lo), "v"(hi)); return r; }
; __device__ __forceinline__ void store16_wt(__amdgpu_buffer_rsrc_t rsrc, unsigned byte_off, v4u v) { __builtin_amdgcn_raw_buffer_store_b128(v, rsrc, byte_off, 0, 16); }
;     __device__ __forceinline__ void operator()(AccRef acc, const Unit& u, int wr, int wc, int, int) const {
;     ...
;         for (int ai = 0; ai < 2; ++ai)
; #pragma unroll
;             for (int m = 0; m < 4; ++m) {
;                 const int row = row0 + ai * 128 + m * 16;
;                 const float r = rs[ai * 4 + m];
;                 float h[8];
; #pragma unroll
;                 for (int n = 0; n < 2; ++n)
; #pragma unroll
;                     for (int j = 0; j < 4; ++j) { const float a = acc[ai][0][m][n][j] * r, b = acc[ai][1][m][n][j] * r; h[4 * n + j] = a * __builtin_amdgcn_rcpf(1.0f + __expf(-a)) * b; }
;                 v4u w; w.x = cvt_pk_bf16(h[0], h[1]); w.y = cvt_pk_bf16(h[2], h[3]); w.z = cvt_pk_bf16(h[4], h[5]); w.w = cvt_pk_bf16(h[6], h[7]);
;                 store16_wt(rsrc, (unsigned)(((size_t)row * DFF + col0) * 2), w);
	v_mul_f32_e32 v146, 0xbfb8aa3b, v88
	v_mul_f32_e32 v147, 0xbfb8aa3b, v89
	v_exp_f32_e32 v140, v140
	v_exp_f32_e32 v141, v141
	v_exp_f32_e32 v142, v142
	v_exp_f32_e32 v143, v143
	v_exp_f32_e32 v144, v144
	v_exp_f32_e32 v145, v145
	v_exp_f32_e32 v146, v146
	v_exp_f32_e32 v147, v147
	v_add_f32_e32 v140, 1.0, v140
	v_add_f32_e32 v141, 1.0, v141
	v_add_f32_e32 v142, 1.0, v142
	v_add_f32_e32 v143, 1.0, v143
	v_add_f32_e32 v144, 1.0, v144
	v_add_f32_e32 v145, 1.0, v145
	v_add_f32_e32 v146, 1.0, v146
	v_add_f32_e32 v147, 1.0, v147
	v_rcp_f32_e32 v140, v140
	v_rcp_f32_e32 v141, v141
	v_rcp_f32_e32 v142, v142
	v_rcp_f32_e32 v143, v143
	v_rcp_f32_e32 v144, v144
	v_rcp_f32_e32 v145, v145
	v_rcp_f32_e32 v146, v146
	v_rcp_f32_e32 v147, v147
	v_mul_f32_e32 v94, v94, v140
	v_mul_f32_e32 v95, v95, v141
	v_mul_f32_e32 v96, v96, v142
	v_mul_f32_e32 v97, v97, v143
	v_mul_f32_e32 v86, v86, v144
	v_mul_f32_e32 v87, v87, v145
	v_mul_f32_e32 v88, v88, v146
	v_mul_f32_e32 v89, v89, v147
	v_mul_f32_e32 v94, v90, v94
	v_mul_f32_e32 v95, v91, v95
	v_mul_f32_e32 v96, v92, v96
	v_mul_f32_e32 v97, v93, v97
	v_mul_f32_e32 v86, v82, v86
	v_mul_f32_e32 v87, v83, v87
	v_mul_f32_e32 v88, v84, v88
	v_mul_f32_e32 v89, v85, v89
	v_cvt_pk_bf16_f32 v148, v94, v95
	v_cvt_pk_bf16_f32 v149, v96, v97
	v_cvt_pk_bf16_f32 v150, v86, v87
	v_cvt_pk_bf16_f32 v151, v88, v89
	v_add_u32_e32 v133, 0x56000, v131
	buffer_store_dwordx4 v[148:151], v133, s[20:23], 0 offen sc1
	v_mul_f32_e32 v78, v245, v78
	v_mul_f32_e32 v79, v245, v79
	v_mul_f32_e32 v80, v245, v80
	v_mul_f32_e32 v81, v245, v81
	v_mul_f32_e32 v70, v245, v70
	v_mul_f32_e32 v71, v245, v71
	v_mul_f32_e32 v72, v245, v72
	v_mul_f32_e32 v73, v245, v73
	v_mul_f32_e32 v74, v245, v74
	v_mul_f32_e32 v75, v245, v75
	v_mul_f32_e32 v76, v245, v76
	v_mul_f32_e32 v77, v245, v77
	v_mul_f32_e32 v66, v245, v66
	v_mul_f32_e32 v67, v245, v67
	v_mul_f32_e32 v68, v245, v68
	v_mul_f32_e32 v69, v245, v69
	v_mul_f32_e32 v140, 0xbfb8aa3b, v78
	v_mul_f32_e32 v141, 0xbfb8aa3b, v79
	v_mul_f32_e32 v142, 0xbfb8aa3b, v80
	v_mul_f32_e32 v143, 0xbfb8aa3b, v81
	v_mul_f32_e32 v144, 0xbfb8aa3b, v70
	v_mul_f32_e32 v145, 0xbfb8aa3b, v71
	v_mul_f32_e32 v146, 0xbfb8aa3b, v72
	v_mul_f32_e32 v147, 0xbfb8aa3b, v73
	v_exp_f32_e32 v140, v140
	v_exp_f32_e32 v141, v141
	v_exp_f32_e32 v142, v142
	v_exp_f32_e32 v143, v143
	v_exp_f32_e32 v144, v144
	v_exp_f32_e32 v145, v145
	v_exp_f32_e32 v146, v146
	v_exp_f32_e32 v147, v147
	v_add_f32_e32 v140, 1.0, v140
	v_add_f32_e32 v141, 1.0, v141
	v_add_f32_e32 v142, 1.0, v142
	v_add_f32_e32 v143, 1.0, v143
	v_add_f32_e32 v144, 1.0, v144
	v_add_f32_e32 v145, 1.0, v145
	v_add_f32_e32 v146, 1.0, v146
	v_add_f32_e32 v147, 1.0, v147
	v_rcp_f32_e32 v140, v140
	v_rcp_f32_e32 v141, v141
	v_rcp_f32_e32 v142, v142
	v_rcp_f32_e32 v143, v143
	v_rcp_f32_e32 v144, v144
	v_rcp_f32_e32 v145, v145
	v_rcp_f32_e32 v146, v146
	v_rcp_f32_e32 v147, v147
	v_mul_f32_e32 v78, v78, v140
	v_mul_f32_e32 v79, v79, v141
	v_mul_f32_e32 v80, v80, v142
	v_mul_f32_e32 v81, v81, v143
	v_mul_f32_e32 v70, v70, v144
	v_mul_f32_e32 v71, v71, v145
	v_mul_f32_e32 v72, v72, v146
	v_mul_f32_e32 v73, v73, v147
	v_mul_f32_e32 v78, v74, v78
	v_mul_f32_e32 v79, v75, v79
	v_mul_f32_e32 v80, v76, v80
	v_mul_f32_e32 v81, v77, v81
	v_mul_f32_e32 v70, v66, v70
	v_mul_f32_e32 v71, v67, v71
	v_mul_f32_e32 v72, v68, v72
	v_mul_f32_e32 v73, v69, v73
	v_cvt_pk_bf16_f32 v152, v78, v79
	v_cvt_pk_bf16_f32 v153, v80, v81
	v_cvt_pk_bf16_f32 v154, v70, v71
	v_cvt_pk_bf16_f32 v155, v72, v73
	v_add_u32_e32 v133, 0x81000, v131
	buffer_store_dwordx4 v[152:155], v133, s[20:23], 0 offen sc1
	v_mul_f32_e32 v62, v246, v62
	v_mul_f32_e32 v63, v246, v63
	v_mul_f32_e32 v64, v246, v64
	v_mul_f32_e32 v65, v246, v65
	v_mul_f32_e32 v54, v246, v54
	v_mul_f32_e32 v55, v246, v55
	v_mul_f32_e32 v56, v246, v56
	v_mul_f32_e32 v57, v246, v57
	v_mul_f32_e32 v58, v246, v58
	v_mul_f32_e32 v59, v246, v59
	v_mul_f32_e32 v60, v246, v60
	v_mul_f32_e32 v61, v246, v61
	v_mul_f32_e32 v50, v246, v50
	v_mul_f32_e32 v51, v246, v51
	v_mul_f32_e32 v52, v246, v52
	v_mul_f32_e32 v53, v246, v53
	v_mul_f32_e32 v140, 0xbfb8aa3b, v62
	v_mul_f32_e32 v141, 0xbfb8aa3b, v63
	v_mul_f32_e32 v142, 0xbfb8aa3b, v64
	v_mul_f32_e32 v143, 0xbfb8aa3b, v65
	v_mul_f32_e32 v144, 0xbfb8aa3b, v54
	v_mul_f32_e32 v145, 0xbfb8aa3b, v55
	v_mul_f32_e32 v146, 0xbfb8aa3b, v56
	v_mul_f32_e32 v147, 0xbfb8aa3b, v57
	v_exp_f32_e32 v140, v140
	v_exp_f32_e32 v141, v141
	v_exp_f32_e32 v142, v142
	v_exp_f32_e32 v143, v143
	v_exp_f32_e32 v144, v144
	v_exp_f32_e32 v145, v145
	v_exp_f32_e32 v146, v146
	v_exp_f32_e32 v147, v147
	v_add_f32_e32 v140, 1.0, v140
	v_add_f32_e32 v141, 1.0, v141
	v_add_f32_e32 v142, 1.0, v142
	v_add_f32_e32 v143, 1.0, v143
	v_add_f32_e32 v144, 1.0, v144
	v_add_f32_e32 v145, 1.0, v145
	v_add_f32_e32 v146, 1.0, v146
	v_add_f32_e32 v147, 1.0, v147
	v_rcp_f32_e32 v140, v140
	v_rcp_f32_e32 v141, v141
	v_rcp_f32_e32 v142, v142
	v_rcp_f32_e32 v143, v143
	v_rcp_f32_e32 v144, v144
	v_rcp_f32_e32 v145, v145
	v_rcp_f32_e32 v146, v146
	v_rcp_f32_e32 v147, v147
	v_mul_f32_e32 v62, v62, v140
	v_mul_f32_e32 v63, v63, v141
	v_mul_f32_e32 v64, v64, v142
	v_mul_f32_e32 v65, v65, v143
	v_mul_f32_e32 v54, v54, v144
	v_mul_f32_e32 v55, v55, v145
	v_mul_f32_e32 v56, v56, v146
	v_mul_f32_e32 v57, v57, v147
	v_mul_f32_e32 v62, v58, v62
	v_mul_f32_e32 v63, v59, v63
	v_mul_f32_e32 v64, v60, v64
	v_mul_f32_e32 v65, v61, v65
	v_mul_f32_e32 v54, v50, v54
	v_mul_f32_e32 v55, v51, v55
	v_mul_f32_e32 v56, v52, v56
	v_mul_f32_e32 v57, v53, v57
	v_cvt_pk_bf16_f32 v148, v62, v63
	v_cvt_pk_bf16_f32 v149, v64, v65
	v_cvt_pk_bf16_f32 v150, v54, v55
	v_cvt_pk_bf16_f32 v151, v56, v57
; __device__ __forceinline__ unsigned cvt_pk_bf16(float lo, float hi) { unsigned r; asm volatile("v_cvt_pk_bf16_f32 %0, %1, %2" : "=v"(r) : "v"(lo), "v"(hi)); return r; }
; __device__ __forceinline__ void store16_wt(__amdgpu_buffer_rsrc_t rsrc, unsigned byte_off, v4u v) { __builtin_amdgcn_raw_buffer_store_b128(v, rsrc, byte_off, 0, 16); }
;     __device__ __forceinline__ void operator()(AccRef acc, const Unit& u, int wr, int wc, int, int) const {
;     ...
;         for (int ai = 0; ai < 2; ++ai)
; #pragma unroll
;             for (int m = 0; m < 4; ++m) {
;                 const int row = row0 + ai * 128 + m * 16;
;                 const float r = rs[ai * 4 + m];
;                 float h[8];
; #pragma unroll
;                 for (int n = 0; n < 2; ++n)
; #pragma unroll
;                     for (int j = 0; j < 4; ++j) { const float a = acc[ai][0][m][n][j] * r, b = acc[ai][1][m][n][j] * r; h[4 * n + j] = a * __builtin_amdgcn_rcpf(1.0f + __expf(-a)) * b; }
;                 v4u w; w.x = cvt_pk_bf16(h[0], h[1]); w.y = cvt_pk_bf16(h[2], h[3]); w.z = cvt_pk_bf16(h[4], h[5]); w.w = cvt_pk_bf16(h[6], h[7]);
;                 store16_wt(rsrc, (unsigned)(((size_t)row * DFF + col0) * 2), w);
;             }
	v_add_u32_e32 v133, 0x158000, v131
	buffer_store_dwordx4 v[148:151], v133, s[20:23], 0 offen sc1
	v_mul_f32_e32 v46, v247, v46
	v_mul_f32_e32 v47, v247, v47
	v_mul_f32_e32 v48, v247, v48
	v_mul_f32_e32 v49, v247, v49
	v_mul_f32_e32 v38, v247, v38
	v_mul_f32_e32 v39, v247, v39
	v_mul_f32_e32 v40, v247, v40
	v_mul_f32_e32 v41, v247, v41
	v_mul_f32_e32 v42, v247, v42
	v_mul_f32_e32 v43, v247, v43
	v_mul_f32_e32 v44, v247, v44
	v_mul_f32_e32 v45, v247, v45
	v_mul_f32_e32 v34, v247, v34
	v_mul_f32_e32 v35, v247, v35
	v_mul_f32_e32 v36, v247, v36
	v_mul_f32_e32 v37, v247, v37
	v_mul_f32_e32 v140, 0xbfb8aa3b, v46
	v_mul_f32_e32 v141, 0xbfb8aa3b, v47
	v_mul_f32_e32 v142, 0xbfb8aa3b, v48
	v_mul_f32_e32 v143, 0xbfb8aa3b, v49
	v_mul_f32_e32 v144, 0xbfb8aa3b, v38
	v_mul_f32_e32 v145, 0xbfb8aa3b, v39
	v_mul_f32_e32 v146, 0xbfb8aa3b, v40
	v_mul_f32_e32 v147, 0xbfb8aa3b, v41
	v_exp_f32_e32 v140, v140
	v_exp_f32_e32 v141, v141
	v_exp_f32_e32 v142, v142
	v_exp_f32_e32 v143, v143
	v_exp_f32_e32 v144, v144
	v_exp_f32_e32 v145, v145
	v_exp_f32_e32 v146, v146
	v_exp_f32_e32 v147, v147
	v_add_f32_e32 v140, 1.0, v140
	v_add_f32_e32 v141, 1.0, v141
	v_add_f32_e32 v142, 1.0, v142
	v_add_f32_e32 v143, 1.0, v143
	v_add_f32_e32 v144, 1.0, v144
	v_add_f32_e32 v145, 1.0, v145
	v_add_f32_e32 v146, 1.0, v146
	v_add_f32_e32 v147, 1.0, v147
	v_rcp_f32_e32 v140, v140
	v_rcp_f32_e32 v141, v141
	v_rcp_f32_e32 v142, v142
	v_rcp_f32_e32 v143, v143
	v_rcp_f32_e32 v144, v144
	v_rcp_f32_e32 v145, v145
	v_rcp_f32_e32 v146, v146
	v_rcp_f32_e32 v147, v147
	v_mul_f32_e32 v46, v46, v140
	v_mul_f32_e32 v47, v47, v141
	v_mul_f32_e32 v48, v48, v142
	v_mul_f32_e32 v49, v49, v143
	v_mul_f32_e32 v38, v38, v144
	v_mul_f32_e32 v39, v39, v145
	v_mul_f32_e32 v40, v40, v146
	v_mul_f32_e32 v41, v41, v147
	v_mul_f32_e32 v46, v42, v46
	v_mul_f32_e32 v47, v43, v47
	v_mul_f32_e32 v48, v44, v48
	v_mul_f32_e32 v49, v45, v49
	v_mul_f32_e32 v38, v34, v38
	v_mul_f32_e32 v39, v35, v39
	v_mul_f32_e32 v40, v36, v40
	v_mul_f32_e32 v41, v37, v41
	v_cvt_pk_bf16_f32 v152, v46, v47
	v_cvt_pk_bf16_f32 v153, v48, v49
	v_cvt_pk_bf16_f32 v154, v38, v39
	v_cvt_pk_bf16_f32 v155, v40, v41
	v_add_u32_e32 v133, 0x183000, v131
	buffer_store_dwordx4 v[152:155], v133, s[20:23], 0 offen sc1
	v_mul_f32_e32 v30, v248, v30
	v_mul_f32_e32 v31, v248, v31
	v_mul_f32_e32 v32, v248, v32
	v_mul_f32_e32 v33, v248, v33
	v_mul_f32_e32 v22, v248, v22
	v_mul_f32_e32 v23, v248, v23
	v_mul_f32_e32 v24, v248, v24
	v_mul_f32_e32 v25, v248, v25
	v_mul_f32_e32 v26, v248, v26
	v_mul_f32_e32 v27, v248, v27
	v_mul_f32_e32 v28, v248, v28
	v_mul_f32_e32 v29, v248, v29
	v_mul_f32_e32 v18, v248, v18
	v_mul_f32_e32 v19, v248, v19
	v_mul_f32_e32 v20, v248, v20
	v_mul_f32_e32 v21, v248, v21
	v_mul_f32_e32 v140, 0xbfb8aa3b, v30
	v_mul_f32_e32 v141, 0xbfb8aa3b, v31
	v_mul_f32_e32 v142, 0xbfb8aa3b, v32
	v_mul_f32_e32 v143, 0xbfb8aa3b, v33
	v_mul_f32_e32 v144, 0xbfb8aa3b, v22
	v_mul_f32_e32 v145, 0xbfb8aa3b, v23
	v_mul_f32_e32 v146, 0xbfb8aa3b, v24
	v_mul_f32_e32 v147, 0xbfb8aa3b, v25
	v_exp_f32_e32 v140, v140
	v_exp_f32_e32 v141, v141
	v_exp_f32_e32 v142, v142
	v_exp_f32_e32 v143, v143
	v_exp_f32_e32 v144, v144
	v_exp_f32_e32 v145, v145
	v_exp_f32_e32 v146, v146
	v_exp_f32_e32 v147, v147
	v_add_f32_e32 v140, 1.0, v140
	v_add_f32_e32 v141, 1.0, v141
	v_add_f32_e32 v142, 1.0, v142
	v_add_f32_e32 v143, 1.0, v143
	v_add_f32_e32 v144, 1.0, v144
	v_add_f32_e32 v145, 1.0, v145
	v_add_f32_e32 v146, 1.0, v146
	v_add_f32_e32 v147, 1.0, v147
	v_rcp_f32_e32 v140, v140
	v_rcp_f32_e32 v141, v141
	v_rcp_f32_e32 v142, v142
	v_rcp_f32_e32 v143, v143
	v_rcp_f32_e32 v144, v144
	v_rcp_f32_e32 v145, v145
	v_rcp_f32_e32 v146, v146
	v_rcp_f32_e32 v147, v147
	v_mul_f32_e32 v30, v30, v140
	v_mul_f32_e32 v31, v31, v141
	v_mul_f32_e32 v32, v32, v142
	v_mul_f32_e32 v33, v33, v143
	v_mul_f32_e32 v22, v22, v144
	v_mul_f32_e32 v23, v23, v145
	v_mul_f32_e32 v24, v24, v146
	v_mul_f32_e32 v25, v25, v147
	v_mul_f32_e32 v30, v26, v30
	v_mul_f32_e32 v31, v27, v31
	v_mul_f32_e32 v32, v28, v32
	v_mul_f32_e32 v33, v29, v33
	v_mul_f32_e32 v22, v18, v22
	v_mul_f32_e32 v23, v19, v23
	v_mul_f32_e32 v24, v20, v24
	v_mul_f32_e32 v25, v21, v25
	v_cvt_pk_bf16_f32 v148, v30, v31
	v_cvt_pk_bf16_f32 v149, v32, v33
	v_cvt_pk_bf16_f32 v150, v22, v23
	v_cvt_pk_bf16_f32 v151, v24, v25
	v_add_u32_e32 v133, 0x1ae000, v131
	buffer_store_dwordx4 v[148:151], v133, s[20:23], 0 offen sc1
	v_mul_f32_e32 v14, v249, v14
	v_mul_f32_e32 v15, v249, v15
	v_mul_f32_e32 v16, v249, v16
	v_mul_f32_e32 v17, v249, v17
	v_mul_f32_e32 v4, v249, v4
	v_mul_f32_e32 v5, v249, v5
	v_mul_f32_e32 v6, v249, v6
	v_mul_f32_e32 v7, v249, v7
	v_mul_f32_e32 v10, v249, v10
	v_mul_f32_e32 v11, v249, v11
	v_mul_f32_e32 v12, v249, v12
	v_mul_f32_e32 v13, v249, v13
	v_mul_f32_e32 v0, v249, v0
	v_mul_f32_e32 v1, v249, v1
	v_mul_f32_e32 v2, v249, v2
	v_mul_f32_e32 v3, v249, v3
	v_mul_f32_e32 v140, 0xbfb8aa3b, v14
	v_mul_f32_e32 v141, 0xbfb8aa3b, v15
	v_mul_f32_e32 v142, 0xbfb8aa3b, v16
	v_mul_f32_e32 v143, 0xbfb8aa3b, v17
	v_mul_f32_e32 v144, 0xbfb8aa3b, v4
	v_mul_f32_e32 v145, 0xbfb8aa3b, v5
	v_mul_f32_e32 v146, 0xbfb8aa3b, v6
	v_mul_f32_e32 v147, 0xbfb8aa3b, v7
	v_exp_f32_e32 v140, v140
	v_exp_f32_e32 v141, v141
	v_exp_f32_e32 v142, v142
	v_exp_f32_e32 v143, v143
	v_exp_f32_e32 v144, v144
	v_exp_f32_e32 v145, v145
	v_exp_f32_e32 v146, v146
	v_exp_f32_e32 v147, v147
	v_add_f32_e32 v140, 1.0, v140
	v_add_f32_e32 v141, 1.0, v141
	v_add_f32_e32 v142, 1.0, v142
	v_add_f32_e32 v143, 1.0, v143
	v_add_f32_e32 v144, 1.0, v144
	v_add_f32_e32 v145, 1.0, v145
	v_add_f32_e32 v146, 1.0, v146
	v_add_f32_e32 v147, 1.0, v147
	v_rcp_f32_e32 v140, v140
	v_rcp_f32_e32 v141, v141
	v_rcp_f32_e32 v142, v142
	v_rcp_f32_e32 v143, v143
	v_rcp_f32_e32 v144, v144
	v_rcp_f32_e32 v145, v145
	v_rcp_f32_e32 v146, v146
	v_rcp_f32_e32 v147, v147
	v_mul_f32_e32 v14, v14, v140
	v_mul_f32_e32 v15, v15, v141
	v_mul_f32_e32 v16, v16, v142
	v_mul_f32_e32 v17, v17, v143
	v_mul_f32_e32 v4, v4, v144
	v_mul_f32_e32 v5, v5, v145
	v_mul_f32_e32 v6, v6, v146
	v_mul_f32_e32 v7, v7, v147
	v_mul_f32_e32 v14, v10, v14
	v_mul_f32_e32 v15, v11, v15
	v_mul_f32_e32 v16, v12, v16
	v_mul_f32_e32 v17, v13, v17
	v_mul_f32_e32 v4, v0, v4
	v_mul_f32_e32 v5, v1, v5
	v_mul_f32_e32 v6, v2, v6
	v_mul_f32_e32 v7, v3, v7
	v_cvt_pk_bf16_f32 v152, v14, v15
	v_cvt_pk_bf16_f32 v153, v16, v17
	v_cvt_pk_bf16_f32 v154, v4, v5
	v_cvt_pk_bf16_f32 v155, v6, v7
	v_add_u32_e32 v133, 0x1d9000, v131
	buffer_store_dwordx4 v[152:155], v133, s[20:23], 0 offen sc1
	s_mov_b64 s[6:7], -1
	s_andn2_b64 vcc, exec, s[4:5]
	s_cbranch_vccnz .LBB0_131
	s_andn2_b64 vcc, exec, s[0:1]
	s_cbranch_vccnz .LBB0_130
	s_barrier
	s_branch .LBB0_130

; #define LAS __attribute__((address_space(3)))
; __global__ void __launch_bounds__(NWAVES * 64, 2) mk_fwd(Args args) {
;     ...
;             PH_LOCALS
;             LAS float* scr = (LAS float*)(lds + RING_OFF + wave * 16640);   static_assert(8 * 16640 <= LDSCTL_OFF, "converter scratch below the LDS control words");
;             constexpr int I_UP = (D / 64) * (NUP / 64), I_DN = (DFF / 64) * (D / 64), I_IN = (D / 64) * (DINP / 64), I_GLU = 16 * 16, I_L = 4 * 16, I_V1 = 16 * 4, I_V2 = 4 * 16,
;                           I_BS5 = 16 * 32, I_BAT = 8 * 32, I_BRW = 16 * 32, I_OUT = 32 * 32;
;             constexpr int NITEMS = 2 * I_UP + 2 * I_DN + I_IN + I_GLU + 3 * I_L + I_V1 + I_V2 + I_BS5 + I_BAT + I_BRW + I_OUT;
;             const int lv = l > 0 ? l - 1 : 0;
;     ...
;             for (int it = gw; it < NITEMS; it += NGW) {
;                 ConvItem ca; CONV_DESC(ca, it);
.LBB0_142:
	v_readlane_b32 s99, v254, 35
	v_readlane_b32 s98, v254, 38
	s_nop 3
	s_cmp_lt_u32 s99, 96
	s_cbranch_scc1 .Lcvskip_p1
	s_cmp_lt_u32 s98, 1
	s_cbranch_scc1 .Lcvskip_p1
	v_mov_b32_e32 v250, v254
	v_mov_b32_e32 v251, v255
	v_writelane_b32 v252, s0, 0
	s_nop 0
	v_writelane_b32 v252, s1, 1
	s_nop 0
	v_writelane_b32 v252, s2, 2
	s_nop 0
	v_writelane_b32 v252, s3, 3
	s_nop 0
	v_writelane_b32 v252, s4, 4
	s_nop 0
	v_writelane_b32 v252, s5, 5
	s_nop 0
	v_writelane_b32 v252, s6, 6
	s_nop 0
	v_writelane_b32 v252, s7, 7
	s_nop 0
	v_writelane_b32 v252, s8, 8
	s_nop 0
	v_writelane_b32 v252, s9, 9
	s_nop 0
	v_writelane_b32 v252, s10, 10
	s_nop 0
	v_writelane_b32 v252, s11, 11
	s_nop 0
	v_writelane_b32 v252, s12, 12
	s_nop 0
	v_writelane_b32 v252, s13, 13
	s_nop 0
	v_writelane_b32 v252, s14, 14
	s_nop 0
	v_writelane_b32 v252, s15, 15
	s_nop 0
	v_writelane_b32 v252, s16, 16
	s_nop 0
	v_writelane_b32 v252, s17, 17
	s_nop 0
	v_writelane_b32 v252, s18, 18
	s_nop 0
	v_writelane_b32 v252, s19, 19
	s_nop 0
	v_writelane_b32 v252, s20, 20
	s_nop 0
	v_writelane_b32 v252, s21, 21
	s_nop 0
	v_writelane_b32 v252, s22, 22
	s_nop 0
	v_writelane_b32 v252, s23, 23
	s_nop 0
	v_writelane_b32 v252, s24, 24
	s_nop 0
	v_writelane_b32 v252, s25, 25
	s_nop 0
	v_writelane_b32 v252, s26, 26
	s_nop 0
	v_writelane_b32 v252, s27, 27
	s_nop 0
	v_writelane_b32 v252, s28, 28
	s_nop 0
	v_writelane_b32 v252, s29, 29
	s_nop 0
	v_writelane_b32 v252, s30, 30
	s_nop 0
	v_writelane_b32 v252, s31, 31
	s_nop 0
	v_writelane_b32 v252, s32, 32
	s_nop 0
	v_writelane_b32 v252, s33, 33
	s_nop 0
	v_writelane_b32 v252, s34, 34
	s_nop 0
	v_writelane_b32 v252, s35, 35
	s_nop 0
	v_writelane_b32 v252, s36, 36
	s_nop 0
	v_writelane_b32 v252, s37, 37
	s_nop 0
	v_writelane_b32 v252, s38, 38
	s_nop 0
	v_writelane_b32 v252, s39, 39
	s_nop 0
	v_writelane_b32 v252, s40, 40
	s_nop 0
	v_writelane_b32 v252, s41, 41
	s_nop 0
	v_writelane_b32 v252, s42, 42
	s_nop 0
	v_writelane_b32 v252, s43, 43
	s_nop 0
	v_writelane_b32 v252, s44, 44
	s_nop 0
	v_writelane_b32 v252, s45, 45
	s_nop 0
	v_writelane_b32 v252, s46, 46
	s_nop 0
	v_writelane_b32 v252, s47, 47
	s_nop 0
	v_writelane_b32 v252, s48, 48
	s_nop 0
	v_writelane_b32 v252, s49, 49
	s_nop 0
	v_writelane_b32 v252, s50, 50
	s_nop 0
	v_writelane_b32 v252, s51, 51
	s_nop 0
	v_writelane_b32 v252, s52, 52
	s_nop 0
	v_writelane_b32 v252, s53, 53
	s_nop 0
	v_writelane_b32 v252, s54, 54
	s_nop 0
	v_writelane_b32 v252, s55, 55
	s_nop 0
	v_writelane_b32 v252, s56, 56
	s_nop 0
	v_writelane_b32 v252, s57, 57
	s_nop 0
	v_writelane_b32 v252, s58, 58
	s_nop 0
	v_writelane_b32 v252, s59, 59
	s_nop 0
	v_writelane_b32 v252, s60, 60
	s_nop 0
	v_writelane_b32 v252, s61, 61
	s_nop 0
	v_writelane_b32 v252, s62, 62
	s_nop 0
	v_writelane_b32 v252, s63, 63
	s_nop 0
	v_writelane_b32 v253, s64, 0
	s_nop 0
	v_writelane_b32 v253, s65, 1
	s_nop 0
	v_writelane_b32 v253, s66, 2
	s_nop 0
	v_writelane_b32 v253, s67, 3
	s_nop 0
	v_writelane_b32 v253, s68, 4
	s_nop 0
	v_writelane_b32 v253, s69, 5
	s_nop 0
	v_writelane_b32 v253, s70, 6
	s_nop 0
	v_writelane_b32 v253, s71, 7
	s_nop 0
	v_writelane_b32 v253, s72, 8
	s_nop 0
	v_writelane_b32 v253, s73, 9
	s_nop 0
	v_writelane_b32 v253, s74, 10
	s_nop 0
	v_writelane_b32 v253, s75, 11
	s_nop 0
	v_writelane_b32 v253, s76, 12
	s_nop 0
	v_writelane_b32 v253, s77, 13
	s_nop 0
	v_writelane_b32 v253, s78, 14
	s_nop 0
	v_writelane_b32 v253, s79, 15
	s_nop 0
	v_writelane_b32 v253, s80, 16
	s_nop 0
	v_writelane_b32 v253, s81, 17
	s_nop 0
	v_writelane_b32 v253, s82, 18
	s_nop 0
	v_writelane_b32 v253, s83, 19
	s_nop 0
	v_writelane_b32 v253, s84, 20
	s_nop 0
	v_writelane_b32 v253, s85, 21
	s_nop 0
	v_writelane_b32 v253, s86, 22
	s_nop 0
	v_writelane_b32 v253, s87, 23
	s_nop 0
	v_writelane_b32 v253, s88, 24
	s_nop 0
	v_writelane_b32 v253, s89, 25
	s_nop 0
	v_writelane_b32 v253, s90, 26
	s_nop 0
	v_writelane_b32 v253, s91, 27
	s_nop 0
	v_writelane_b32 v253, s92, 28
	s_nop 0
	v_writelane_b32 v253, s93, 29
	s_nop 0
	v_writelane_b32 v253, s94, 30
	s_nop 0
	v_writelane_b32 v253, s95, 31
	s_nop 0
	v_writelane_b32 v253, s96, 32
	s_nop 0
	v_writelane_b32 v253, s97, 33
	s_nop 0
	v_writelane_b32 v253, vcc_lo, 34
	s_nop 0
	v_writelane_b32 v253, vcc_hi, 35
	s_nop 1
	v_readlane_b32 s84, v254, 35
	s_nop 3
	v_readlane_b32 s0, v254, 8
	v_readlane_b32 s4, v254, 10
	v_readlane_b32 s1, v254, 9
	v_mbcnt_lo_u32_b32 v11, -1, 0
	v_mbcnt_hi_u32_b32 v11, -1, v11
	s_load_dword s6, s[0:1], 0x0
	s_mov_b32 s3, s84
	s_waitcnt lgkmcnt(0)
	s_movk_i32 s6, 160
	s_lshl_b32 s3, s3, 3
	v_readlane_b32 s0, v254, 0
	s_add_i32 s3, s3, s4
	s_add_i32 s3, s3, 0x1280
	v_readlane_b32 s1, v254, 1
	s_cmpk_gt_i32 s3, 11007
	s_cbranch_scc1 .Lcvp10_ret
	s_load_dwordx2 s[8:9], s[0:1], 0x138
	v_readlane_b32 s14, v254, 38
	s_mulk_i32 s4, 0x4100
	s_add_i32 s7, s4, 0
	v_sub_u32_e64 v0, s14, 1 clamp
	s_lshl_b32 s33, s6, 3
	v_readfirstlane_b32 s4, v0
	s_lshl_b32 s96, s4, 16
	s_waitcnt lgkmcnt(0)
	s_add_u32 s4, s8, 0x22800000
	s_addc_u32 s5, s9, 0
	v_writelane_b32 v254, s4, 39
	s_mov_b32 s15, s97
	v_and_b32_e32 v0, 7, v11
	v_writelane_b32 v254, s5, 40
	s_add_u32 s4, s8, 0x22780000
	s_addc_u32 s5, s9, 0
	v_writelane_b32 v254, s4, 41
	v_ashrrev_i32_e32 v13, 3, v11
	v_lshlrev_b32_e32 v10, 3, v0
	v_writelane_b32 v254, s5, 42
	s_lshl_b32 s4, s14, 18
	s_add_u32 s10, s8, 0x22700000
	s_addc_u32 s11, s9, 0
	v_writelane_b32 v254, s10, 43
	s_mov_b32 s5, s97
	v_mul_u32_u24_e32 v0, 0x820, v0
	v_writelane_b32 v254, s11, 44
	s_mul_i32 s10, s14, 0x18000
	s_mov_b32 s11, s97
	v_writelane_b32 v254, s10, 45
	v_lshlrev_b32_e32 v1, 2, v13
	v_lshl_add_u32 v12, v11, 2, s7
	v_writelane_b32 v254, s11, 46
	s_add_u32 s10, s8, 0x22680000
	s_addc_u32 s11, s9, 0
	v_writelane_b32 v254, s10, 47
	v_add3_u32 v14, s7, v0, v1
	s_mov_b32 s41, s97
	v_writelane_b32 v254, s11, 48
	s_add_u32 s10, s8, 0x22600000
	s_addc_u32 s11, s9, 0
	v_writelane_b32 v254, s10, 49
	s_nop 1
	v_writelane_b32 v254, s11, 50
	s_lshl_b32 s10, s14, 20
	s_mov_b32 s11, s97
	v_writelane_b32 v254, s10, 51
	s_nop 1
	v_writelane_b32 v254, s11, 52
	s_add_u32 s10, s8, 0x22400000
	s_addc_u32 s11, s9, 0
	v_writelane_b32 v254, s10, 53
	s_nop 1
	v_writelane_b32 v254, s11, 54
	s_lshl_b32 s10, s14, 21
	s_mov_b32 s11, s97
	v_writelane_b32 v254, s10, 55
	s_nop 1
	v_writelane_b32 v254, s11, 56
	s_add_u32 s10, s8, 0x22e80000
	s_addc_u32 s11, s9, 0
	v_writelane_b32 v254, s10, 57
	s_nop 1
	v_writelane_b32 v254, s11, 58
	s_add_u32 s10, s8, 0x27b80000
	s_addc_u32 s11, s9, 0
	v_writelane_b32 v254, s10, 59
	s_nop 1
	v_writelane_b32 v254, s11, 60
	s_add_u32 s10, s8, 0x22880000
	s_addc_u32 s11, s9, 0
	v_writelane_b32 v254, s10, 61
	s_nop 1
	v_writelane_b32 v254, s11, 62
	s_lshl_b32 s10, s14, 22
	s_add_u32 s12, s8, 0x23280000
	s_addc_u32 s13, s9, 0
	v_writelane_b32 v254, s12, 63
	s_mov_b32 s11, s97
	s_nop 0
	v_writelane_b32 v255, s13, 0
	s_mul_i32 s12, s14, 0xac0000
	s_mov_b32 s13, s97
	v_writelane_b32 v255, s12, 1
	s_nop 1
	v_writelane_b32 v255, s13, 2
	s_add_u32 s12, s8, 0x26580000
	s_addc_u32 s13, s9, 0
	v_writelane_b32 v255, s12, 3
	s_nop 1
	v_writelane_b32 v255, s13, 4
	s_add_u32 s12, s8, 0x1d200000
	s_addc_u32 s13, s9, 0
	s_lshl_b32 s40, s14, 11
	v_writelane_b32 v255, s12, 5
	s_add_u32 s16, s8, 0x1e800000
	s_addc_u32 s17, s9, 0
	v_writelane_b32 v255, s13, 6
	v_writelane_b32 v255, s16, 7
	s_mul_i32 s12, s14, 0x1de0000
	s_mul_i32 s14, s14, 0x1580000
	v_writelane_b32 v255, s17, 8
	v_writelane_b32 v255, s14, 9
	s_mov_b32 s13, s97
	s_nop 0
	v_writelane_b32 v255, s15, 10
	s_add_u32 s14, s8, 0x23a80000
	s_addc_u32 s15, s9, 0
	v_writelane_b32 v255, s14, 11
	s_add_u32 s8, s8, 0x1a700000
	s_addc_u32 s9, s9, 0
	v_writelane_b32 v255, s15, 12
	v_writelane_b32 v255, s8, 13
	s_lshl_b64 s[4:5], s[4:5], 2
	s_lshl_b32 s7, s3, 4
	v_writelane_b32 v255, s9, 14
	v_writelane_b32 v255, s4, 15
	s_add_i32 s72, s7, 0xc00
	s_lshl_b32 s7, s3, 1
	v_writelane_b32 v255, s5, 16
	s_lshl_b64 s[4:5], s[10:11], 2
	v_writelane_b32 v255, s4, 17
	s_lshl_b32 s66, s3, 6
	s_lshl_b32 s67, s6, 9
	v_writelane_b32 v255, s5, 18
	s_lshl_b64 s[4:5], s[12:13], 2
	v_writelane_b32 v255, s4, 19
	s_lshl_b32 s68, s3, 5
	s_lshl_b32 s69, s6, 8
	v_writelane_b32 v255, s5, 20
	v_writelane_b32 v255, s80, 21
	s_lshl_b32 s70, s3, 2
	s_lshl_b32 s71, s6, 5
	v_writelane_b32 v255, s81, 22
	v_writelane_b32 v255, s82, 23
	s_lshl_b32 s73, s6, 7
	s_add_i32 s74, s7, 0x13500
	s_lshl_b32 s75, s6, 4
	v_writelane_b32 v255, s83, 24
	s_branch .Lcvp10_31

; #define LAS __attribute__((address_space(3)))
; __device__ __forceinline__ void conv_load(const ConvItem& ci, int lane, float (&v)[64]) {
;     const bool okc = ci.srcc >= 0 && (ci.srcc + lane) < ci.ncols;
;     const float* base = ci.W + (okc ? ci.srcc + lane : 0);
;     const int kmax = ci.Ksrc - 1;
; #pragma unroll
;     for (int i = 0; i < 64; ++i) { const int k = ci.k0 + i, kk = k < kmax ? k : kmax; v[i] = __builtin_nontemporal_load(base + (size_t)kk * ci.ldw); }
; #pragma unroll
;     for (int i = 0; i < 64; ++i) v[i] = (okc && (ci.k0 + i) < ci.Ksrc) ? v[i] : 0.f;
; }
; __device__ __forceinline__ void conv_store(const ConvItem& ci, LAS float* scr, int lane, const float (&v)[64]) {
;     const int c = lane & 7;
;     f32x4 s0 = {1.f, 1.f, 1.f, 1.f}, s1 = s0;
;     if (ci.ks) { const int kb = ci.k0 + 8 * c < ci.Ksrc - 8 ? ci.k0 + 8 * c : ci.Ksrc - 8; s0 = *(const f32x4*)(ci.ks + kb); s1 = *(const f32x4*)(ci.ks + kb + 4); }
; #pragma unroll
;     for (int i = 0; i < 64; ++i) scr[i * 65 + lane] = v[i];
.Lcvp10_30:
	s_cmp_lt_i32 s58, s76
	s_cselect_b64 s[4:5], -1, 0
	s_and_b64 s[4:5], vcc, s[4:5]
	s_cmp_lt_i32 s64, s76
	s_waitcnt vmcnt(62)
	v_cndmask_b32_e64 v21, 0, v21, s[4:5]
	s_cselect_b64 s[4:5], -1, 0
	s_and_b64 s[4:5], vcc, s[4:5]
	s_cmp_lt_i32 s65, s76
	v_cndmask_b32_e64 v20, 0, v20, s[4:5]
	s_cselect_b64 s[4:5], -1, 0
	s_and_b64 s[4:5], vcc, s[4:5]
	s_cmp_lt_i32 s78, s76
	s_waitcnt vmcnt(61)
	v_cndmask_b32_e64 v19, 0, v19, s[4:5]
	s_cselect_b64 s[4:5], -1, 0
	s_and_b64 s[4:5], vcc, s[4:5]
	s_cmp_lt_i32 s79, s76
	s_waitcnt vmcnt(60)
	v_cndmask_b32_e64 v18, 0, v18, s[4:5]
	s_cselect_b64 s[4:5], -1, 0
	s_and_b64 s[4:5], vcc, s[4:5]
	s_cmp_lt_i32 s80, s76
	s_waitcnt vmcnt(59)
	v_cndmask_b32_e64 v17, 0, v17, s[4:5]
	s_cselect_b64 s[4:5], -1, 0
	s_and_b64 s[4:5], vcc, s[4:5]
	s_cmp_lt_i32 s81, s76
	s_waitcnt vmcnt(58)
	v_cndmask_b32_e64 v16, 0, v16, s[4:5]
	s_cselect_b64 s[4:5], -1, 0
	s_and_b64 s[4:5], vcc, s[4:5]
	s_cmp_lt_i32 s82, s76
	s_waitcnt vmcnt(57)
	v_cndmask_b32_e64 v15, 0, v15, s[4:5]
	s_cselect_b64 s[4:5], -1, 0
	s_and_b64 s[4:5], vcc, s[4:5]
	s_cmp_lt_i32 s83, s76
	s_waitcnt vmcnt(56)
	v_cndmask_b32_e64 v8, 0, v8, s[4:5]
	s_cselect_b64 s[4:5], -1, 0
	s_and_b64 s[4:5], vcc, s[4:5]
	s_cmp_lt_i32 s85, s76
	s_waitcnt vmcnt(55)
	v_cndmask_b32_e64 v29, 0, v29, s[4:5]
	s_cselect_b64 s[4:5], -1, 0
	s_and_b64 s[4:5], vcc, s[4:5]
	s_cmp_lt_i32 s86, s76
	s_waitcnt vmcnt(54)
	v_cndmask_b32_e64 v28, 0, v28, s[4:5]
	s_cselect_b64 s[4:5], -1, 0
	s_and_b64 s[4:5], vcc, s[4:5]
	s_cmp_lt_i32 s87, s76
	s_waitcnt vmcnt(53)
	v_cndmask_b32_e64 v27, 0, v27, s[4:5]
	s_cselect_b64 s[4:5], -1, 0
	s_and_b64 s[4:5], vcc, s[4:5]
	s_cmp_lt_i32 s88, s76
	s_waitcnt vmcnt(52)
	v_cndmask_b32_e64 v26, 0, v26, s[4:5]
	s_cselect_b64 s[4:5], -1, 0
	s_and_b64 s[4:5], vcc, s[4:5]
	s_cmp_lt_i32 s89, s76
	s_waitcnt vmcnt(51)
	v_cndmask_b32_e64 v25, 0, v25, s[4:5]
	s_cselect_b64 s[4:5], -1, 0
	s_and_b64 s[4:5], vcc, s[4:5]
	s_cmp_lt_i32 s90, s76
	s_waitcnt vmcnt(50)
	v_cndmask_b32_e64 v24, 0, v24, s[4:5]
	s_cselect_b64 s[4:5], -1, 0
	s_and_b64 s[4:5], vcc, s[4:5]
	s_cmp_lt_i32 s92, s76
	s_waitcnt vmcnt(49)
	v_cndmask_b32_e64 v23, 0, v23, s[4:5]
	s_cselect_b64 s[4:5], -1, 0
	s_and_b64 s[4:5], vcc, s[4:5]
	s_cmp_lt_i32 s93, s76
	s_waitcnt vmcnt(48)
	v_cndmask_b32_e64 v22, 0, v22, s[4:5]
	s_cselect_b64 s[4:5], -1, 0
	s_and_b64 s[4:5], vcc, s[4:5]
	s_cmp_lt_i32 s94, s76
	s_waitcnt vmcnt(47)
	v_cndmask_b32_e64 v37, 0, v37, s[4:5]
	s_cselect_b64 s[4:5], -1, 0
	s_and_b64 s[4:5], vcc, s[4:5]
	s_cmp_lt_i32 s95, s76
	s_waitcnt vmcnt(46)
	v_cndmask_b32_e64 v36, 0, v36, s[4:5]
	s_cselect_b64 s[4:5], -1, 0
	s_and_b64 s[4:5], vcc, s[4:5]
	s_cmp_lt_i32 s50, s76
	s_waitcnt vmcnt(45)
	v_cndmask_b32_e64 v35, 0, v35, s[4:5]
	s_cselect_b64 s[4:5], -1, 0
	s_and_b64 s[4:5], vcc, s[4:5]
	s_cmp_lt_i32 s51, s76
	s_waitcnt vmcnt(44)
	v_cndmask_b32_e64 v34, 0, v34, s[4:5]
	s_cselect_b64 s[4:5], -1, 0
	s_and_b64 s[4:5], vcc, s[4:5]
	s_cmp_lt_i32 s52, s76
	s_waitcnt vmcnt(43)
	v_cndmask_b32_e64 v33, 0, v33, s[4:5]
	s_cselect_b64 s[4:5], -1, 0
	s_and_b64 s[4:5], vcc, s[4:5]
	s_cmp_lt_i32 s53, s76
	s_waitcnt vmcnt(42)
	v_cndmask_b32_e64 v32, 0, v32, s[4:5]
	s_cselect_b64 s[4:5], -1, 0
	s_and_b64 s[4:5], vcc, s[4:5]
	s_cmp_lt_i32 s6, s76
	s_waitcnt vmcnt(41)
	v_cndmask_b32_e64 v31, 0, v31, s[4:5]
	s_cselect_b64 s[4:5], -1, 0
	s_and_b64 s[4:5], vcc, s[4:5]
	s_cmp_lt_i32 s7, s76
	s_waitcnt vmcnt(40)
	v_cndmask_b32_e64 v30, 0, v30, s[4:5]
	s_cselect_b64 s[4:5], -1, 0
	s_and_b64 s[4:5], vcc, s[4:5]
	s_cmp_lt_i32 s8, s76
	s_waitcnt vmcnt(39)
	v_cndmask_b32_e64 v45, 0, v45, s[4:5]
	s_cselect_b64 s[4:5], -1, 0
	s_and_b64 s[4:5], vcc, s[4:5]
	s_cmp_lt_i32 s9, s76
	s_waitcnt vmcnt(38)
	v_cndmask_b32_e64 v44, 0, v44, s[4:5]
	s_cselect_b64 s[4:5], -1, 0
	s_and_b64 s[4:5], vcc, s[4:5]
	s_cmp_lt_i32 s10, s76
	s_waitcnt vmcnt(37)
	v_cndmask_b32_e64 v43, 0, v43, s[4:5]
	s_cselect_b64 s[4:5], -1, 0
	s_and_b64 s[4:5], vcc, s[4:5]
	s_cmp_lt_i32 s11, s76
	s_waitcnt vmcnt(36)
	v_cndmask_b32_e64 v42, 0, v42, s[4:5]
	s_cselect_b64 s[4:5], -1, 0
	s_and_b64 s[4:5], vcc, s[4:5]
	s_cmp_lt_i32 s14, s76
	s_waitcnt vmcnt(35)
	v_cndmask_b32_e64 v41, 0, v41, s[4:5]
	s_cselect_b64 s[4:5], -1, 0
	s_and_b64 s[4:5], vcc, s[4:5]
	s_cmp_lt_i32 s15, s76
	s_waitcnt vmcnt(34)
	v_cndmask_b32_e64 v40, 0, v40, s[4:5]
	s_cselect_b64 s[4:5], -1, 0
	s_and_b64 s[4:5], vcc, s[4:5]
	s_cmp_lt_i32 s16, s76
	s_waitcnt vmcnt(33)
	v_cndmask_b32_e64 v39, 0, v39, s[4:5]
	s_cselect_b64 s[4:5], -1, 0
	s_and_b64 s[4:5], vcc, s[4:5]
	s_cmp_lt_i32 s17, s76
	s_waitcnt vmcnt(32)
	v_cndmask_b32_e64 v38, 0, v38, s[4:5]
	s_cselect_b64 s[4:5], -1, 0
	s_and_b64 s[4:5], vcc, s[4:5]
	s_cmp_lt_i32 s12, s76
	s_waitcnt vmcnt(31)
	v_cndmask_b32_e64 v53, 0, v53, s[4:5]
	s_cselect_b64 s[4:5], -1, 0
	s_and_b64 s[4:5], vcc, s[4:5]
	s_cmp_lt_i32 s13, s76
	s_waitcnt vmcnt(30)
	v_cndmask_b32_e64 v52, 0, v52, s[4:5]
	s_cselect_b64 s[4:5], -1, 0
	s_and_b64 s[4:5], vcc, s[4:5]
	s_cmp_lt_i32 s20, s76
	s_waitcnt vmcnt(29)
	v_cndmask_b32_e64 v51, 0, v51, s[4:5]
	s_cselect_b64 s[4:5], -1, 0
	s_and_b64 s[4:5], vcc, s[4:5]
	s_cmp_lt_i32 s21, s76
	s_waitcnt vmcnt(28)
	v_cndmask_b32_e64 v50, 0, v50, s[4:5]
	s_cselect_b64 s[4:5], -1, 0
	s_and_b64 s[4:5], vcc, s[4:5]
	s_cmp_lt_i32 s24, s76
	s_waitcnt vmcnt(27)
	v_cndmask_b32_e64 v49, 0, v49, s[4:5]
	s_cselect_b64 s[4:5], -1, 0
	s_and_b64 s[4:5], vcc, s[4:5]
	s_cmp_lt_i32 s25, s76
	s_waitcnt vmcnt(26)
	v_cndmask_b32_e64 v48, 0, v48, s[4:5]
	s_cselect_b64 s[4:5], -1, 0
	s_and_b64 s[4:5], vcc, s[4:5]
	s_cmp_lt_i32 s26, s76
	s_waitcnt vmcnt(25)
	v_cndmask_b32_e64 v47, 0, v47, s[4:5]
	s_cselect_b64 s[4:5], -1, 0
	s_and_b64 s[4:5], vcc, s[4:5]
	s_cmp_lt_i32 s27, s76
	s_waitcnt vmcnt(24)
; __device__ __forceinline__ unsigned cvt_pk_bf16(float lo, float hi) { unsigned r; asm volatile("v_cvt_pk_bf16_f32 %0, %1, %2" : "=v"(r) : "v"(lo), "v"(hi)); return r; }
; #define LAS __attribute__((address_space(3)))
; #define LDS_WAIT() asm volatile("s_waitcnt lgkmcnt(0)" ::: "memory")
; __device__ __forceinline__ void conv_load(const ConvItem& ci, int lane, float (&v)[64]) {
;     ...
;     for (int i = 0; i < 64; ++i) v[i] = (okc && (ci.k0 + i) < ci.Ksrc) ? v[i] : 0.f;
; }
; __device__ __forceinline__ void conv_store(const ConvItem& ci, LAS float* scr, int lane, const float (&v)[64]) {
;     const int c = lane & 7;
;     f32x4 s0 = {1.f, 1.f, 1.f, 1.f}, s1 = s0;
;     if (ci.ks) { const int kb = ci.k0 + 8 * c < ci.Ksrc - 8 ? ci.k0 + 8 * c : ci.Ksrc - 8; s0 = *(const f32x4*)(ci.ks + kb); s1 = *(const f32x4*)(ci.ks + kb + 4); }
; #pragma unroll
;     for (int i = 0; i < 64; ++i) scr[i * 65 + lane] = v[i];
;     LDS_WAIT(); asm volatile("" ::: "memory");
; #pragma unroll
;     for (int j = 0; j < 8; ++j) { const int n = (lane >> 3) + 8 * j; const LAS float* s = scr + (8 * c) * 65 + n;
;         v4u o; o.x = cvt_pk_bf16(s[0 * 65] * s0[0], s[1 * 65] * s0[1]); o.y = cvt_pk_bf16(s[2 * 65] * s0[2], s[3 * 65] * s0[3]); o.z = cvt_pk_bf16(s[4 * 65] * s1[0], s[5 * 65] * s1[1]); o.w = cvt_pk_bf16(s[6 * 65] * s1[2], s[7 * 65] * s1[3]);
	v_cndmask_b32_e64 v46, 0, v46, s[4:5]
	s_cselect_b64 s[4:5], -1, 0
	s_and_b64 s[4:5], vcc, s[4:5]
	s_cmp_lt_i32 s18, s76
	s_waitcnt vmcnt(23)
	v_cndmask_b32_e64 v61, 0, v61, s[4:5]
	s_cselect_b64 s[4:5], -1, 0
	s_and_b64 s[4:5], vcc, s[4:5]
	s_cmp_lt_i32 s19, s76
	s_waitcnt vmcnt(22)
	v_cndmask_b32_e64 v60, 0, v60, s[4:5]
	s_cselect_b64 s[4:5], -1, 0
	s_and_b64 s[4:5], vcc, s[4:5]
	s_cmp_lt_i32 s28, s76
	s_waitcnt vmcnt(21)
	v_cndmask_b32_e64 v59, 0, v59, s[4:5]
	s_cselect_b64 s[4:5], -1, 0
	s_and_b64 s[4:5], vcc, s[4:5]
	s_cmp_lt_i32 s29, s76
	s_waitcnt vmcnt(20)
	v_cndmask_b32_e64 v58, 0, v58, s[4:5]
	s_cselect_b64 s[4:5], -1, 0
	s_and_b64 s[4:5], vcc, s[4:5]
	s_cmp_lt_i32 s22, s76
	s_waitcnt vmcnt(19)
	v_cndmask_b32_e64 v57, 0, v57, s[4:5]
	s_cselect_b64 s[4:5], -1, 0
	s_and_b64 s[4:5], vcc, s[4:5]
	s_cmp_lt_i32 s23, s76
	s_waitcnt vmcnt(18)
	v_cndmask_b32_e64 v56, 0, v56, s[4:5]
	s_cselect_b64 s[4:5], -1, 0
	s_and_b64 s[4:5], vcc, s[4:5]
	s_cmp_lt_i32 s30, s76
	s_waitcnt vmcnt(17)
	v_cndmask_b32_e64 v55, 0, v55, s[4:5]
	s_cselect_b64 s[4:5], -1, 0
	s_and_b64 s[4:5], vcc, s[4:5]
	s_cmp_lt_i32 s31, s76
	s_waitcnt vmcnt(16)
	v_cndmask_b32_e64 v54, 0, v54, s[4:5]
	s_cselect_b64 s[4:5], -1, 0
	s_and_b64 s[4:5], vcc, s[4:5]
	s_cmp_lt_i32 s36, s76
	s_waitcnt vmcnt(15)
	v_cndmask_b32_e64 v70, 0, v70, s[4:5]
	s_cselect_b64 s[4:5], -1, 0
	s_and_b64 s[4:5], vcc, s[4:5]
	s_cmp_lt_i32 s37, s76
	s_waitcnt vmcnt(14)
	v_cndmask_b32_e64 v69, 0, v69, s[4:5]
	s_cselect_b64 s[4:5], -1, 0
	s_and_b64 s[4:5], vcc, s[4:5]
	s_cmp_lt_i32 s38, s76
	s_waitcnt vmcnt(13)
	v_cndmask_b32_e64 v68, 0, v68, s[4:5]
	s_cselect_b64 s[4:5], -1, 0
	s_and_b64 s[4:5], vcc, s[4:5]
	s_cmp_lt_i32 s39, s76
	s_waitcnt vmcnt(12)
	v_cndmask_b32_e64 v67, 0, v67, s[4:5]
	s_cselect_b64 s[4:5], -1, 0
	s_and_b64 s[4:5], vcc, s[4:5]
	s_cmp_lt_i32 s34, s76
	s_waitcnt vmcnt(11)
	v_cndmask_b32_e64 v66, 0, v66, s[4:5]
	s_cselect_b64 s[4:5], -1, 0
	s_and_b64 s[4:5], vcc, s[4:5]
	s_cmp_lt_i32 s35, s76
	s_waitcnt vmcnt(10)
	v_cndmask_b32_e64 v64, 0, v64, s[4:5]
	s_cselect_b64 s[4:5], -1, 0
	s_and_b64 s[4:5], vcc, s[4:5]
	s_cmp_lt_i32 s42, s76
	s_waitcnt vmcnt(9)
	v_cndmask_b32_e64 v63, 0, v63, s[4:5]
	s_cselect_b64 s[4:5], -1, 0
	s_and_b64 s[4:5], vcc, s[4:5]
	s_cmp_lt_i32 s43, s76
	s_waitcnt vmcnt(8)
	v_cndmask_b32_e64 v62, 0, v62, s[4:5]
	s_cselect_b64 s[4:5], -1, 0
	s_and_b64 s[4:5], vcc, s[4:5]
	s_cmp_lt_i32 s54, s76
	s_waitcnt vmcnt(7)
	v_cndmask_b32_e64 v65, 0, v65, s[4:5]
	s_cselect_b64 s[4:5], -1, 0
	s_and_b64 s[4:5], vcc, s[4:5]
	s_cmp_lt_i32 s55, s76
	s_waitcnt vmcnt(6)
	v_cndmask_b32_e64 v74, 0, v74, s[4:5]
	s_cselect_b64 s[4:5], -1, 0
	s_and_b64 s[4:5], vcc, s[4:5]
	s_cmp_lt_i32 s46, s76
	ds_write2_b32 v12, v21, v20 offset1:65
	ds_write2_b32 v12, v19, v18 offset0:130 offset1:195
	v_add_u32_e32 v18, 0x400, v12
	s_waitcnt vmcnt(5)
	v_cndmask_b32_e64 v73, 0, v73, s[4:5]
	s_cselect_b64 s[4:5], -1, 0
	ds_write2_b32 v18, v17, v16 offset0:4 offset1:69
	ds_write2_b32 v18, v15, v8 offset0:134 offset1:199
	v_add_u32_e32 v8, 0x800, v12
	s_and_b64 s[4:5], vcc, s[4:5]
	ds_write2_b32 v8, v29, v28 offset0:8 offset1:73
	ds_write2_b32 v8, v27, v26 offset0:138 offset1:203
	v_add_u32_e32 v8, 0xc00, v12
	s_cmp_lt_i32 s47, s76
	ds_write2_b32 v8, v25, v24 offset0:12 offset1:77
	ds_write2_b32 v8, v23, v22 offset0:142 offset1:207
	v_add_u32_e32 v8, 0x1000, v12
	s_waitcnt vmcnt(4)
	v_cndmask_b32_e64 v72, 0, v72, s[4:5]
	s_cselect_b64 s[4:5], -1, 0
	ds_write2_b32 v8, v37, v36 offset0:16 offset1:81
	ds_write2_b32 v8, v35, v34 offset0:146 offset1:211
	v_add_u32_e32 v8, 0x1400, v12
	s_and_b64 s[4:5], vcc, s[4:5]
	ds_write2_b32 v8, v33, v32 offset0:20 offset1:85
	ds_write2_b32 v8, v31, v30 offset0:150 offset1:215
	v_add_u32_e32 v8, 0x1800, v12
	s_cmp_lt_i32 s48, s76
	ds_write2_b32 v8, v45, v44 offset0:24 offset1:89
	ds_write2_b32 v8, v43, v42 offset0:154 offset1:219
	v_add_u32_e32 v8, 0x1c00, v12
	s_waitcnt vmcnt(3)
	v_cndmask_b32_e64 v71, 0, v71, s[4:5]
	s_cselect_b64 s[4:5], -1, 0
	ds_write2_b32 v8, v41, v40 offset0:28 offset1:93
	ds_write2_b32 v8, v39, v38 offset0:158 offset1:223
	v_add_u32_e32 v8, 0x2000, v12
	s_and_b64 s[4:5], vcc, s[4:5]
	ds_write2_b32 v8, v53, v52 offset0:32 offset1:97
	ds_write2_b32 v8, v51, v50 offset0:162 offset1:227
	v_add_u32_e32 v8, 0x2400, v12
	s_cmp_lt_i32 s49, s76
	ds_write2_b32 v8, v49, v48 offset0:36 offset1:101
	ds_write2_b32 v8, v47, v46 offset0:166 offset1:231
	v_add_u32_e32 v8, 0x2800, v12
	s_waitcnt vmcnt(2)
	v_cndmask_b32_e64 v77, 0, v77, s[4:5]
	s_cselect_b64 s[4:5], -1, 0
	ds_write2_b32 v8, v61, v60 offset0:40 offset1:105
	ds_write2_b32 v8, v59, v58 offset0:170 offset1:235
	v_add_u32_e32 v8, 0x2c00, v12
	s_and_b64 s[4:5], vcc, s[4:5]
	ds_write2_b32 v8, v57, v56 offset0:44 offset1:109
	ds_write2_b32 v8, v55, v54 offset0:174 offset1:239
	v_add_u32_e32 v8, 0x3000, v12
	s_cmp_lt_i32 s44, s76
	ds_write2_b32 v8, v70, v69 offset0:48 offset1:113
	ds_write2_b32 v8, v68, v67 offset0:178 offset1:243
	v_add_u32_e32 v8, 0x3400, v12
	s_waitcnt vmcnt(1)
	v_cndmask_b32_e64 v76, 0, v76, s[4:5]
	s_cselect_b64 s[4:5], -1, 0
	ds_write2_b32 v8, v66, v64 offset0:52 offset1:117
	ds_write2_b32 v8, v63, v62 offset0:182 offset1:247
	v_add_u32_e32 v8, 0x3800, v12
	s_and_b64 vcc, vcc, s[4:5]
	ds_write2_b32 v8, v65, v74 offset0:56 offset1:121
	ds_write2_b32 v8, v73, v72 offset0:186 offset1:251
	v_add_u32_e32 v8, 0x3c00, v12
	s_waitcnt vmcnt(0)
	v_cndmask_b32_e32 v75, 0, v75, vcc
	ds_write2_b32 v8, v71, v77 offset0:60 offset1:125
	ds_write2_b32 v8, v76, v75 offset0:190 offset1:255
	s_waitcnt lgkmcnt(0)
	ds_read2_b32 v[16:17], v14 offset1:65
	v_add_u32_e32 v24, s59, v13
	v_mul_lo_u32 v22, s57, v24
	s_ashr_i32 s59, s58, 31
	v_readlane_b32 s76, v254, 31
	s_waitcnt lgkmcnt(0)
; __device__ __forceinline__ unsigned cvt_pk_bf16(float lo, float hi) { unsigned r; asm volatile("v_cvt_pk_bf16_f32 %0, %1, %2" : "=v"(r) : "v"(lo), "v"(hi)); return r; }
; #define LAS __attribute__((address_space(3)))
; __device__ __forceinline__ void conv_store(const ConvItem& ci, LAS float* scr, int lane, const float (&v)[64]) {
;     ...
; #pragma unroll
;     for (int j = 0; j < 8; ++j) { const int n = (lane >> 3) + 8 * j; const LAS float* s = scr + (8 * c) * 65 + n;
;         v4u o; o.x = cvt_pk_bf16(s[0 * 65] * s0[0], s[1 * 65] * s0[1]); o.y = cvt_pk_bf16(s[2 * 65] * s0[2], s[3 * 65] * s0[3]); o.z = cvt_pk_bf16(s[4 * 65] * s1[0], s[5 * 65] * s1[1]); o.w = cvt_pk_bf16(s[6 * 65] * s1[2], s[7 * 65] * s1[3]);
;         *(v4u*)(ci.dst + (size_t)(ci.drow0 + n) * ci.ldd + ci.k0 + 8 * c) = o; }
	v_mul_f32_e32 v8, v4, v16
	v_mul_f32_e32 v15, v5, v17
	v_cvt_pk_bf16_f32 v16, v8, v15
	ds_read2_b32 v[18:19], v14 offset0:130 offset1:195
	s_add_i32 s3, s3, s33
	s_add_i32 s66, s66, s67
	s_add_i32 s68, s68, s69
	s_add_i32 s70, s70, s71
	s_waitcnt lgkmcnt(0)
	v_mul_f32_e32 v15, v7, v19
	v_mul_f32_e32 v8, v6, v18
	v_cvt_pk_bf16_f32 v17, v8, v15
	v_add_u32_e32 v15, 0x400, v14
	ds_read2_b32 v[18:19], v15 offset0:4 offset1:69
	s_add_i32 s72, s72, s73
	s_add_i32 s74, s74, s75
	v_readlane_b32 s78, v254, 33
	v_readlane_b32 s79, v254, 34
	s_waitcnt lgkmcnt(0)
	v_mul_f32_e32 v8, v0, v18
	v_mul_f32_e32 v18, v1, v19
	v_cvt_pk_bf16_f32 v18, v8, v18
	ds_read2_b32 v[20:21], v15 offset0:134 offset1:199
	v_readlane_b32 s80, v255, 21
	v_readlane_b32 s77, v254, 32
	s_movk_i32 s78, 0x1580
	v_readlane_b32 s82, v255, 23
	s_waitcnt lgkmcnt(0)
	v_mul_f32_e32 v8, v2, v20
	v_mul_f32_e32 v19, v3, v21
	v_cvt_pk_bf16_f32 v19, v8, v19
	v_ashrrev_i32_e32 v8, 31, v24
	v_mul_lo_u32 v8, s56, v8
	v_mad_u64_u32 v[20:21], s[4:5], s56, v24, 0
	v_add3_u32 v21, v21, v8, v22
	ds_read2_b32 v[22:23], v14 offset0:8 offset1:73
	v_lshl_add_u64 v[20:21], v[20:21], 1, s[60:61]
	s_lshl_b64 s[4:5], s[58:59], 1
	v_lshl_add_u64 v[20:21], v[20:21], 0, s[4:5]
	v_lshlrev_b32_e32 v8, 1, v10
	v_lshl_add_u64 v[20:21], v[20:21], 0, v[8:9]
	global_store_dwordx4 v[20:21], v[16:19], off
	s_cmpk_lt_i32 s3, 11008
	v_readlane_b32 s83, v255, 24
	s_waitcnt lgkmcnt(0)
	v_mul_f32_e32 v16, v4, v22
	v_mul_f32_e32 v17, v5, v23
	v_cvt_pk_bf16_f32 v16, v16, v17
	ds_read2_b32 v[18:19], v14 offset0:138 offset1:203
	s_mov_b32 s79, 0x3f22f983
	s_mov_b32 s85, 0xbfc90fda
	s_brev_b32 s86, 1
	s_movk_i32 s87, 0x1f8
	s_waitcnt lgkmcnt(0)
	v_mul_f32_e32 v17, v6, v18
	v_mul_f32_e32 v18, v7, v19
	v_cvt_pk_bf16_f32 v17, v17, v18
	ds_read2_b32 v[18:19], v15 offset0:12 offset1:77
	s_mov_b64 s[88:89], 0x80
	s_mov_b64 s[92:93], 0x4000
	s_mov_b64 s[94:95], 0x4800
	v_readlane_b32 s81, v255, 22
	s_waitcnt lgkmcnt(0)
	v_mul_f32_e32 v18, v0, v18
	v_mul_f32_e32 v19, v1, v19
	v_cvt_pk_bf16_f32 v18, v18, v19
	ds_read2_b32 v[20:21], v15 offset0:142 offset1:207
	s_waitcnt lgkmcnt(0)
	v_mul_f32_e32 v19, v2, v20
	v_mul_f32_e32 v20, v3, v21
	v_cvt_pk_bf16_f32 v19, v19, v20
	v_add_u32_e32 v20, 8, v24
	v_ashrrev_i32_e32 v21, 31, v20
	v_mul_lo_u32 v22, s56, v21
	v_mul_lo_u32 v23, s57, v20
	v_mad_u64_u32 v[20:21], s[6:7], s56, v20, 0
	v_add3_u32 v21, v21, v22, v23
	ds_read2_b32 v[22:23], v14 offset0:16 offset1:81
	v_lshl_add_u64 v[20:21], v[20:21], 1, s[60:61]
	v_lshl_add_u64 v[20:21], v[20:21], 0, s[4:5]
	v_lshl_add_u64 v[20:21], v[20:21], 0, v[8:9]
	global_store_dwordx4 v[20:21], v[16:19], off
	s_waitcnt lgkmcnt(0)
	s_nop 0
	v_mul_f32_e32 v16, v4, v22
	v_mul_f32_e32 v17, v5, v23
	v_cvt_pk_bf16_f32 v16, v16, v17
	ds_read2_b32 v[18:19], v14 offset0:146 offset1:211
	s_waitcnt lgkmcnt(0)
	v_mul_f32_e32 v17, v6, v18
	v_mul_f32_e32 v18, v7, v19
	v_cvt_pk_bf16_f32 v17, v17, v18
	ds_read2_b32 v[18:19], v15 offset0:20 offset1:85
	s_waitcnt lgkmcnt(0)
	v_mul_f32_e32 v18, v0, v18
	v_mul_f32_e32 v19, v1, v19
	v_cvt_pk_bf16_f32 v18, v18, v19
	ds_read2_b32 v[20:21], v15 offset0:150 offset1:215
	s_waitcnt lgkmcnt(0)
	v_mul_f32_e32 v19, v2, v20
	v_mul_f32_e32 v20, v3, v21
	v_cvt_pk_bf16_f32 v19, v19, v20
	v_add_u32_e32 v20, 16, v24
	v_ashrrev_i32_e32 v21, 31, v20
	v_mul_lo_u32 v22, s56, v21
	v_mul_lo_u32 v23, s57, v20
	v_mad_u64_u32 v[20:21], s[6:7], s56, v20, 0
	v_add3_u32 v21, v21, v22, v23
	ds_read2_b32 v[22:23], v14 offset0:24 offset1:89
	v_lshl_add_u64 v[20:21], v[20:21], 1, s[60:61]
	v_lshl_add_u64 v[20:21], v[20:21], 0, s[4:5]
	v_lshl_add_u64 v[20:21], v[20:21], 0, v[8:9]
	global_store_dwordx4 v[20:21], v[16:19], off
	s_waitcnt lgkmcnt(0)
	s_nop 0
	v_mul_f32_e32 v16, v4, v22
	v_mul_f32_e32 v17, v5, v23
	v_cvt_pk_bf16_f32 v16, v16, v17
	ds_read2_b32 v[18:19], v14 offset0:154 offset1:219
	s_waitcnt lgkmcnt(0)
	v_mul_f32_e32 v17, v6, v18
	v_mul_f32_e32 v18, v7, v19
	v_cvt_pk_bf16_f32 v17, v17, v18
	ds_read2_b32 v[18:19], v15 offset0:28 offset1:93
	s_waitcnt lgkmcnt(0)
	v_mul_f32_e32 v18, v0, v18
	v_mul_f32_e32 v19, v1, v19
	v_cvt_pk_bf16_f32 v18, v18, v19
	ds_read2_b32 v[20:21], v15 offset0:158 offset1:223
	s_waitcnt lgkmcnt(0)
; __device__ __forceinline__ unsigned cvt_pk_bf16(float lo, float hi) { unsigned r; asm volatile("v_cvt_pk_bf16_f32 %0, %1, %2" : "=v"(r) : "v"(lo), "v"(hi)); return r; }
; #define LAS __attribute__((address_space(3)))
; #define LDS_WAIT() asm volatile("s_waitcnt lgkmcnt(0)" ::: "memory")
; __device__ __forceinline__ void conv_store(const ConvItem& ci, LAS float* scr, int lane, const float (&v)[64]) {
;     ...
; #pragma unroll
;     for (int j = 0; j < 8; ++j) { const int n = (lane >> 3) + 8 * j; const LAS float* s = scr + (8 * c) * 65 + n;
;         v4u o; o.x = cvt_pk_bf16(s[0 * 65] * s0[0], s[1 * 65] * s0[1]); o.y = cvt_pk_bf16(s[2 * 65] * s0[2], s[3 * 65] * s0[3]); o.z = cvt_pk_bf16(s[4 * 65] * s1[0], s[5 * 65] * s1[1]); o.w = cvt_pk_bf16(s[6 * 65] * s1[2], s[7 * 65] * s1[3]);
;         *(v4u*)(ci.dst + (size_t)(ci.drow0 + n) * ci.ldd + ci.k0 + 8 * c) = o; }
;     LDS_WAIT(); asm volatile("" ::: "memory");
; }
	v_mul_f32_e32 v19, v2, v20
	v_mul_f32_e32 v20, v3, v21
	v_cvt_pk_bf16_f32 v19, v19, v20
	v_add_u32_e32 v20, 24, v24
	v_ashrrev_i32_e32 v21, 31, v20
	v_mul_lo_u32 v22, s56, v21
	v_mul_lo_u32 v23, s57, v20
	v_mad_u64_u32 v[20:21], s[6:7], s56, v20, 0
	v_add3_u32 v21, v21, v22, v23
	ds_read2_b32 v[22:23], v14 offset0:32 offset1:97
	v_lshl_add_u64 v[20:21], v[20:21], 1, s[60:61]
	v_lshl_add_u64 v[20:21], v[20:21], 0, s[4:5]
	v_lshl_add_u64 v[20:21], v[20:21], 0, v[8:9]
	global_store_dwordx4 v[20:21], v[16:19], off
	s_waitcnt lgkmcnt(0)
	s_nop 0
	v_mul_f32_e32 v16, v4, v22
	v_mul_f32_e32 v17, v5, v23
	v_cvt_pk_bf16_f32 v16, v16, v17
	ds_read2_b32 v[18:19], v14 offset0:162 offset1:227
	s_waitcnt lgkmcnt(0)
	v_mul_f32_e32 v17, v6, v18
	v_mul_f32_e32 v18, v7, v19
	v_cvt_pk_bf16_f32 v17, v17, v18
	ds_read2_b32 v[18:19], v15 offset0:36 offset1:101
	s_waitcnt lgkmcnt(0)
	v_mul_f32_e32 v18, v0, v18
	v_mul_f32_e32 v19, v1, v19
	v_cvt_pk_bf16_f32 v18, v18, v19
	ds_read2_b32 v[20:21], v15 offset0:166 offset1:231
	s_waitcnt lgkmcnt(0)
	v_mul_f32_e32 v19, v2, v20
	v_mul_f32_e32 v20, v3, v21
	v_cvt_pk_bf16_f32 v19, v19, v20
	v_add_u32_e32 v20, 32, v24
	v_ashrrev_i32_e32 v21, 31, v20
	v_mul_lo_u32 v22, s56, v21
	v_mul_lo_u32 v23, s57, v20
	v_mad_u64_u32 v[20:21], s[6:7], s56, v20, 0
	v_add3_u32 v21, v21, v22, v23
	ds_read2_b32 v[22:23], v14 offset0:40 offset1:105
	v_lshl_add_u64 v[20:21], v[20:21], 1, s[60:61]
	v_lshl_add_u64 v[20:21], v[20:21], 0, s[4:5]
	v_lshl_add_u64 v[20:21], v[20:21], 0, v[8:9]
	global_store_dwordx4 v[20:21], v[16:19], off
	s_waitcnt lgkmcnt(0)
	s_nop 0
	v_mul_f32_e32 v16, v4, v22
	v_mul_f32_e32 v17, v5, v23
	v_cvt_pk_bf16_f32 v16, v16, v17
	ds_read2_b32 v[18:19], v14 offset0:170 offset1:235
	s_waitcnt lgkmcnt(0)
	v_mul_f32_e32 v17, v6, v18
	v_mul_f32_e32 v18, v7, v19
	v_cvt_pk_bf16_f32 v17, v17, v18
	ds_read2_b32 v[18:19], v15 offset0:44 offset1:109
	s_waitcnt lgkmcnt(0)
	v_mul_f32_e32 v18, v0, v18
	v_mul_f32_e32 v19, v1, v19
	v_cvt_pk_bf16_f32 v18, v18, v19
	ds_read2_b32 v[20:21], v15 offset0:174 offset1:239
	s_waitcnt lgkmcnt(0)
	v_mul_f32_e32 v19, v2, v20
	v_mul_f32_e32 v20, v3, v21
	v_cvt_pk_bf16_f32 v19, v19, v20
	v_add_u32_e32 v20, 40, v24
	v_ashrrev_i32_e32 v21, 31, v20
	v_mul_lo_u32 v22, s56, v21
	v_mul_lo_u32 v23, s57, v20
	v_mad_u64_u32 v[20:21], s[6:7], s56, v20, 0
	v_add3_u32 v21, v21, v22, v23
	ds_read2_b32 v[22:23], v14 offset0:48 offset1:113
	v_lshl_add_u64 v[20:21], v[20:21], 1, s[60:61]
	v_lshl_add_u64 v[20:21], v[20:21], 0, s[4:5]
	v_lshl_add_u64 v[20:21], v[20:21], 0, v[8:9]
	global_store_dwordx4 v[20:21], v[16:19], off
	s_waitcnt lgkmcnt(0)
	s_nop 0
	v_mul_f32_e32 v16, v4, v22
	v_mul_f32_e32 v17, v5, v23
	v_cvt_pk_bf16_f32 v16, v16, v17
	ds_read2_b32 v[18:19], v14 offset0:178 offset1:243
	s_waitcnt lgkmcnt(0)
	v_mul_f32_e32 v17, v6, v18
	v_mul_f32_e32 v18, v7, v19
	v_cvt_pk_bf16_f32 v17, v17, v18
	ds_read2_b32 v[18:19], v15 offset0:52 offset1:117
	s_waitcnt lgkmcnt(0)
	v_mul_f32_e32 v18, v0, v18
	v_mul_f32_e32 v19, v1, v19
	v_cvt_pk_bf16_f32 v18, v18, v19
	ds_read2_b32 v[20:21], v15 offset0:182 offset1:247
	s_waitcnt lgkmcnt(0)
	v_mul_f32_e32 v19, v2, v20
	v_mul_f32_e32 v20, v3, v21
	v_cvt_pk_bf16_f32 v19, v19, v20
	v_add_u32_e32 v20, 48, v24
	v_ashrrev_i32_e32 v21, 31, v20
	v_mul_lo_u32 v22, s56, v21
	v_mul_lo_u32 v23, s57, v20
	v_mad_u64_u32 v[20:21], s[6:7], s56, v20, 0
	v_add3_u32 v21, v21, v22, v23
	ds_read2_b32 v[22:23], v14 offset0:56 offset1:121
	v_lshl_add_u64 v[20:21], v[20:21], 1, s[60:61]
	v_lshl_add_u64 v[20:21], v[20:21], 0, s[4:5]
	v_lshl_add_u64 v[20:21], v[20:21], 0, v[8:9]
	global_store_dwordx4 v[20:21], v[16:19], off
	s_waitcnt lgkmcnt(0)
	v_mul_f32_e32 v4, v4, v22
	v_mul_f32_e32 v5, v5, v23
	v_cvt_pk_bf16_f32 v4, v4, v5
	ds_read2_b32 v[16:17], v14 offset0:186 offset1:251
	s_waitcnt lgkmcnt(0)
	v_mul_f32_e32 v5, v6, v16
	v_mul_f32_e32 v6, v7, v17
	v_cvt_pk_bf16_f32 v5, v5, v6
	ds_read2_b32 v[6:7], v15 offset0:60 offset1:125
	s_waitcnt lgkmcnt(0)
	v_mul_f32_e32 v0, v0, v6
	v_mul_f32_e32 v1, v1, v7
	v_cvt_pk_bf16_f32 v6, v0, v1
	ds_read2_b32 v[0:1], v15 offset0:190 offset1:255
	s_waitcnt lgkmcnt(0)
	v_mul_f32_e32 v0, v2, v0
	v_mul_f32_e32 v1, v3, v1
	v_cvt_pk_bf16_f32 v7, v0, v1
	v_add_u32_e32 v0, 56, v24
	v_ashrrev_i32_e32 v1, 31, v0
	v_mul_lo_u32 v2, s56, v1
	v_mul_lo_u32 v3, s57, v0
	v_mad_u64_u32 v[0:1], s[6:7], s56, v0, 0
	v_add3_u32 v1, v1, v2, v3
	v_lshl_add_u64 v[0:1], v[0:1], 1, s[60:61]
	v_lshl_add_u64 v[0:1], v[0:1], 0, s[4:5]
	v_lshl_add_u64 v[0:1], v[0:1], 0, v[8:9]
	global_store_dwordx4 v[0:1], v[4:7], off
	s_waitcnt lgkmcnt(0)
	s_cbranch_scc0 .Lcvp10_ret

; __global__ void __launch_bounds__(NWAVES * 64, 2) mk_fwd(Args args) {
;     ...
;             for (int it = gw; it < NITEMS; it += NGW) {
;                 ConvItem ca; CONV_DESC(ca, it);
;                 float va[64];
;                 conv_load(ca, lane, va);
;                 conv_store(ca, scr, lane, va);
;             }
.Lcvp10_ret:
	v_mov_b32_e32 v254, v250
	v_mov_b32_e32 v255, v251
	s_nop 1
	v_readlane_b32 s0, v252, 0
	v_readlane_b32 s1, v252, 1
	v_readlane_b32 s2, v252, 2
	v_readlane_b32 s3, v252, 3
	v_readlane_b32 s4, v252, 4
	v_readlane_b32 s5, v252, 5
	v_readlane_b32 s6, v252, 6
	v_readlane_b32 s7, v252, 7
	v_readlane_b32 s8, v252, 8
	v_readlane_b32 s9, v252, 9
	v_readlane_b32 s10, v252, 10
	v_readlane_b32 s11, v252, 11
	v_readlane_b32 s12, v252, 12
	v_readlane_b32 s13, v252, 13
	v_readlane_b32 s14, v252, 14
	v_readlane_b32 s15, v252, 15
	v_readlane_b32 s16, v252, 16
	v_readlane_b32 s17, v252, 17
	v_readlane_b32 s18, v252, 18
	v_readlane_b32 s19, v252, 19
	v_readlane_b32 s20, v252, 20
	v_readlane_b32 s21, v252, 21
	v_readlane_b32 s22, v252, 22
	v_readlane_b32 s23, v252, 23
	v_readlane_b32 s24, v252, 24
	v_readlane_b32 s25, v252, 25
	v_readlane_b32 s26, v252, 26
	v_readlane_b32 s27, v252, 27
	v_readlane_b32 s28, v252, 28
	v_readlane_b32 s29, v252, 29
	v_readlane_b32 s30, v252, 30
	v_readlane_b32 s31, v252, 31
	v_readlane_b32 s32, v252, 32
	v_readlane_b32 s33, v252, 33
	v_readlane_b32 s34, v252, 34
	v_readlane_b32 s35, v252, 35
	v_readlane_b32 s36, v252, 36
	v_readlane_b32 s37, v252, 37
	v_readlane_b32 s38, v252, 38
	v_readlane_b32 s39, v252, 39
	v_readlane_b32 s40, v252, 40
	v_readlane_b32 s41, v252, 41
	v_readlane_b32 s42, v252, 42
	v_readlane_b32 s43, v252, 43
	v_readlane_b32 s44, v252, 44
	v_readlane_b32 s45, v252, 45
	v_readlane_b32 s46, v252, 46
	v_readlane_b32 s47, v252, 47
	v_readlane_b32 s48, v252, 48
	v_readlane_b32 s49, v252, 49
	v_readlane_b32 s50, v252, 50
	v_readlane_b32 s51, v252, 51
	v_readlane_b32 s52, v252, 52
	v_readlane_b32 s53, v252, 53
	v_readlane_b32 s54, v252, 54
	v_readlane_b32 s55, v252, 55
	v_readlane_b32 s56, v252, 56
	v_readlane_b32 s57, v252, 57
	v_readlane_b32 s58, v252, 58
	v_readlane_b32 s59, v252, 59
	v_readlane_b32 s60, v252, 60
	v_readlane_b32 s61, v252, 61
	v_readlane_b32 s62, v252, 62
	v_readlane_b32 s63, v252, 63
	v_readlane_b32 s64, v253, 0
	v_readlane_b32 s65, v253, 1
	v_readlane_b32 s66, v253, 2
	v_readlane_b32 s67, v253, 3
	v_readlane_b32 s68, v253, 4
	v_readlane_b32 s69, v253, 5
	v_readlane_b32 s70, v253, 6
	v_readlane_b32 s71, v253, 7
	v_readlane_b32 s72, v253, 8
	v_readlane_b32 s73, v253, 9
	v_readlane_b32 s74, v253, 10
	v_readlane_b32 s75, v253, 11
	v_readlane_b32 s76, v253, 12
	v_readlane_b32 s77, v253, 13
	v_readlane_b32 s78, v253, 14
	v_readlane_b32 s79, v253, 15
	v_readlane_b32 s80, v253, 16
	v_readlane_b32 s81, v253, 17
	v_readlane_b32 s82, v253, 18
	v_readlane_b32 s83, v253, 19
	v_readlane_b32 s84, v253, 20
	v_readlane_b32 s85, v253, 21
	v_readlane_b32 s86, v253, 22
	v_readlane_b32 s87, v253, 23
	v_readlane_b32 s88, v253, 24
	v_readlane_b32 s89, v253, 25
	v_readlane_b32 s90, v253, 26
	v_readlane_b32 s91, v253, 27
	v_readlane_b32 s92, v253, 28
	v_readlane_b32 s93, v253, 29
	v_readlane_b32 s94, v253, 30
	v_readlane_b32 s95, v253, 31
	v_readlane_b32 s96, v253, 32
	v_readlane_b32 s97, v253, 33
	v_readlane_b32 vcc_lo, v253, 34
	v_readlane_b32 vcc_hi, v253, 35
	s_nop 4

; #define LAS __attribute__((address_space(3)))
; __global__ void __launch_bounds__(NWAVES * 64, 2) mk_fwd(Args args) {
;     ...
;             PH_LOCALS
;             LAS float* scr = (LAS float*)(lds + RING_OFF + wave * 16640);   static_assert(8 * 16640 <= LDSCTL_OFF, "converter scratch below the LDS control words");
;             constexpr int I_UP = (D / 64) * (NUP / 64), I_DN = (DFF / 64) * (D / 64), I_IN = (D / 64) * (DINP / 64), I_GLU = 16 * 16, I_L = 4 * 16, I_V1 = 16 * 4, I_V2 = 4 * 16,
;                           I_BS5 = 16 * 32, I_BAT = 8 * 32, I_BRW = 16 * 32, I_OUT = 32 * 32;
;             constexpr int NITEMS = 2 * I_UP + 2 * I_DN + I_IN + I_GLU + 3 * I_L + I_V1 + I_V2 + I_BS5 + I_BAT + I_BRW + I_OUT;
;             const int lv = l > 0 ? l - 1 : 0;
;     ...
;             for (int it = gw; it < NITEMS; it += NGW) {
;                 ConvItem ca; CONV_DESC(ca, it);
.LBB0_346:
	v_readlane_b32 s99, v254, 35
	v_readlane_b32 s98, v254, 38
	s_nop 3
	s_cmp_lt_u32 s99, 128
	s_cbranch_scc1 .Lcvskip_p3
	s_cmp_gt_u32 s98, 2
	s_cbranch_scc1 .Lcvskip_p3
	v_mov_b32_e32 v250, v254
	v_mov_b32_e32 v251, v255
	v_writelane_b32 v252, s0, 0
	s_nop 0
	v_writelane_b32 v252, s1, 1
	s_nop 0
	v_writelane_b32 v252, s2, 2
	s_nop 0
	v_writelane_b32 v252, s3, 3
	s_nop 0
	v_writelane_b32 v252, s4, 4
	s_nop 0
	v_writelane_b32 v252, s5, 5
	s_nop 0
	v_writelane_b32 v252, s6, 6
	s_nop 0
	v_writelane_b32 v252, s7, 7
	s_nop 0
	v_writelane_b32 v252, s8, 8
	s_nop 0
	v_writelane_b32 v252, s9, 9
	s_nop 0
	v_writelane_b32 v252, s10, 10
	s_nop 0
	v_writelane_b32 v252, s11, 11
	s_nop 0
	v_writelane_b32 v252, s12, 12
	s_nop 0
	v_writelane_b32 v252, s13, 13
	s_nop 0
	v_writelane_b32 v252, s14, 14
	s_nop 0
	v_writelane_b32 v252, s15, 15
	s_nop 0
	v_writelane_b32 v252, s16, 16
	s_nop 0
	v_writelane_b32 v252, s17, 17
	s_nop 0
	v_writelane_b32 v252, s18, 18
	s_nop 0
	v_writelane_b32 v252, s19, 19
	s_nop 0
	v_writelane_b32 v252, s20, 20
	s_nop 0
	v_writelane_b32 v252, s21, 21
	s_nop 0
	v_writelane_b32 v252, s22, 22
	s_nop 0
	v_writelane_b32 v252, s23, 23
	s_nop 0
	v_writelane_b32 v252, s24, 24
	s_nop 0
	v_writelane_b32 v252, s25, 25
	s_nop 0
	v_writelane_b32 v252, s26, 26
	s_nop 0
	v_writelane_b32 v252, s27, 27
	s_nop 0
	v_writelane_b32 v252, s28, 28
	s_nop 0
	v_writelane_b32 v252, s29, 29
	s_nop 0
	v_writelane_b32 v252, s30, 30
	s_nop 0
	v_writelane_b32 v252, s31, 31
	s_nop 0
	v_writelane_b32 v252, s32, 32
	s_nop 0
	v_writelane_b32 v252, s33, 33
	s_nop 0
	v_writelane_b32 v252, s34, 34
	s_nop 0
	v_writelane_b32 v252, s35, 35
	s_nop 0
	v_writelane_b32 v252, s36, 36
	s_nop 0
	v_writelane_b32 v252, s37, 37
	s_nop 0
	v_writelane_b32 v252, s38, 38
	s_nop 0
	v_writelane_b32 v252, s39, 39
	s_nop 0
	v_writelane_b32 v252, s40, 40
	s_nop 0
	v_writelane_b32 v252, s41, 41
	s_nop 0
	v_writelane_b32 v252, s42, 42
	s_nop 0
	v_writelane_b32 v252, s43, 43
	s_nop 0
	v_writelane_b32 v252, s44, 44
	s_nop 0
	v_writelane_b32 v252, s45, 45
	s_nop 0
	v_writelane_b32 v252, s46, 46
	s_nop 0
	v_writelane_b32 v252, s47, 47
	s_nop 0
	v_writelane_b32 v252, s48, 48
	s_nop 0
	v_writelane_b32 v252, s49, 49
	s_nop 0
	v_writelane_b32 v252, s50, 50
	s_nop 0
	v_writelane_b32 v252, s51, 51
	s_nop 0
	v_writelane_b32 v252, s52, 52
	s_nop 0
	v_writelane_b32 v252, s53, 53
	s_nop 0
	v_writelane_b32 v252, s54, 54
	s_nop 0
	v_writelane_b32 v252, s55, 55
	s_nop 0
	v_writelane_b32 v252, s56, 56
	s_nop 0
	v_writelane_b32 v252, s57, 57
	s_nop 0
	v_writelane_b32 v252, s58, 58
	s_nop 0
	v_writelane_b32 v252, s59, 59
	s_nop 0
	v_writelane_b32 v252, s60, 60
	s_nop 0
	v_writelane_b32 v252, s61, 61
	s_nop 0
	v_writelane_b32 v252, s62, 62
	s_nop 0
	v_writelane_b32 v252, s63, 63
	s_nop 0
	v_writelane_b32 v253, s64, 0
	s_nop 0
	v_writelane_b32 v253, s65, 1
	s_nop 0
	v_writelane_b32 v253, s66, 2
	s_nop 0
	v_writelane_b32 v253, s67, 3
	s_nop 0
	v_writelane_b32 v253, s68, 4
	s_nop 0
	v_writelane_b32 v253, s69, 5
	s_nop 0
	v_writelane_b32 v253, s70, 6
	s_nop 0
	v_writelane_b32 v253, s71, 7
	s_nop 0
	v_writelane_b32 v253, s72, 8
	s_nop 0
	v_writelane_b32 v253, s73, 9
	s_nop 0
	v_writelane_b32 v253, s74, 10
	s_nop 0
	v_writelane_b32 v253, s75, 11
	s_nop 0
	v_writelane_b32 v253, s76, 12
	s_nop 0
	v_writelane_b32 v253, s77, 13
	s_nop 0
	v_writelane_b32 v253, s78, 14
	s_nop 0
	v_writelane_b32 v253, s79, 15
	s_nop 0
	v_writelane_b32 v253, s80, 16
	s_nop 0
	v_writelane_b32 v253, s81, 17
	s_nop 0
	v_writelane_b32 v253, s82, 18
	s_nop 0
	v_writelane_b32 v253, s83, 19
	s_nop 0
	v_writelane_b32 v253, s84, 20
	s_nop 0
	v_writelane_b32 v253, s85, 21
	s_nop 0
	v_writelane_b32 v253, s86, 22
	s_nop 0
	v_writelane_b32 v253, s87, 23
	s_nop 0
	v_writelane_b32 v253, s88, 24
	s_nop 0
	v_writelane_b32 v253, s89, 25
	s_nop 0
	v_writelane_b32 v253, s90, 26
	s_nop 0
	v_writelane_b32 v253, s91, 27
	s_nop 0
	v_writelane_b32 v253, s92, 28
	s_nop 0
	v_writelane_b32 v253, s93, 29
	s_nop 0
	v_writelane_b32 v253, s94, 30
	s_nop 0
	v_writelane_b32 v253, s95, 31
	s_nop 0
	v_writelane_b32 v253, s96, 32
	s_nop 0
	v_writelane_b32 v253, s97, 33
	s_nop 0
	v_writelane_b32 v253, vcc_lo, 34
	s_nop 0
	v_writelane_b32 v253, vcc_hi, 35
	s_nop 1
	v_readlane_b32 s84, v254, 35
	s_nop 3
	v_readlane_b32 s0, v254, 8
	v_readlane_b32 s4, v254, 10
	v_readlane_b32 s1, v254, 9
	v_mbcnt_lo_u32_b32 v11, -1, 0
	v_mbcnt_hi_u32_b32 v11, -1, v11
	s_load_dword s6, s[0:1], 0x0
	s_mov_b32 s3, s84
	s_waitcnt lgkmcnt(0)
	s_movk_i32 s6, 128
	s_lshl_b32 s3, s3, 3
	v_readlane_b32 s0, v254, 0
	s_add_i32 s3, s3, s4
	s_add_i32 s3, s3, 0xfffffc00
	v_readlane_b32 s1, v254, 1
	s_cmpk_gt_i32 s3, 5503
	s_cbranch_scc1 .Lcvp30_ret
	s_load_dwordx2 s[8:9], s[0:1], 0x138
	v_readlane_b32 s14, v254, 38
	s_nop 0
	s_add_i32 s14, s14, 1
	s_mulk_i32 s4, 0x4100
	s_add_i32 s7, s4, 0
	v_sub_u32_e64 v0, s14, 1 clamp
	s_lshl_b32 s33, s6, 3
	v_readfirstlane_b32 s4, v0
	s_lshl_b32 s96, s4, 16
	s_waitcnt lgkmcnt(0)
	s_add_u32 s4, s8, 0x22800000
	s_addc_u32 s5, s9, 0
	v_writelane_b32 v254, s4, 39
	s_mov_b32 s15, s97
	v_and_b32_e32 v0, 7, v11
	v_writelane_b32 v254, s5, 40
	s_add_u32 s4, s8, 0x22780000
	s_addc_u32 s5, s9, 0
	v_writelane_b32 v254, s4, 41
	v_ashrrev_i32_e32 v13, 3, v11
	v_lshlrev_b32_e32 v10, 3, v0
	v_writelane_b32 v254, s5, 42
	s_lshl_b32 s4, s14, 18
	s_add_u32 s10, s8, 0x22700000
	s_addc_u32 s11, s9, 0
	v_writelane_b32 v254, s10, 43
	s_mov_b32 s5, s97
	v_mul_u32_u24_e32 v0, 0x820, v0
	v_writelane_b32 v254, s11, 44
	s_mul_i32 s10, s14, 0x18000
	s_mov_b32 s11, s97
	v_writelane_b32 v254, s10, 45
	v_lshlrev_b32_e32 v1, 2, v13
	v_lshl_add_u32 v12, v11, 2, s7
	v_writelane_b32 v254, s11, 46
	s_add_u32 s10, s8, 0x22680000
	s_addc_u32 s11, s9, 0
	v_writelane_b32 v254, s10, 47
	v_add3_u32 v14, s7, v0, v1
	s_mov_b32 s41, s97
	v_writelane_b32 v254, s11, 48
	s_add_u32 s10, s8, 0x22600000
	s_addc_u32 s11, s9, 0
	v_writelane_b32 v254, s10, 49
	s_nop 1
	v_writelane_b32 v254, s11, 50
	s_lshl_b32 s10, s14, 20
	s_mov_b32 s11, s97
	v_writelane_b32 v254, s10, 51
	s_nop 1
	v_writelane_b32 v254, s11, 52
	s_add_u32 s10, s8, 0x22400000
	s_addc_u32 s11, s9, 0
	v_writelane_b32 v254, s10, 53
	s_nop 1
	v_writelane_b32 v254, s11, 54
	s_lshl_b32 s10, s14, 21
	s_mov_b32 s11, s97
	v_writelane_b32 v254, s10, 55
	s_nop 1
	v_writelane_b32 v254, s11, 56
	s_add_u32 s10, s8, 0x22e80000
	s_addc_u32 s11, s9, 0
	v_writelane_b32 v254, s10, 57
	s_nop 1
	v_writelane_b32 v254, s11, 58
	s_add_u32 s10, s8, 0x27b80000
	s_addc_u32 s11, s9, 0
	v_writelane_b32 v254, s10, 59
	s_nop 1
	v_writelane_b32 v254, s11, 60
	s_add_u32 s10, s8, 0x22880000
	s_addc_u32 s11, s9, 0
	v_writelane_b32 v254, s10, 61
	s_nop 1
	v_writelane_b32 v254, s11, 62
	s_lshl_b32 s10, s14, 22
	s_add_u32 s12, s8, 0x23280000
	s_addc_u32 s13, s9, 0
	v_writelane_b32 v254, s12, 63
	s_mov_b32 s11, s97
	s_nop 0
	v_writelane_b32 v255, s13, 0
	s_mul_i32 s12, s14, 0xac0000
	s_mov_b32 s13, s97
	v_writelane_b32 v255, s12, 1
	s_nop 1
	v_writelane_b32 v255, s13, 2
	s_add_u32 s12, s8, 0x26580000
	s_addc_u32 s13, s9, 0
	v_writelane_b32 v255, s12, 3
	s_nop 1
	v_writelane_b32 v255, s13, 4
	s_add_u32 s12, s8, 0x1d200000
	s_addc_u32 s13, s9, 0
	s_lshl_b32 s40, s14, 11
	v_writelane_b32 v255, s12, 5
	s_add_u32 s16, s8, 0x1e800000
	s_addc_u32 s17, s9, 0
	v_writelane_b32 v255, s13, 6
	v_writelane_b32 v255, s16, 7
	s_mul_i32 s12, s14, 0x1de0000
	s_mul_i32 s14, s14, 0x1580000
	v_writelane_b32 v255, s17, 8
	v_writelane_b32 v255, s14, 9
	s_mov_b32 s13, s97
	s_nop 0
	v_writelane_b32 v255, s15, 10
	s_add_u32 s14, s8, 0x23a80000
	s_addc_u32 s15, s9, 0
	v_writelane_b32 v255, s14, 11
	s_add_u32 s8, s8, 0x1a700000
	s_addc_u32 s9, s9, 0
	v_writelane_b32 v255, s15, 12
	v_writelane_b32 v255, s8, 13
	s_lshl_b64 s[4:5], s[4:5], 2
	s_lshl_b32 s7, s3, 4
	v_writelane_b32 v255, s9, 14
	v_writelane_b32 v255, s4, 15
	s_add_i32 s72, s7, 0xc00
	s_lshl_b32 s7, s3, 1
	v_writelane_b32 v255, s5, 16
	s_lshl_b64 s[4:5], s[10:11], 2
	v_writelane_b32 v255, s4, 17
	s_lshl_b32 s66, s3, 6
	s_lshl_b32 s67, s6, 9
	v_writelane_b32 v255, s5, 18
	s_lshl_b64 s[4:5], s[12:13], 2
	v_writelane_b32 v255, s4, 19
	s_lshl_b32 s68, s3, 5
	s_lshl_b32 s69, s6, 8
	v_writelane_b32 v255, s5, 20
	v_writelane_b32 v255, s80, 21
	s_lshl_b32 s70, s3, 2
	s_lshl_b32 s71, s6, 5
	v_writelane_b32 v255, s81, 22
	v_writelane_b32 v255, s82, 23
	s_lshl_b32 s73, s6, 7
	s_add_i32 s74, s7, 0x13500
	s_lshl_b32 s75, s6, 4
	v_writelane_b32 v255, s83, 24
	s_branch .Lcvp30_31

; #define LAS __attribute__((address_space(3)))
; __device__ __forceinline__ void conv_load(const ConvItem& ci, int lane, float (&v)[64]) {
;     const bool okc = ci.srcc >= 0 && (ci.srcc + lane) < ci.ncols;
;     const float* base = ci.W + (okc ? ci.srcc + lane : 0);
;     const int kmax = ci.Ksrc - 1;
; #pragma unroll
;     for (int i = 0; i < 64; ++i) { const int k = ci.k0 + i, kk = k < kmax ? k : kmax; v[i] = __builtin_nontemporal_load(base + (size_t)kk * ci.ldw); }
; #pragma unroll
;     for (int i = 0; i < 64; ++i) v[i] = (okc && (ci.k0 + i) < ci.Ksrc) ? v[i] : 0.f;
; }
; __device__ __forceinline__ void conv_store(const ConvItem& ci, LAS float* scr, int lane, const float (&v)[64]) {
;     const int c = lane & 7;
;     f32x4 s0 = {1.f, 1.f, 1.f, 1.f}, s1 = s0;
;     if (ci.ks) { const int kb = ci.k0 + 8 * c < ci.Ksrc - 8 ? ci.k0 + 8 * c : ci.Ksrc - 8; s0 = *(const f32x4*)(ci.ks + kb); s1 = *(const f32x4*)(ci.ks + kb + 4); }
; #pragma unroll
;     for (int i = 0; i < 64; ++i) scr[i * 65 + lane] = v[i];
.Lcvp30_30:
	s_cmp_lt_i32 s58, s76
	s_cselect_b64 s[4:5], -1, 0
	s_and_b64 s[4:5], vcc, s[4:5]
	s_cmp_lt_i32 s64, s76
	s_waitcnt vmcnt(62)
	v_cndmask_b32_e64 v21, 0, v21, s[4:5]
	s_cselect_b64 s[4:5], -1, 0
	s_and_b64 s[4:5], vcc, s[4:5]
	s_cmp_lt_i32 s65, s76
	v_cndmask_b32_e64 v20, 0, v20, s[4:5]
	s_cselect_b64 s[4:5], -1, 0
	s_and_b64 s[4:5], vcc, s[4:5]
	s_cmp_lt_i32 s78, s76
	s_waitcnt vmcnt(61)
	v_cndmask_b32_e64 v19, 0, v19, s[4:5]
	s_cselect_b64 s[4:5], -1, 0
	s_and_b64 s[4:5], vcc, s[4:5]
	s_cmp_lt_i32 s79, s76
	s_waitcnt vmcnt(60)
	v_cndmask_b32_e64 v18, 0, v18, s[4:5]
	s_cselect_b64 s[4:5], -1, 0
	s_and_b64 s[4:5], vcc, s[4:5]
	s_cmp_lt_i32 s80, s76
	s_waitcnt vmcnt(59)
	v_cndmask_b32_e64 v17, 0, v17, s[4:5]
	s_cselect_b64 s[4:5], -1, 0
	s_and_b64 s[4:5], vcc, s[4:5]
	s_cmp_lt_i32 s81, s76
	s_waitcnt vmcnt(58)
	v_cndmask_b32_e64 v16, 0, v16, s[4:5]
	s_cselect_b64 s[4:5], -1, 0
	s_and_b64 s[4:5], vcc, s[4:5]
	s_cmp_lt_i32 s82, s76
	s_waitcnt vmcnt(57)
	v_cndmask_b32_e64 v15, 0, v15, s[4:5]
	s_cselect_b64 s[4:5], -1, 0
	s_and_b64 s[4:5], vcc, s[4:5]
	s_cmp_lt_i32 s83, s76
	s_waitcnt vmcnt(56)
	v_cndmask_b32_e64 v8, 0, v8, s[4:5]
	s_cselect_b64 s[4:5], -1, 0
	s_and_b64 s[4:5], vcc, s[4:5]
	s_cmp_lt_i32 s85, s76
	s_waitcnt vmcnt(55)
	v_cndmask_b32_e64 v29, 0, v29, s[4:5]
	s_cselect_b64 s[4:5], -1, 0
	s_and_b64 s[4:5], vcc, s[4:5]
	s_cmp_lt_i32 s86, s76
	s_waitcnt vmcnt(54)
	v_cndmask_b32_e64 v28, 0, v28, s[4:5]
	s_cselect_b64 s[4:5], -1, 0
	s_and_b64 s[4:5], vcc, s[4:5]
	s_cmp_lt_i32 s87, s76
	s_waitcnt vmcnt(53)
	v_cndmask_b32_e64 v27, 0, v27, s[4:5]
	s_cselect_b64 s[4:5], -1, 0
	s_and_b64 s[4:5], vcc, s[4:5]
	s_cmp_lt_i32 s88, s76
	s_waitcnt vmcnt(52)
	v_cndmask_b32_e64 v26, 0, v26, s[4:5]
	s_cselect_b64 s[4:5], -1, 0
	s_and_b64 s[4:5], vcc, s[4:5]
	s_cmp_lt_i32 s89, s76
	s_waitcnt vmcnt(51)
	v_cndmask_b32_e64 v25, 0, v25, s[4:5]
	s_cselect_b64 s[4:5], -1, 0
	s_and_b64 s[4:5], vcc, s[4:5]
	s_cmp_lt_i32 s90, s76
	s_waitcnt vmcnt(50)
	v_cndmask_b32_e64 v24, 0, v24, s[4:5]
	s_cselect_b64 s[4:5], -1, 0
	s_and_b64 s[4:5], vcc, s[4:5]
	s_cmp_lt_i32 s92, s76
	s_waitcnt vmcnt(49)
	v_cndmask_b32_e64 v23, 0, v23, s[4:5]
	s_cselect_b64 s[4:5], -1, 0
	s_and_b64 s[4:5], vcc, s[4:5]
	s_cmp_lt_i32 s93, s76
	s_waitcnt vmcnt(48)
	v_cndmask_b32_e64 v22, 0, v22, s[4:5]
	s_cselect_b64 s[4:5], -1, 0
	s_and_b64 s[4:5], vcc, s[4:5]
	s_cmp_lt_i32 s94, s76
	s_waitcnt vmcnt(47)
	v_cndmask_b32_e64 v37, 0, v37, s[4:5]
	s_cselect_b64 s[4:5], -1, 0
	s_and_b64 s[4:5], vcc, s[4:5]
	s_cmp_lt_i32 s95, s76
	s_waitcnt vmcnt(46)
	v_cndmask_b32_e64 v36, 0, v36, s[4:5]
	s_cselect_b64 s[4:5], -1, 0
	s_and_b64 s[4:5], vcc, s[4:5]
	s_cmp_lt_i32 s50, s76
	s_waitcnt vmcnt(45)
	v_cndmask_b32_e64 v35, 0, v35, s[4:5]
	s_cselect_b64 s[4:5], -1, 0
	s_and_b64 s[4:5], vcc, s[4:5]
	s_cmp_lt_i32 s51, s76
	s_waitcnt vmcnt(44)
	v_cndmask_b32_e64 v34, 0, v34, s[4:5]
	s_cselect_b64 s[4:5], -1, 0
	s_and_b64 s[4:5], vcc, s[4:5]
	s_cmp_lt_i32 s52, s76
	s_waitcnt vmcnt(43)
	v_cndmask_b32_e64 v33, 0, v33, s[4:5]
	s_cselect_b64 s[4:5], -1, 0
	s_and_b64 s[4:5], vcc, s[4:5]
	s_cmp_lt_i32 s53, s76
	s_waitcnt vmcnt(42)
	v_cndmask_b32_e64 v32, 0, v32, s[4:5]
	s_cselect_b64 s[4:5], -1, 0
	s_and_b64 s[4:5], vcc, s[4:5]
	s_cmp_lt_i32 s6, s76
	s_waitcnt vmcnt(41)
	v_cndmask_b32_e64 v31, 0, v31, s[4:5]
	s_cselect_b64 s[4:5], -1, 0
	s_and_b64 s[4:5], vcc, s[4:5]
	s_cmp_lt_i32 s7, s76
	s_waitcnt vmcnt(40)
	v_cndmask_b32_e64 v30, 0, v30, s[4:5]
	s_cselect_b64 s[4:5], -1, 0
	s_and_b64 s[4:5], vcc, s[4:5]
	s_cmp_lt_i32 s8, s76
	s_waitcnt vmcnt(39)
	v_cndmask_b32_e64 v45, 0, v45, s[4:5]
	s_cselect_b64 s[4:5], -1, 0
	s_and_b64 s[4:5], vcc, s[4:5]
	s_cmp_lt_i32 s9, s76
	s_waitcnt vmcnt(38)
	v_cndmask_b32_e64 v44, 0, v44, s[4:5]
	s_cselect_b64 s[4:5], -1, 0
	s_and_b64 s[4:5], vcc, s[4:5]
	s_cmp_lt_i32 s10, s76
	s_waitcnt vmcnt(37)
	v_cndmask_b32_e64 v43, 0, v43, s[4:5]
	s_cselect_b64 s[4:5], -1, 0
	s_and_b64 s[4:5], vcc, s[4:5]
	s_cmp_lt_i32 s11, s76
	s_waitcnt vmcnt(36)
	v_cndmask_b32_e64 v42, 0, v42, s[4:5]
	s_cselect_b64 s[4:5], -1, 0
	s_and_b64 s[4:5], vcc, s[4:5]
	s_cmp_lt_i32 s14, s76
	s_waitcnt vmcnt(35)
	v_cndmask_b32_e64 v41, 0, v41, s[4:5]
	s_cselect_b64 s[4:5], -1, 0
	s_and_b64 s[4:5], vcc, s[4:5]
	s_cmp_lt_i32 s15, s76
	s_waitcnt vmcnt(34)
	v_cndmask_b32_e64 v40, 0, v40, s[4:5]
	s_cselect_b64 s[4:5], -1, 0
	s_and_b64 s[4:5], vcc, s[4:5]
	s_cmp_lt_i32 s16, s76
	s_waitcnt vmcnt(33)
	v_cndmask_b32_e64 v39, 0, v39, s[4:5]
	s_cselect_b64 s[4:5], -1, 0
	s_and_b64 s[4:5], vcc, s[4:5]
	s_cmp_lt_i32 s17, s76
	s_waitcnt vmcnt(32)
	v_cndmask_b32_e64 v38, 0, v38, s[4:5]
	s_cselect_b64 s[4:5], -1, 0
	s_and_b64 s[4:5], vcc, s[4:5]
	s_cmp_lt_i32 s12, s76
	s_waitcnt vmcnt(31)
	v_cndmask_b32_e64 v53, 0, v53, s[4:5]
	s_cselect_b64 s[4:5], -1, 0
	s_and_b64 s[4:5], vcc, s[4:5]
	s_cmp_lt_i32 s13, s76
	s_waitcnt vmcnt(30)
	v_cndmask_b32_e64 v52, 0, v52, s[4:5]
	s_cselect_b64 s[4:5], -1, 0
	s_and_b64 s[4:5], vcc, s[4:5]
	s_cmp_lt_i32 s20, s76
	s_waitcnt vmcnt(29)
	v_cndmask_b32_e64 v51, 0, v51, s[4:5]
	s_cselect_b64 s[4:5], -1, 0
	s_and_b64 s[4:5], vcc, s[4:5]
	s_cmp_lt_i32 s21, s76
	s_waitcnt vmcnt(28)
	v_cndmask_b32_e64 v50, 0, v50, s[4:5]
	s_cselect_b64 s[4:5], -1, 0
	s_and_b64 s[4:5], vcc, s[4:5]
	s_cmp_lt_i32 s24, s76
	s_waitcnt vmcnt(27)
	v_cndmask_b32_e64 v49, 0, v49, s[4:5]
	s_cselect_b64 s[4:5], -1, 0
	s_and_b64 s[4:5], vcc, s[4:5]
	s_cmp_lt_i32 s25, s76
	s_waitcnt vmcnt(26)
	v_cndmask_b32_e64 v48, 0, v48, s[4:5]
	s_cselect_b64 s[4:5], -1, 0
	s_and_b64 s[4:5], vcc, s[4:5]
	s_cmp_lt_i32 s26, s76
	s_waitcnt vmcnt(25)
	v_cndmask_b32_e64 v47, 0, v47, s[4:5]
	s_cselect_b64 s[4:5], -1, 0
	s_and_b64 s[4:5], vcc, s[4:5]
	s_cmp_lt_i32 s27, s76
	s_waitcnt vmcnt(24)
; __device__ __forceinline__ unsigned cvt_pk_bf16(float lo, float hi) { unsigned r; asm volatile("v_cvt_pk_bf16_f32 %0, %1, %2" : "=v"(r) : "v"(lo), "v"(hi)); return r; }
; #define LAS __attribute__((address_space(3)))
; #define LDS_WAIT() asm volatile("s_waitcnt lgkmcnt(0)" ::: "memory")
; __device__ __forceinline__ void conv_load(const ConvItem& ci, int lane, float (&v)[64]) {
;     ...
;     for (int i = 0; i < 64; ++i) v[i] = (okc && (ci.k0 + i) < ci.Ksrc) ? v[i] : 0.f;
; }
; __device__ __forceinline__ void conv_store(const ConvItem& ci, LAS float* scr, int lane, const float (&v)[64]) {
;     const int c = lane & 7;
;     f32x4 s0 = {1.f, 1.f, 1.f, 1.f}, s1 = s0;
;     if (ci.ks) { const int kb = ci.k0 + 8 * c < ci.Ksrc - 8 ? ci.k0 + 8 * c : ci.Ksrc - 8; s0 = *(const f32x4*)(ci.ks + kb); s1 = *(const f32x4*)(ci.ks + kb + 4); }
; #pragma unroll
;     for (int i = 0; i < 64; ++i) scr[i * 65 + lane] = v[i];
;     LDS_WAIT(); asm volatile("" ::: "memory");
; #pragma unroll
;     for (int j = 0; j < 8; ++j) { const int n = (lane >> 3) + 8 * j; const LAS float* s = scr + (8 * c) * 65 + n;
;         v4u o; o.x = cvt_pk_bf16(s[0 * 65] * s0[0], s[1 * 65] * s0[1]); o.y = cvt_pk_bf16(s[2 * 65] * s0[2], s[3 * 65] * s0[3]); o.z = cvt_pk_bf16(s[4 * 65] * s1[0], s[5 * 65] * s1[1]); o.w = cvt_pk_bf16(s[6 * 65] * s1[2], s[7 * 65] * s1[3]);
	v_cndmask_b32_e64 v46, 0, v46, s[4:5]
	s_cselect_b64 s[4:5], -1, 0
	s_and_b64 s[4:5], vcc, s[4:5]
	s_cmp_lt_i32 s18, s76
	s_waitcnt vmcnt(23)
	v_cndmask_b32_e64 v61, 0, v61, s[4:5]
	s_cselect_b64 s[4:5], -1, 0
	s_and_b64 s[4:5], vcc, s[4:5]
	s_cmp_lt_i32 s19, s76
	s_waitcnt vmcnt(22)
	v_cndmask_b32_e64 v60, 0, v60, s[4:5]
	s_cselect_b64 s[4:5], -1, 0
	s_and_b64 s[4:5], vcc, s[4:5]
	s_cmp_lt_i32 s28, s76
	s_waitcnt vmcnt(21)
	v_cndmask_b32_e64 v59, 0, v59, s[4:5]
	s_cselect_b64 s[4:5], -1, 0
	s_and_b64 s[4:5], vcc, s[4:5]
	s_cmp_lt_i32 s29, s76
	s_waitcnt vmcnt(20)
	v_cndmask_b32_e64 v58, 0, v58, s[4:5]
	s_cselect_b64 s[4:5], -1, 0
	s_and_b64 s[4:5], vcc, s[4:5]
	s_cmp_lt_i32 s22, s76
	s_waitcnt vmcnt(19)
	v_cndmask_b32_e64 v57, 0, v57, s[4:5]
	s_cselect_b64 s[4:5], -1, 0
	s_and_b64 s[4:5], vcc, s[4:5]
	s_cmp_lt_i32 s23, s76
	s_waitcnt vmcnt(18)
	v_cndmask_b32_e64 v56, 0, v56, s[4:5]
	s_cselect_b64 s[4:5], -1, 0
	s_and_b64 s[4:5], vcc, s[4:5]
	s_cmp_lt_i32 s30, s76
	s_waitcnt vmcnt(17)
	v_cndmask_b32_e64 v55, 0, v55, s[4:5]
	s_cselect_b64 s[4:5], -1, 0
	s_and_b64 s[4:5], vcc, s[4:5]
	s_cmp_lt_i32 s31, s76
	s_waitcnt vmcnt(16)
	v_cndmask_b32_e64 v54, 0, v54, s[4:5]
	s_cselect_b64 s[4:5], -1, 0
	s_and_b64 s[4:5], vcc, s[4:5]
	s_cmp_lt_i32 s36, s76
	s_waitcnt vmcnt(15)
	v_cndmask_b32_e64 v70, 0, v70, s[4:5]
	s_cselect_b64 s[4:5], -1, 0
	s_and_b64 s[4:5], vcc, s[4:5]
	s_cmp_lt_i32 s37, s76
	s_waitcnt vmcnt(14)
	v_cndmask_b32_e64 v69, 0, v69, s[4:5]
	s_cselect_b64 s[4:5], -1, 0
	s_and_b64 s[4:5], vcc, s[4:5]
	s_cmp_lt_i32 s38, s76
	s_waitcnt vmcnt(13)
	v_cndmask_b32_e64 v68, 0, v68, s[4:5]
	s_cselect_b64 s[4:5], -1, 0
	s_and_b64 s[4:5], vcc, s[4:5]
	s_cmp_lt_i32 s39, s76
	s_waitcnt vmcnt(12)
	v_cndmask_b32_e64 v67, 0, v67, s[4:5]
	s_cselect_b64 s[4:5], -1, 0
	s_and_b64 s[4:5], vcc, s[4:5]
	s_cmp_lt_i32 s34, s76
	s_waitcnt vmcnt(11)
	v_cndmask_b32_e64 v66, 0, v66, s[4:5]
	s_cselect_b64 s[4:5], -1, 0
	s_and_b64 s[4:5], vcc, s[4:5]
	s_cmp_lt_i32 s35, s76
	s_waitcnt vmcnt(10)
	v_cndmask_b32_e64 v64, 0, v64, s[4:5]
	s_cselect_b64 s[4:5], -1, 0
	s_and_b64 s[4:5], vcc, s[4:5]
	s_cmp_lt_i32 s42, s76
	s_waitcnt vmcnt(9)
	v_cndmask_b32_e64 v63, 0, v63, s[4:5]
	s_cselect_b64 s[4:5], -1, 0
	s_and_b64 s[4:5], vcc, s[4:5]
	s_cmp_lt_i32 s43, s76
	s_waitcnt vmcnt(8)
	v_cndmask_b32_e64 v62, 0, v62, s[4:5]
	s_cselect_b64 s[4:5], -1, 0
	s_and_b64 s[4:5], vcc, s[4:5]
	s_cmp_lt_i32 s54, s76
	s_waitcnt vmcnt(7)
	v_cndmask_b32_e64 v65, 0, v65, s[4:5]
	s_cselect_b64 s[4:5], -1, 0
	s_and_b64 s[4:5], vcc, s[4:5]
	s_cmp_lt_i32 s55, s76
	s_waitcnt vmcnt(6)
	v_cndmask_b32_e64 v74, 0, v74, s[4:5]
	s_cselect_b64 s[4:5], -1, 0
	s_and_b64 s[4:5], vcc, s[4:5]
	s_cmp_lt_i32 s46, s76
	ds_write2_b32 v12, v21, v20 offset1:65
	ds_write2_b32 v12, v19, v18 offset0:130 offset1:195
	v_add_u32_e32 v18, 0x400, v12
	s_waitcnt vmcnt(5)
	v_cndmask_b32_e64 v73, 0, v73, s[4:5]
	s_cselect_b64 s[4:5], -1, 0
	ds_write2_b32 v18, v17, v16 offset0:4 offset1:69
	ds_write2_b32 v18, v15, v8 offset0:134 offset1:199
	v_add_u32_e32 v8, 0x800, v12
	s_and_b64 s[4:5], vcc, s[4:5]
	ds_write2_b32 v8, v29, v28 offset0:8 offset1:73
	ds_write2_b32 v8, v27, v26 offset0:138 offset1:203
	v_add_u32_e32 v8, 0xc00, v12
	s_cmp_lt_i32 s47, s76
	ds_write2_b32 v8, v25, v24 offset0:12 offset1:77
	ds_write2_b32 v8, v23, v22 offset0:142 offset1:207
	v_add_u32_e32 v8, 0x1000, v12
	s_waitcnt vmcnt(4)
	v_cndmask_b32_e64 v72, 0, v72, s[4:5]
	s_cselect_b64 s[4:5], -1, 0
	ds_write2_b32 v8, v37, v36 offset0:16 offset1:81
	ds_write2_b32 v8, v35, v34 offset0:146 offset1:211
	v_add_u32_e32 v8, 0x1400, v12
	s_and_b64 s[4:5], vcc, s[4:5]
	ds_write2_b32 v8, v33, v32 offset0:20 offset1:85
	ds_write2_b32 v8, v31, v30 offset0:150 offset1:215
	v_add_u32_e32 v8, 0x1800, v12
	s_cmp_lt_i32 s48, s76
	ds_write2_b32 v8, v45, v44 offset0:24 offset1:89
	ds_write2_b32 v8, v43, v42 offset0:154 offset1:219
	v_add_u32_e32 v8, 0x1c00, v12
	s_waitcnt vmcnt(3)
	v_cndmask_b32_e64 v71, 0, v71, s[4:5]
	s_cselect_b64 s[4:5], -1, 0
	ds_write2_b32 v8, v41, v40 offset0:28 offset1:93
	ds_write2_b32 v8, v39, v38 offset0:158 offset1:223
	v_add_u32_e32 v8, 0x2000, v12
	s_and_b64 s[4:5], vcc, s[4:5]
	ds_write2_b32 v8, v53, v52 offset0:32 offset1:97
	ds_write2_b32 v8, v51, v50 offset0:162 offset1:227
	v_add_u32_e32 v8, 0x2400, v12
	s_cmp_lt_i32 s49, s76
	ds_write2_b32 v8, v49, v48 offset0:36 offset1:101
	ds_write2_b32 v8, v47, v46 offset0:166 offset1:231
	v_add_u32_e32 v8, 0x2800, v12
	s_waitcnt vmcnt(2)
	v_cndmask_b32_e64 v77, 0, v77, s[4:5]
	s_cselect_b64 s[4:5], -1, 0
	ds_write2_b32 v8, v61, v60 offset0:40 offset1:105
	ds_write2_b32 v8, v59, v58 offset0:170 offset1:235
	v_add_u32_e32 v8, 0x2c00, v12
	s_and_b64 s[4:5], vcc, s[4:5]
	ds_write2_b32 v8, v57, v56 offset0:44 offset1:109
	ds_write2_b32 v8, v55, v54 offset0:174 offset1:239
	v_add_u32_e32 v8, 0x3000, v12
	s_cmp_lt_i32 s44, s76
	ds_write2_b32 v8, v70, v69 offset0:48 offset1:113
	ds_write2_b32 v8, v68, v67 offset0:178 offset1:243
	v_add_u32_e32 v8, 0x3400, v12
	s_waitcnt vmcnt(1)
	v_cndmask_b32_e64 v76, 0, v76, s[4:5]
	s_cselect_b64 s[4:5], -1, 0
	ds_write2_b32 v8, v66, v64 offset0:52 offset1:117
	ds_write2_b32 v8, v63, v62 offset0:182 offset1:247
	v_add_u32_e32 v8, 0x3800, v12
	s_and_b64 vcc, vcc, s[4:5]
	ds_write2_b32 v8, v65, v74 offset0:56 offset1:121
	ds_write2_b32 v8, v73, v72 offset0:186 offset1:251
	v_add_u32_e32 v8, 0x3c00, v12
	s_waitcnt vmcnt(0)
	v_cndmask_b32_e32 v75, 0, v75, vcc
	ds_write2_b32 v8, v71, v77 offset0:60 offset1:125
	ds_write2_b32 v8, v76, v75 offset0:190 offset1:255
	s_waitcnt lgkmcnt(0)
	ds_read2_b32 v[16:17], v14 offset1:65
	v_add_u32_e32 v24, s59, v13
	v_mul_lo_u32 v22, s57, v24
	s_ashr_i32 s59, s58, 31
	v_readlane_b32 s76, v254, 31
	s_waitcnt lgkmcnt(0)
; __device__ __forceinline__ unsigned cvt_pk_bf16(float lo, float hi) { unsigned r; asm volatile("v_cvt_pk_bf16_f32 %0, %1, %2" : "=v"(r) : "v"(lo), "v"(hi)); return r; }
; #define LAS __attribute__((address_space(3)))
; __device__ __forceinline__ void conv_store(const ConvItem& ci, LAS float* scr, int lane, const float (&v)[64]) {
;     ...
; #pragma unroll
;     for (int j = 0; j < 8; ++j) { const int n = (lane >> 3) + 8 * j; const LAS float* s = scr + (8 * c) * 65 + n;
;         v4u o; o.x = cvt_pk_bf16(s[0 * 65] * s0[0], s[1 * 65] * s0[1]); o.y = cvt_pk_bf16(s[2 * 65] * s0[2], s[3 * 65] * s0[3]); o.z = cvt_pk_bf16(s[4 * 65] * s1[0], s[5 * 65] * s1[1]); o.w = cvt_pk_bf16(s[6 * 65] * s1[2], s[7 * 65] * s1[3]);
;         *(v4u*)(ci.dst + (size_t)(ci.drow0 + n) * ci.ldd + ci.k0 + 8 * c) = o; }
	v_mul_f32_e32 v8, v4, v16
	v_mul_f32_e32 v15, v5, v17
	v_cvt_pk_bf16_f32 v16, v8, v15
	ds_read2_b32 v[18:19], v14 offset0:130 offset1:195
	s_add_i32 s3, s3, s33
	s_add_i32 s66, s66, s67
	s_add_i32 s68, s68, s69
	s_add_i32 s70, s70, s71
	s_waitcnt lgkmcnt(0)
	v_mul_f32_e32 v15, v7, v19
	v_mul_f32_e32 v8, v6, v18
	v_cvt_pk_bf16_f32 v17, v8, v15
	v_add_u32_e32 v15, 0x400, v14
	ds_read2_b32 v[18:19], v15 offset0:4 offset1:69
	s_add_i32 s72, s72, s73
	s_add_i32 s74, s74, s75
	v_readlane_b32 s78, v254, 33
	v_readlane_b32 s79, v254, 34
	s_waitcnt lgkmcnt(0)
	v_mul_f32_e32 v8, v0, v18
	v_mul_f32_e32 v18, v1, v19
	v_cvt_pk_bf16_f32 v18, v8, v18
	ds_read2_b32 v[20:21], v15 offset0:134 offset1:199
	v_readlane_b32 s80, v255, 21
	v_readlane_b32 s77, v254, 32
	s_movk_i32 s78, 0x1580
	v_readlane_b32 s82, v255, 23
	s_waitcnt lgkmcnt(0)
	v_mul_f32_e32 v8, v2, v20
	v_mul_f32_e32 v19, v3, v21
	v_cvt_pk_bf16_f32 v19, v8, v19
	v_ashrrev_i32_e32 v8, 31, v24
	v_mul_lo_u32 v8, s56, v8
	v_mad_u64_u32 v[20:21], s[4:5], s56, v24, 0
	v_add3_u32 v21, v21, v8, v22
	ds_read2_b32 v[22:23], v14 offset0:8 offset1:73
	v_lshl_add_u64 v[20:21], v[20:21], 1, s[60:61]
	s_lshl_b64 s[4:5], s[58:59], 1
	v_lshl_add_u64 v[20:21], v[20:21], 0, s[4:5]
	v_lshlrev_b32_e32 v8, 1, v10
	v_lshl_add_u64 v[20:21], v[20:21], 0, v[8:9]
	global_store_dwordx4 v[20:21], v[16:19], off
	s_cmpk_lt_i32 s3, 5504
	v_readlane_b32 s83, v255, 24
	s_waitcnt lgkmcnt(0)
	v_mul_f32_e32 v16, v4, v22
	v_mul_f32_e32 v17, v5, v23
	v_cvt_pk_bf16_f32 v16, v16, v17
	ds_read2_b32 v[18:19], v14 offset0:138 offset1:203
	s_mov_b32 s79, 0x3f22f983
	s_mov_b32 s85, 0xbfc90fda
	s_brev_b32 s86, 1
	s_movk_i32 s87, 0x1f8
	s_waitcnt lgkmcnt(0)
	v_mul_f32_e32 v17, v6, v18
	v_mul_f32_e32 v18, v7, v19
	v_cvt_pk_bf16_f32 v17, v17, v18
	ds_read2_b32 v[18:19], v15 offset0:12 offset1:77
	s_mov_b64 s[88:89], 0x80
	s_mov_b64 s[92:93], 0x4000
	s_mov_b64 s[94:95], 0x4800
	v_readlane_b32 s81, v255, 22
	s_waitcnt lgkmcnt(0)
	v_mul_f32_e32 v18, v0, v18
	v_mul_f32_e32 v19, v1, v19
	v_cvt_pk_bf16_f32 v18, v18, v19
	ds_read2_b32 v[20:21], v15 offset0:142 offset1:207
	s_waitcnt lgkmcnt(0)
	v_mul_f32_e32 v19, v2, v20
	v_mul_f32_e32 v20, v3, v21
	v_cvt_pk_bf16_f32 v19, v19, v20
	v_add_u32_e32 v20, 8, v24
	v_ashrrev_i32_e32 v21, 31, v20
	v_mul_lo_u32 v22, s56, v21
	v_mul_lo_u32 v23, s57, v20
	v_mad_u64_u32 v[20:21], s[6:7], s56, v20, 0
	v_add3_u32 v21, v21, v22, v23
	ds_read2_b32 v[22:23], v14 offset0:16 offset1:81
	v_lshl_add_u64 v[20:21], v[20:21], 1, s[60:61]
	v_lshl_add_u64 v[20:21], v[20:21], 0, s[4:5]
	v_lshl_add_u64 v[20:21], v[20:21], 0, v[8:9]
	global_store_dwordx4 v[20:21], v[16:19], off
	s_waitcnt lgkmcnt(0)
	s_nop 0
	v_mul_f32_e32 v16, v4, v22
	v_mul_f32_e32 v17, v5, v23
	v_cvt_pk_bf16_f32 v16, v16, v17
	ds_read2_b32 v[18:19], v14 offset0:146 offset1:211
	s_waitcnt lgkmcnt(0)
	v_mul_f32_e32 v17, v6, v18
	v_mul_f32_e32 v18, v7, v19
	v_cvt_pk_bf16_f32 v17, v17, v18
	ds_read2_b32 v[18:19], v15 offset0:20 offset1:85
	s_waitcnt lgkmcnt(0)
	v_mul_f32_e32 v18, v0, v18
	v_mul_f32_e32 v19, v1, v19
	v_cvt_pk_bf16_f32 v18, v18, v19
	ds_read2_b32 v[20:21], v15 offset0:150 offset1:215
	s_waitcnt lgkmcnt(0)
	v_mul_f32_e32 v19, v2, v20
	v_mul_f32_e32 v20, v3, v21
	v_cvt_pk_bf16_f32 v19, v19, v20
	v_add_u32_e32 v20, 16, v24
	v_ashrrev_i32_e32 v21, 31, v20
	v_mul_lo_u32 v22, s56, v21
	v_mul_lo_u32 v23, s57, v20
	v_mad_u64_u32 v[20:21], s[6:7], s56, v20, 0
	v_add3_u32 v21, v21, v22, v23
	ds_read2_b32 v[22:23], v14 offset0:24 offset1:89
	v_lshl_add_u64 v[20:21], v[20:21], 1, s[60:61]
	v_lshl_add_u64 v[20:21], v[20:21], 0, s[4:5]
	v_lshl_add_u64 v[20:21], v[20:21], 0, v[8:9]
	global_store_dwordx4 v[20:21], v[16:19], off
	s_waitcnt lgkmcnt(0)
	s_nop 0
	v_mul_f32_e32 v16, v4, v22
	v_mul_f32_e32 v17, v5, v23
	v_cvt_pk_bf16_f32 v16, v16, v17
	ds_read2_b32 v[18:19], v14 offset0:154 offset1:219
	s_waitcnt lgkmcnt(0)
	v_mul_f32_e32 v17, v6, v18
	v_mul_f32_e32 v18, v7, v19
	v_cvt_pk_bf16_f32 v17, v17, v18
	ds_read2_b32 v[18:19], v15 offset0:28 offset1:93
	s_waitcnt lgkmcnt(0)
	v_mul_f32_e32 v18, v0, v18
	v_mul_f32_e32 v19, v1, v19
	v_cvt_pk_bf16_f32 v18, v18, v19
	ds_read2_b32 v[20:21], v15 offset0:158 offset1:223
	s_waitcnt lgkmcnt(0)
; __device__ __forceinline__ unsigned cvt_pk_bf16(float lo, float hi) { unsigned r; asm volatile("v_cvt_pk_bf16_f32 %0, %1, %2" : "=v"(r) : "v"(lo), "v"(hi)); return r; }
; #define LAS __attribute__((address_space(3)))
; #define LDS_WAIT() asm volatile("s_waitcnt lgkmcnt(0)" ::: "memory")
; __device__ __forceinline__ void conv_store(const ConvItem& ci, LAS float* scr, int lane, const float (&v)[64]) {
;     ...
; #pragma unroll
;     for (int j = 0; j < 8; ++j) { const int n = (lane >> 3) + 8 * j; const LAS float* s = scr + (8 * c) * 65 + n;
;         v4u o; o.x = cvt_pk_bf16(s[0 * 65] * s0[0], s[1 * 65] * s0[1]); o.y = cvt_pk_bf16(s[2 * 65] * s0[2], s[3 * 65] * s0[3]); o.z = cvt_pk_bf16(s[4 * 65] * s1[0], s[5 * 65] * s1[1]); o.w = cvt_pk_bf16(s[6 * 65] * s1[2], s[7 * 65] * s1[3]);
;         *(v4u*)(ci.dst + (size_t)(ci.drow0 + n) * ci.ldd + ci.k0 + 8 * c) = o; }
;     LDS_WAIT(); asm volatile("" ::: "memory");
; }
	v_mul_f32_e32 v19, v2, v20
	v_mul_f32_e32 v20, v3, v21
	v_cvt_pk_bf16_f32 v19, v19, v20
	v_add_u32_e32 v20, 24, v24
	v_ashrrev_i32_e32 v21, 31, v20
	v_mul_lo_u32 v22, s56, v21
	v_mul_lo_u32 v23, s57, v20
	v_mad_u64_u32 v[20:21], s[6:7], s56, v20, 0
	v_add3_u32 v21, v21, v22, v23
	ds_read2_b32 v[22:23], v14 offset0:32 offset1:97
	v_lshl_add_u64 v[20:21], v[20:21], 1, s[60:61]
	v_lshl_add_u64 v[20:21], v[20:21], 0, s[4:5]
	v_lshl_add_u64 v[20:21], v[20:21], 0, v[8:9]
	global_store_dwordx4 v[20:21], v[16:19], off
	s_waitcnt lgkmcnt(0)
	s_nop 0
	v_mul_f32_e32 v16, v4, v22
	v_mul_f32_e32 v17, v5, v23
	v_cvt_pk_bf16_f32 v16, v16, v17
	ds_read2_b32 v[18:19], v14 offset0:162 offset1:227
	s_waitcnt lgkmcnt(0)
	v_mul_f32_e32 v17, v6, v18
	v_mul_f32_e32 v18, v7, v19
	v_cvt_pk_bf16_f32 v17, v17, v18
	ds_read2_b32 v[18:19], v15 offset0:36 offset1:101
	s_waitcnt lgkmcnt(0)
	v_mul_f32_e32 v18, v0, v18
	v_mul_f32_e32 v19, v1, v19
	v_cvt_pk_bf16_f32 v18, v18, v19
	ds_read2_b32 v[20:21], v15 offset0:166 offset1:231
	s_waitcnt lgkmcnt(0)
	v_mul_f32_e32 v19, v2, v20
	v_mul_f32_e32 v20, v3, v21
	v_cvt_pk_bf16_f32 v19, v19, v20
	v_add_u32_e32 v20, 32, v24
	v_ashrrev_i32_e32 v21, 31, v20
	v_mul_lo_u32 v22, s56, v21
	v_mul_lo_u32 v23, s57, v20
	v_mad_u64_u32 v[20:21], s[6:7], s56, v20, 0
	v_add3_u32 v21, v21, v22, v23
	ds_read2_b32 v[22:23], v14 offset0:40 offset1:105
	v_lshl_add_u64 v[20:21], v[20:21], 1, s[60:61]
	v_lshl_add_u64 v[20:21], v[20:21], 0, s[4:5]
	v_lshl_add_u64 v[20:21], v[20:21], 0, v[8:9]
	global_store_dwordx4 v[20:21], v[16:19], off
	s_waitcnt lgkmcnt(0)
	s_nop 0
	v_mul_f32_e32 v16, v4, v22
	v_mul_f32_e32 v17, v5, v23
	v_cvt_pk_bf16_f32 v16, v16, v17
	ds_read2_b32 v[18:19], v14 offset0:170 offset1:235
	s_waitcnt lgkmcnt(0)
	v_mul_f32_e32 v17, v6, v18
	v_mul_f32_e32 v18, v7, v19
	v_cvt_pk_bf16_f32 v17, v17, v18
	ds_read2_b32 v[18:19], v15 offset0:44 offset1:109
	s_waitcnt lgkmcnt(0)
	v_mul_f32_e32 v18, v0, v18
	v_mul_f32_e32 v19, v1, v19
	v_cvt_pk_bf16_f32 v18, v18, v19
	ds_read2_b32 v[20:21], v15 offset0:174 offset1:239
	s_waitcnt lgkmcnt(0)
	v_mul_f32_e32 v19, v2, v20
	v_mul_f32_e32 v20, v3, v21
	v_cvt_pk_bf16_f32 v19, v19, v20
	v_add_u32_e32 v20, 40, v24
	v_ashrrev_i32_e32 v21, 31, v20
	v_mul_lo_u32 v22, s56, v21
	v_mul_lo_u32 v23, s57, v20
	v_mad_u64_u32 v[20:21], s[6:7], s56, v20, 0
	v_add3_u32 v21, v21, v22, v23
	ds_read2_b32 v[22:23], v14 offset0:48 offset1:113
	v_lshl_add_u64 v[20:21], v[20:21], 1, s[60:61]
	v_lshl_add_u64 v[20:21], v[20:21], 0, s[4:5]
	v_lshl_add_u64 v[20:21], v[20:21], 0, v[8:9]
	global_store_dwordx4 v[20:21], v[16:19], off
	s_waitcnt lgkmcnt(0)
	s_nop 0
	v_mul_f32_e32 v16, v4, v22
	v_mul_f32_e32 v17, v5, v23
	v_cvt_pk_bf16_f32 v16, v16, v17
	ds_read2_b32 v[18:19], v14 offset0:178 offset1:243
	s_waitcnt lgkmcnt(0)
	v_mul_f32_e32 v17, v6, v18
	v_mul_f32_e32 v18, v7, v19
	v_cvt_pk_bf16_f32 v17, v17, v18
	ds_read2_b32 v[18:19], v15 offset0:52 offset1:117
	s_waitcnt lgkmcnt(0)
	v_mul_f32_e32 v18, v0, v18
	v_mul_f32_e32 v19, v1, v19
	v_cvt_pk_bf16_f32 v18, v18, v19
	ds_read2_b32 v[20:21], v15 offset0:182 offset1:247
	s_waitcnt lgkmcnt(0)
	v_mul_f32_e32 v19, v2, v20
	v_mul_f32_e32 v20, v3, v21
	v_cvt_pk_bf16_f32 v19, v19, v20
	v_add_u32_e32 v20, 48, v24
	v_ashrrev_i32_e32 v21, 31, v20
	v_mul_lo_u32 v22, s56, v21
	v_mul_lo_u32 v23, s57, v20
	v_mad_u64_u32 v[20:21], s[6:7], s56, v20, 0
	v_add3_u32 v21, v21, v22, v23
	ds_read2_b32 v[22:23], v14 offset0:56 offset1:121
	v_lshl_add_u64 v[20:21], v[20:21], 1, s[60:61]
	v_lshl_add_u64 v[20:21], v[20:21], 0, s[4:5]
	v_lshl_add_u64 v[20:21], v[20:21], 0, v[8:9]
	global_store_dwordx4 v[20:21], v[16:19], off
	s_waitcnt lgkmcnt(0)
	v_mul_f32_e32 v4, v4, v22
	v_mul_f32_e32 v5, v5, v23
	v_cvt_pk_bf16_f32 v4, v4, v5
	ds_read2_b32 v[16:17], v14 offset0:186 offset1:251
	s_waitcnt lgkmcnt(0)
	v_mul_f32_e32 v5, v6, v16
	v_mul_f32_e32 v6, v7, v17
	v_cvt_pk_bf16_f32 v5, v5, v6
	ds_read2_b32 v[6:7], v15 offset0:60 offset1:125
	s_waitcnt lgkmcnt(0)
	v_mul_f32_e32 v0, v0, v6
	v_mul_f32_e32 v1, v1, v7
	v_cvt_pk_bf16_f32 v6, v0, v1
	ds_read2_b32 v[0:1], v15 offset0:190 offset1:255
	s_waitcnt lgkmcnt(0)
	v_mul_f32_e32 v0, v2, v0
	v_mul_f32_e32 v1, v3, v1
	v_cvt_pk_bf16_f32 v7, v0, v1
	v_add_u32_e32 v0, 56, v24
	v_ashrrev_i32_e32 v1, 31, v0
	v_mul_lo_u32 v2, s56, v1
	v_mul_lo_u32 v3, s57, v0
	v_mad_u64_u32 v[0:1], s[6:7], s56, v0, 0
	v_add3_u32 v1, v1, v2, v3
	v_lshl_add_u64 v[0:1], v[0:1], 1, s[60:61]
	v_lshl_add_u64 v[0:1], v[0:1], 0, s[4:5]
	v_lshl_add_u64 v[0:1], v[0:1], 0, v[8:9]
	global_store_dwordx4 v[0:1], v[4:7], off
	s_waitcnt lgkmcnt(0)
	s_cbranch_scc0 .Lcvp30_ret

; #define LAS __attribute__((address_space(3)))
; __global__ void __launch_bounds__(NWAVES * 64, 2) mk_fwd(Args args) {
;     ...
;             PH_LOCALS
;             LAS float* scr = (LAS float*)(lds + RING_OFF + wave * 16640);   static_assert(8 * 16640 <= LDSCTL_OFF, "converter scratch below the LDS control words");
;             constexpr int I_UP = (D / 64) * (NUP / 64), I_DN = (DFF / 64) * (D / 64), I_IN = (D / 64) * (DINP / 64), I_GLU = 16 * 16, I_L = 4 * 16, I_V1 = 16 * 4, I_V2 = 4 * 16,
;                           I_BS5 = 16 * 32, I_BAT = 8 * 32, I_BRW = 16 * 32, I_OUT = 32 * 32;
;             constexpr int NITEMS = 2 * I_UP + 2 * I_DN + I_IN + I_GLU + 3 * I_L + I_V1 + I_V2 + I_BS5 + I_BAT + I_BRW + I_OUT;
;             const int lv = l > 0 ? l - 1 : 0;
;     ...
;             for (int it = gw; it < NITEMS; it += NGW) {
;                 ConvItem ca; CONV_DESC(ca, it);
.LBB0_1151:
	v_readlane_b32 s99, v254, 35
	v_readlane_b32 s98, v254, 38
	s_nop 3
	s_cmp_lt_u32 s99, 96
	s_cbranch_scc1 .Lcvskip_p13
	s_cmp_gt_u32 s98, 2
	s_cbranch_scc1 .Lcvskip_p13
	v_mov_b32_e32 v250, v254
	v_mov_b32_e32 v251, v255
	v_writelane_b32 v252, s0, 0
	s_nop 0
	v_writelane_b32 v252, s1, 1
	s_nop 0
	v_writelane_b32 v252, s2, 2
	s_nop 0
	v_writelane_b32 v252, s3, 3
	s_nop 0
	v_writelane_b32 v252, s4, 4
	s_nop 0
	v_writelane_b32 v252, s5, 5
	s_nop 0
	v_writelane_b32 v252, s6, 6
	s_nop 0
	v_writelane_b32 v252, s7, 7
	s_nop 0
	v_writelane_b32 v252, s8, 8
	s_nop 0
	v_writelane_b32 v252, s9, 9
	s_nop 0
	v_writelane_b32 v252, s10, 10
	s_nop 0
	v_writelane_b32 v252, s11, 11
	s_nop 0
	v_writelane_b32 v252, s12, 12
	s_nop 0
	v_writelane_b32 v252, s13, 13
	s_nop 0
	v_writelane_b32 v252, s14, 14
	s_nop 0
	v_writelane_b32 v252, s15, 15
	s_nop 0
	v_writelane_b32 v252, s16, 16
	s_nop 0
	v_writelane_b32 v252, s17, 17
	s_nop 0
	v_writelane_b32 v252, s18, 18
	s_nop 0
	v_writelane_b32 v252, s19, 19
	s_nop 0
	v_writelane_b32 v252, s20, 20
	s_nop 0
	v_writelane_b32 v252, s21, 21
	s_nop 0
	v_writelane_b32 v252, s22, 22
	s_nop 0
	v_writelane_b32 v252, s23, 23
	s_nop 0
	v_writelane_b32 v252, s24, 24
	s_nop 0
	v_writelane_b32 v252, s25, 25
	s_nop 0
	v_writelane_b32 v252, s26, 26
	s_nop 0
	v_writelane_b32 v252, s27, 27
	s_nop 0
	v_writelane_b32 v252, s28, 28
	s_nop 0
	v_writelane_b32 v252, s29, 29
	s_nop 0
	v_writelane_b32 v252, s30, 30
	s_nop 0
	v_writelane_b32 v252, s31, 31
	s_nop 0
	v_writelane_b32 v252, s32, 32
	s_nop 0
	v_writelane_b32 v252, s33, 33
	s_nop 0
	v_writelane_b32 v252, s34, 34
	s_nop 0
	v_writelane_b32 v252, s35, 35
	s_nop 0
	v_writelane_b32 v252, s36, 36
	s_nop 0
	v_writelane_b32 v252, s37, 37
	s_nop 0
	v_writelane_b32 v252, s38, 38
	s_nop 0
	v_writelane_b32 v252, s39, 39
	s_nop 0
	v_writelane_b32 v252, s40, 40
	s_nop 0
	v_writelane_b32 v252, s41, 41
	s_nop 0
	v_writelane_b32 v252, s42, 42
	s_nop 0
	v_writelane_b32 v252, s43, 43
	s_nop 0
	v_writelane_b32 v252, s44, 44
	s_nop 0
	v_writelane_b32 v252, s45, 45
	s_nop 0
	v_writelane_b32 v252, s46, 46
	s_nop 0
	v_writelane_b32 v252, s47, 47
	s_nop 0
	v_writelane_b32 v252, s48, 48
	s_nop 0
	v_writelane_b32 v252, s49, 49
	s_nop 0
	v_writelane_b32 v252, s50, 50
	s_nop 0
	v_writelane_b32 v252, s51, 51
	s_nop 0
	v_writelane_b32 v252, s52, 52
	s_nop 0
	v_writelane_b32 v252, s53, 53
	s_nop 0
	v_writelane_b32 v252, s54, 54
	s_nop 0
	v_writelane_b32 v252, s55, 55
	s_nop 0
	v_writelane_b32 v252, s56, 56
	s_nop 0
	v_writelane_b32 v252, s57, 57
	s_nop 0
	v_writelane_b32 v252, s58, 58
	s_nop 0
	v_writelane_b32 v252, s59, 59
	s_nop 0
	v_writelane_b32 v252, s60, 60
	s_nop 0
	v_writelane_b32 v252, s61, 61
	s_nop 0
	v_writelane_b32 v252, s62, 62
	s_nop 0
	v_writelane_b32 v252, s63, 63
	s_nop 0
	v_writelane_b32 v253, s64, 0
	s_nop 0
	v_writelane_b32 v253, s65, 1
	s_nop 0
	v_writelane_b32 v253, s66, 2
	s_nop 0
	v_writelane_b32 v253, s67, 3
	s_nop 0
	v_writelane_b32 v253, s68, 4
	s_nop 0
	v_writelane_b32 v253, s69, 5
	s_nop 0
	v_writelane_b32 v253, s70, 6
	s_nop 0
	v_writelane_b32 v253, s71, 7
	s_nop 0
	v_writelane_b32 v253, s72, 8
	s_nop 0
	v_writelane_b32 v253, s73, 9
	s_nop 0
	v_writelane_b32 v253, s74, 10
	s_nop 0
	v_writelane_b32 v253, s75, 11
	s_nop 0
	v_writelane_b32 v253, s76, 12
	s_nop 0
	v_writelane_b32 v253, s77, 13
	s_nop 0
	v_writelane_b32 v253, s78, 14
	s_nop 0
	v_writelane_b32 v253, s79, 15
	s_nop 0
	v_writelane_b32 v253, s80, 16
	s_nop 0
	v_writelane_b32 v253, s81, 17
	s_nop 0
	v_writelane_b32 v253, s82, 18
	s_nop 0
	v_writelane_b32 v253, s83, 19
	s_nop 0
	v_writelane_b32 v253, s84, 20
	s_nop 0
	v_writelane_b32 v253, s85, 21
	s_nop 0
	v_writelane_b32 v253, s86, 22
	s_nop 0
	v_writelane_b32 v253, s87, 23
	s_nop 0
	v_writelane_b32 v253, s88, 24
	s_nop 0
	v_writelane_b32 v253, s89, 25
	s_nop 0
	v_writelane_b32 v253, s90, 26
	s_nop 0
	v_writelane_b32 v253, s91, 27
	s_nop 0
	v_writelane_b32 v253, s92, 28
	s_nop 0
	v_writelane_b32 v253, s93, 29
	s_nop 0
	v_writelane_b32 v253, s94, 30
	s_nop 0
	v_writelane_b32 v253, s95, 31
	s_nop 0
	v_writelane_b32 v253, s96, 32
	s_nop 0
	v_writelane_b32 v253, s97, 33
	s_nop 0
	v_writelane_b32 v253, vcc_lo, 34
	s_nop 0
	v_writelane_b32 v253, vcc_hi, 35
	s_nop 1
	v_readlane_b32 s84, v254, 35
	s_nop 3
	v_readlane_b32 s0, v254, 8
	v_readlane_b32 s4, v254, 10
	v_readlane_b32 s1, v254, 9
	v_mbcnt_lo_u32_b32 v11, -1, 0
	v_mbcnt_hi_u32_b32 v11, -1, v11
	s_load_dword s6, s[0:1], 0x0
	s_mov_b32 s3, s84
	s_waitcnt lgkmcnt(0)
	s_movk_i32 s6, 160
	s_lshl_b32 s3, s3, 3
	v_readlane_b32 s0, v254, 0
	s_add_i32 s3, s3, s4
	s_add_i32 s3, s3, 0x2800
	v_readlane_b32 s1, v254, 1
	s_cmpk_gt_i32 s3, 16767
	s_cbranch_scc1 .Lcvp130_ret
	s_load_dwordx2 s[8:9], s[0:1], 0x138
	v_readlane_b32 s14, v254, 38
	s_nop 0
	s_add_i32 s14, s14, 1
	s_mulk_i32 s4, 0x4100
	s_add_i32 s7, s4, 0
	v_sub_u32_e64 v0, s14, 1 clamp
	s_lshl_b32 s33, s6, 3
	v_readfirstlane_b32 s4, v0
	s_lshl_b32 s96, s4, 16
	s_waitcnt lgkmcnt(0)
	s_add_u32 s4, s8, 0x22800000
	s_addc_u32 s5, s9, 0
	v_writelane_b32 v254, s4, 39
	s_mov_b32 s15, s97
	v_and_b32_e32 v0, 7, v11
	v_writelane_b32 v254, s5, 40
	s_add_u32 s4, s8, 0x22780000
	s_addc_u32 s5, s9, 0
	v_writelane_b32 v254, s4, 41
	v_ashrrev_i32_e32 v13, 3, v11
	v_lshlrev_b32_e32 v10, 3, v0
	v_writelane_b32 v254, s5, 42
	s_lshl_b32 s4, s14, 18
	s_add_u32 s10, s8, 0x22700000
	s_addc_u32 s11, s9, 0
	v_writelane_b32 v254, s10, 43
	s_mov_b32 s5, s97
	v_mul_u32_u24_e32 v0, 0x820, v0
	v_writelane_b32 v254, s11, 44
	s_mul_i32 s10, s14, 0x18000
	s_mov_b32 s11, s97
	v_writelane_b32 v254, s10, 45
	v_lshlrev_b32_e32 v1, 2, v13
	v_lshl_add_u32 v12, v11, 2, s7
	v_writelane_b32 v254, s11, 46
	s_add_u32 s10, s8, 0x22680000
	s_addc_u32 s11, s9, 0
	v_writelane_b32 v254, s10, 47
	v_add3_u32 v14, s7, v0, v1
	s_mov_b32 s41, s97
	v_writelane_b32 v254, s11, 48
	s_add_u32 s10, s8, 0x22600000
	s_addc_u32 s11, s9, 0
	v_writelane_b32 v254, s10, 49
	s_nop 1
	v_writelane_b32 v254, s11, 50
	s_lshl_b32 s10, s14, 20
	s_mov_b32 s11, s97
	v_writelane_b32 v254, s10, 51
	s_nop 1
	v_writelane_b32 v254, s11, 52
	s_add_u32 s10, s8, 0x22400000
	s_addc_u32 s11, s9, 0
	v_writelane_b32 v254, s10, 53
	s_nop 1
	v_writelane_b32 v254, s11, 54
	s_lshl_b32 s10, s14, 21
	s_mov_b32 s11, s97
	v_writelane_b32 v254, s10, 55
	s_nop 1
	v_writelane_b32 v254, s11, 56
	s_add_u32 s10, s8, 0x22e80000
	s_addc_u32 s11, s9, 0
	v_writelane_b32 v254, s10, 57
	s_nop 1
	v_writelane_b32 v254, s11, 58
	s_add_u32 s10, s8, 0x27b80000
	s_addc_u32 s11, s9, 0
	v_writelane_b32 v254, s10, 59
	s_nop 1
	v_writelane_b32 v254, s11, 60
	s_add_u32 s10, s8, 0x22880000
	s_addc_u32 s11, s9, 0
	v_writelane_b32 v254, s10, 61
	s_nop 1
	v_writelane_b32 v254, s11, 62
	s_lshl_b32 s10, s14, 22
	s_add_u32 s12, s8, 0x23280000
	s_addc_u32 s13, s9, 0
	v_writelane_b32 v254, s12, 63
	s_mov_b32 s11, s97
	s_nop 0
	v_writelane_b32 v255, s13, 0
	s_mul_i32 s12, s14, 0xac0000
	s_mov_b32 s13, s97
	v_writelane_b32 v255, s12, 1
	s_nop 1
	v_writelane_b32 v255, s13, 2
	s_add_u32 s12, s8, 0x26580000
	s_addc_u32 s13, s9, 0
	v_writelane_b32 v255, s12, 3
	s_nop 1
	v_writelane_b32 v255, s13, 4
	s_add_u32 s12, s8, 0x1d200000
	s_addc_u32 s13, s9, 0
	s_lshl_b32 s40, s14, 11
	v_writelane_b32 v255, s12, 5
	s_add_u32 s16, s8, 0x1e800000
	s_addc_u32 s17, s9, 0
	v_writelane_b32 v255, s13, 6
	v_writelane_b32 v255, s16, 7
	s_mul_i32 s12, s14, 0x1de0000
	s_mul_i32 s14, s14, 0x1580000
	v_writelane_b32 v255, s17, 8
	v_writelane_b32 v255, s14, 9
	s_mov_b32 s13, s97
	s_nop 0
	v_writelane_b32 v255, s15, 10
	s_add_u32 s14, s8, 0x23a80000
	s_addc_u32 s15, s9, 0
	v_writelane_b32 v255, s14, 11
	s_add_u32 s8, s8, 0x1a700000
	s_addc_u32 s9, s9, 0
	v_writelane_b32 v255, s15, 12
	v_writelane_b32 v255, s8, 13
	s_lshl_b64 s[4:5], s[4:5], 2
	s_lshl_b32 s7, s3, 4
	v_writelane_b32 v255, s9, 14
	v_writelane_b32 v255, s4, 15
	s_add_i32 s72, s7, 0xc00
	s_lshl_b32 s7, s3, 1
	v_writelane_b32 v255, s5, 16
	s_lshl_b64 s[4:5], s[10:11], 2
	v_writelane_b32 v255, s4, 17
	s_lshl_b32 s66, s3, 6
	s_lshl_b32 s67, s6, 9
	v_writelane_b32 v255, s5, 18
	s_lshl_b64 s[4:5], s[12:13], 2
	v_writelane_b32 v255, s4, 19
	s_lshl_b32 s68, s3, 5
	s_lshl_b32 s69, s6, 8
	v_writelane_b32 v255, s5, 20
	v_writelane_b32 v255, s80, 21
	s_lshl_b32 s70, s3, 2
	s_lshl_b32 s71, s6, 5
	v_writelane_b32 v255, s81, 22
	v_writelane_b32 v255, s82, 23
	s_lshl_b32 s73, s6, 7
	s_add_i32 s74, s7, 0x13500
	s_lshl_b32 s75, s6, 4
	v_writelane_b32 v255, s83, 24
	s_branch .Lcvp130_31

; #define LAS __attribute__((address_space(3)))
; __device__ __forceinline__ void conv_load(const ConvItem& ci, int lane, float (&v)[64]) {
;     const bool okc = ci.srcc >= 0 && (ci.srcc + lane) < ci.ncols;
;     const float* base = ci.W + (okc ? ci.srcc + lane : 0);
;     const int kmax = ci.Ksrc - 1;
; #pragma unroll
;     for (int i = 0; i < 64; ++i) { const int k = ci.k0 + i, kk = k < kmax ? k : kmax; v[i] = __builtin_nontemporal_load(base + (size_t)kk * ci.ldw); }
; #pragma unroll
;     for (int i = 0; i < 64; ++i) v[i] = (okc && (ci.k0 + i) < ci.Ksrc) ? v[i] : 0.f;
; }
; __device__ __forceinline__ void conv_store(const ConvItem& ci, LAS float* scr, int lane, const float (&v)[64]) {
;     const int c = lane & 7;
;     f32x4 s0 = {1.f, 1.f, 1.f, 1.f}, s1 = s0;
;     if (ci.ks) { const int kb = ci.k0 + 8 * c < ci.Ksrc - 8 ? ci.k0 + 8 * c : ci.Ksrc - 8; s0 = *(const f32x4*)(ci.ks + kb); s1 = *(const f32x4*)(ci.ks + kb + 4); }
; #pragma unroll
;     for (int i = 0; i < 64; ++i) scr[i * 65 + lane] = v[i];
.Lcvp130_30:
	s_cmp_lt_i32 s58, s76
	s_cselect_b64 s[4:5], -1, 0
	s_and_b64 s[4:5], vcc, s[4:5]
	s_cmp_lt_i32 s64, s76
	s_waitcnt vmcnt(62)
	v_cndmask_b32_e64 v21, 0, v21, s[4:5]
	s_cselect_b64 s[4:5], -1, 0
	s_and_b64 s[4:5], vcc, s[4:5]
	s_cmp_lt_i32 s65, s76
	v_cndmask_b32_e64 v20, 0, v20, s[4:5]
	s_cselect_b64 s[4:5], -1, 0
	s_and_b64 s[4:5], vcc, s[4:5]
	s_cmp_lt_i32 s78, s76
	s_waitcnt vmcnt(61)
	v_cndmask_b32_e64 v19, 0, v19, s[4:5]
	s_cselect_b64 s[4:5], -1, 0
	s_and_b64 s[4:5], vcc, s[4:5]
	s_cmp_lt_i32 s79, s76
	s_waitcnt vmcnt(60)
	v_cndmask_b32_e64 v18, 0, v18, s[4:5]
	s_cselect_b64 s[4:5], -1, 0
	s_and_b64 s[4:5], vcc, s[4:5]
	s_cmp_lt_i32 s80, s76
	s_waitcnt vmcnt(59)
	v_cndmask_b32_e64 v17, 0, v17, s[4:5]
	s_cselect_b64 s[4:5], -1, 0
	s_and_b64 s[4:5], vcc, s[4:5]
	s_cmp_lt_i32 s81, s76
	s_waitcnt vmcnt(58)
	v_cndmask_b32_e64 v16, 0, v16, s[4:5]
	s_cselect_b64 s[4:5], -1, 0
	s_and_b64 s[4:5], vcc, s[4:5]
	s_cmp_lt_i32 s82, s76
	s_waitcnt vmcnt(57)
	v_cndmask_b32_e64 v15, 0, v15, s[4:5]
	s_cselect_b64 s[4:5], -1, 0
	s_and_b64 s[4:5], vcc, s[4:5]
	s_cmp_lt_i32 s83, s76
	s_waitcnt vmcnt(56)
	v_cndmask_b32_e64 v8, 0, v8, s[4:5]
	s_cselect_b64 s[4:5], -1, 0
	s_and_b64 s[4:5], vcc, s[4:5]
	s_cmp_lt_i32 s85, s76
	s_waitcnt vmcnt(55)
	v_cndmask_b32_e64 v29, 0, v29, s[4:5]
	s_cselect_b64 s[4:5], -1, 0
	s_and_b64 s[4:5], vcc, s[4:5]
	s_cmp_lt_i32 s86, s76
	s_waitcnt vmcnt(54)
	v_cndmask_b32_e64 v28, 0, v28, s[4:5]
	s_cselect_b64 s[4:5], -1, 0
	s_and_b64 s[4:5], vcc, s[4:5]
	s_cmp_lt_i32 s87, s76
	s_waitcnt vmcnt(53)
	v_cndmask_b32_e64 v27, 0, v27, s[4:5]
	s_cselect_b64 s[4:5], -1, 0
	s_and_b64 s[4:5], vcc, s[4:5]
	s_cmp_lt_i32 s88, s76
	s_waitcnt vmcnt(52)
	v_cndmask_b32_e64 v26, 0, v26, s[4:5]
	s_cselect_b64 s[4:5], -1, 0
	s_and_b64 s[4:5], vcc, s[4:5]
	s_cmp_lt_i32 s89, s76
	s_waitcnt vmcnt(51)
	v_cndmask_b32_e64 v25, 0, v25, s[4:5]
	s_cselect_b64 s[4:5], -1, 0
	s_and_b64 s[4:5], vcc, s[4:5]
	s_cmp_lt_i32 s90, s76
	s_waitcnt vmcnt(50)
	v_cndmask_b32_e64 v24, 0, v24, s[4:5]
	s_cselect_b64 s[4:5], -1, 0
	s_and_b64 s[4:5], vcc, s[4:5]
	s_cmp_lt_i32 s92, s76
	s_waitcnt vmcnt(49)
	v_cndmask_b32_e64 v23, 0, v23, s[4:5]
	s_cselect_b64 s[4:5], -1, 0
	s_and_b64 s[4:5], vcc, s[4:5]
	s_cmp_lt_i32 s93, s76
	s_waitcnt vmcnt(48)
	v_cndmask_b32_e64 v22, 0, v22, s[4:5]
	s_cselect_b64 s[4:5], -1, 0
	s_and_b64 s[4:5], vcc, s[4:5]
	s_cmp_lt_i32 s94, s76
	s_waitcnt vmcnt(47)
	v_cndmask_b32_e64 v37, 0, v37, s[4:5]
	s_cselect_b64 s[4:5], -1, 0
	s_and_b64 s[4:5], vcc, s[4:5]
	s_cmp_lt_i32 s95, s76
	s_waitcnt vmcnt(46)
	v_cndmask_b32_e64 v36, 0, v36, s[4:5]
	s_cselect_b64 s[4:5], -1, 0
	s_and_b64 s[4:5], vcc, s[4:5]
	s_cmp_lt_i32 s50, s76
	s_waitcnt vmcnt(45)
	v_cndmask_b32_e64 v35, 0, v35, s[4:5]
	s_cselect_b64 s[4:5], -1, 0
	s_and_b64 s[4:5], vcc, s[4:5]
	s_cmp_lt_i32 s51, s76
	s_waitcnt vmcnt(44)
	v_cndmask_b32_e64 v34, 0, v34, s[4:5]
	s_cselect_b64 s[4:5], -1, 0
	s_and_b64 s[4:5], vcc, s[4:5]
	s_cmp_lt_i32 s52, s76
	s_waitcnt vmcnt(43)
	v_cndmask_b32_e64 v33, 0, v33, s[4:5]
	s_cselect_b64 s[4:5], -1, 0
	s_and_b64 s[4:5], vcc, s[4:5]
	s_cmp_lt_i32 s53, s76
	s_waitcnt vmcnt(42)
	v_cndmask_b32_e64 v32, 0, v32, s[4:5]
	s_cselect_b64 s[4:5], -1, 0
	s_and_b64 s[4:5], vcc, s[4:5]
	s_cmp_lt_i32 s6, s76
	s_waitcnt vmcnt(41)
	v_cndmask_b32_e64 v31, 0, v31, s[4:5]
	s_cselect_b64 s[4:5], -1, 0
	s_and_b64 s[4:5], vcc, s[4:5]
	s_cmp_lt_i32 s7, s76
	s_waitcnt vmcnt(40)
	v_cndmask_b32_e64 v30, 0, v30, s[4:5]
	s_cselect_b64 s[4:5], -1, 0
	s_and_b64 s[4:5], vcc, s[4:5]
	s_cmp_lt_i32 s8, s76
	s_waitcnt vmcnt(39)
	v_cndmask_b32_e64 v45, 0, v45, s[4:5]
	s_cselect_b64 s[4:5], -1, 0
	s_and_b64 s[4:5], vcc, s[4:5]
	s_cmp_lt_i32 s9, s76
	s_waitcnt vmcnt(38)
	v_cndmask_b32_e64 v44, 0, v44, s[4:5]
	s_cselect_b64 s[4:5], -1, 0
	s_and_b64 s[4:5], vcc, s[4:5]
	s_cmp_lt_i32 s10, s76
	s_waitcnt vmcnt(37)
	v_cndmask_b32_e64 v43, 0, v43, s[4:5]
	s_cselect_b64 s[4:5], -1, 0
	s_and_b64 s[4:5], vcc, s[4:5]
	s_cmp_lt_i32 s11, s76
	s_waitcnt vmcnt(36)
	v_cndmask_b32_e64 v42, 0, v42, s[4:5]
	s_cselect_b64 s[4:5], -1, 0
	s_and_b64 s[4:5], vcc, s[4:5]
	s_cmp_lt_i32 s14, s76
	s_waitcnt vmcnt(35)
	v_cndmask_b32_e64 v41, 0, v41, s[4:5]
	s_cselect_b64 s[4:5], -1, 0
	s_and_b64 s[4:5], vcc, s[4:5]
	s_cmp_lt_i32 s15, s76
	s_waitcnt vmcnt(34)
	v_cndmask_b32_e64 v40, 0, v40, s[4:5]
	s_cselect_b64 s[4:5], -1, 0
	s_and_b64 s[4:5], vcc, s[4:5]
	s_cmp_lt_i32 s16, s76
	s_waitcnt vmcnt(33)
	v_cndmask_b32_e64 v39, 0, v39, s[4:5]
	s_cselect_b64 s[4:5], -1, 0
	s_and_b64 s[4:5], vcc, s[4:5]
	s_cmp_lt_i32 s17, s76
	s_waitcnt vmcnt(32)
	v_cndmask_b32_e64 v38, 0, v38, s[4:5]
	s_cselect_b64 s[4:5], -1, 0
	s_and_b64 s[4:5], vcc, s[4:5]
	s_cmp_lt_i32 s12, s76
	s_waitcnt vmcnt(31)
	v_cndmask_b32_e64 v53, 0, v53, s[4:5]
	s_cselect_b64 s[4:5], -1, 0
	s_and_b64 s[4:5], vcc, s[4:5]
	s_cmp_lt_i32 s13, s76
	s_waitcnt vmcnt(30)
	v_cndmask_b32_e64 v52, 0, v52, s[4:5]
	s_cselect_b64 s[4:5], -1, 0
	s_and_b64 s[4:5], vcc, s[4:5]
	s_cmp_lt_i32 s20, s76
	s_waitcnt vmcnt(29)
	v_cndmask_b32_e64 v51, 0, v51, s[4:5]
	s_cselect_b64 s[4:5], -1, 0
	s_and_b64 s[4:5], vcc, s[4:5]
	s_cmp_lt_i32 s21, s76
	s_waitcnt vmcnt(28)
	v_cndmask_b32_e64 v50, 0, v50, s[4:5]
	s_cselect_b64 s[4:5], -1, 0
	s_and_b64 s[4:5], vcc, s[4:5]
	s_cmp_lt_i32 s24, s76
	s_waitcnt vmcnt(27)
	v_cndmask_b32_e64 v49, 0, v49, s[4:5]
	s_cselect_b64 s[4:5], -1, 0
	s_and_b64 s[4:5], vcc, s[4:5]
	s_cmp_lt_i32 s25, s76
	s_waitcnt vmcnt(26)
	v_cndmask_b32_e64 v48, 0, v48, s[4:5]
	s_cselect_b64 s[4:5], -1, 0
	s_and_b64 s[4:5], vcc, s[4:5]
	s_cmp_lt_i32 s26, s76
	s_waitcnt vmcnt(25)
	v_cndmask_b32_e64 v47, 0, v47, s[4:5]
	s_cselect_b64 s[4:5], -1, 0
	s_and_b64 s[4:5], vcc, s[4:5]
	s_cmp_lt_i32 s27, s76
	s_waitcnt vmcnt(24)
; __device__ __forceinline__ unsigned cvt_pk_bf16(float lo, float hi) { unsigned r; asm volatile("v_cvt_pk_bf16_f32 %0, %1, %2" : "=v"(r) : "v"(lo), "v"(hi)); return r; }
; #define LAS __attribute__((address_space(3)))
; #define LDS_WAIT() asm volatile("s_waitcnt lgkmcnt(0)" ::: "memory")
; __device__ __forceinline__ void conv_load(const ConvItem& ci, int lane, float (&v)[64]) {
;     ...
;     for (int i = 0; i < 64; ++i) v[i] = (okc && (ci.k0 + i) < ci.Ksrc) ? v[i] : 0.f;
; }
; __device__ __forceinline__ void conv_store(const ConvItem& ci, LAS float* scr, int lane, const float (&v)[64]) {
;     const int c = lane & 7;
;     f32x4 s0 = {1.f, 1.f, 1.f, 1.f}, s1 = s0;
;     if (ci.ks) { const int kb = ci.k0 + 8 * c < ci.Ksrc - 8 ? ci.k0 + 8 * c : ci.Ksrc - 8; s0 = *(const f32x4*)(ci.ks + kb); s1 = *(const f32x4*)(ci.ks + kb + 4); }
; #pragma unroll
;     for (int i = 0; i < 64; ++i) scr[i * 65 + lane] = v[i];
;     LDS_WAIT(); asm volatile("" ::: "memory");
; #pragma unroll
;     for (int j = 0; j < 8; ++j) { const int n = (lane >> 3) + 8 * j; const LAS float* s = scr + (8 * c) * 65 + n;
;         v4u o; o.x = cvt_pk_bf16(s[0 * 65] * s0[0], s[1 * 65] * s0[1]); o.y = cvt_pk_bf16(s[2 * 65] * s0[2], s[3 * 65] * s0[3]); o.z = cvt_pk_bf16(s[4 * 65] * s1[0], s[5 * 65] * s1[1]); o.w = cvt_pk_bf16(s[6 * 65] * s1[2], s[7 * 65] * s1[3]);
	v_cndmask_b32_e64 v46, 0, v46, s[4:5]
	s_cselect_b64 s[4:5], -1, 0
	s_and_b64 s[4:5], vcc, s[4:5]
	s_cmp_lt_i32 s18, s76
	s_waitcnt vmcnt(23)
	v_cndmask_b32_e64 v61, 0, v61, s[4:5]
	s_cselect_b64 s[4:5], -1, 0
	s_and_b64 s[4:5], vcc, s[4:5]
	s_cmp_lt_i32 s19, s76
	s_waitcnt vmcnt(22)
	v_cndmask_b32_e64 v60, 0, v60, s[4:5]
	s_cselect_b64 s[4:5], -1, 0
	s_and_b64 s[4:5], vcc, s[4:5]
	s_cmp_lt_i32 s28, s76
	s_waitcnt vmcnt(21)
	v_cndmask_b32_e64 v59, 0, v59, s[4:5]
	s_cselect_b64 s[4:5], -1, 0
	s_and_b64 s[4:5], vcc, s[4:5]
	s_cmp_lt_i32 s29, s76
	s_waitcnt vmcnt(20)
	v_cndmask_b32_e64 v58, 0, v58, s[4:5]
	s_cselect_b64 s[4:5], -1, 0
	s_and_b64 s[4:5], vcc, s[4:5]
	s_cmp_lt_i32 s22, s76
	s_waitcnt vmcnt(19)
	v_cndmask_b32_e64 v57, 0, v57, s[4:5]
	s_cselect_b64 s[4:5], -1, 0
	s_and_b64 s[4:5], vcc, s[4:5]
	s_cmp_lt_i32 s23, s76
	s_waitcnt vmcnt(18)
	v_cndmask_b32_e64 v56, 0, v56, s[4:5]
	s_cselect_b64 s[4:5], -1, 0
	s_and_b64 s[4:5], vcc, s[4:5]
	s_cmp_lt_i32 s30, s76
	s_waitcnt vmcnt(17)
	v_cndmask_b32_e64 v55, 0, v55, s[4:5]
	s_cselect_b64 s[4:5], -1, 0
	s_and_b64 s[4:5], vcc, s[4:5]
	s_cmp_lt_i32 s31, s76
	s_waitcnt vmcnt(16)
	v_cndmask_b32_e64 v54, 0, v54, s[4:5]
	s_cselect_b64 s[4:5], -1, 0
	s_and_b64 s[4:5], vcc, s[4:5]
	s_cmp_lt_i32 s36, s76
	s_waitcnt vmcnt(15)
	v_cndmask_b32_e64 v70, 0, v70, s[4:5]
	s_cselect_b64 s[4:5], -1, 0
	s_and_b64 s[4:5], vcc, s[4:5]
	s_cmp_lt_i32 s37, s76
	s_waitcnt vmcnt(14)
	v_cndmask_b32_e64 v69, 0, v69, s[4:5]
	s_cselect_b64 s[4:5], -1, 0
	s_and_b64 s[4:5], vcc, s[4:5]
	s_cmp_lt_i32 s38, s76
	s_waitcnt vmcnt(13)
	v_cndmask_b32_e64 v68, 0, v68, s[4:5]
	s_cselect_b64 s[4:5], -1, 0
	s_and_b64 s[4:5], vcc, s[4:5]
	s_cmp_lt_i32 s39, s76
	s_waitcnt vmcnt(12)
	v_cndmask_b32_e64 v67, 0, v67, s[4:5]
	s_cselect_b64 s[4:5], -1, 0
	s_and_b64 s[4:5], vcc, s[4:5]
	s_cmp_lt_i32 s34, s76
	s_waitcnt vmcnt(11)
	v_cndmask_b32_e64 v66, 0, v66, s[4:5]
	s_cselect_b64 s[4:5], -1, 0
	s_and_b64 s[4:5], vcc, s[4:5]
	s_cmp_lt_i32 s35, s76
	s_waitcnt vmcnt(10)
	v_cndmask_b32_e64 v64, 0, v64, s[4:5]
	s_cselect_b64 s[4:5], -1, 0
	s_and_b64 s[4:5], vcc, s[4:5]
	s_cmp_lt_i32 s42, s76
	s_waitcnt vmcnt(9)
	v_cndmask_b32_e64 v63, 0, v63, s[4:5]
	s_cselect_b64 s[4:5], -1, 0
	s_and_b64 s[4:5], vcc, s[4:5]
	s_cmp_lt_i32 s43, s76
	s_waitcnt vmcnt(8)
	v_cndmask_b32_e64 v62, 0, v62, s[4:5]
	s_cselect_b64 s[4:5], -1, 0
	s_and_b64 s[4:5], vcc, s[4:5]
	s_cmp_lt_i32 s54, s76
	s_waitcnt vmcnt(7)
	v_cndmask_b32_e64 v65, 0, v65, s[4:5]
	s_cselect_b64 s[4:5], -1, 0
	s_and_b64 s[4:5], vcc, s[4:5]
	s_cmp_lt_i32 s55, s76
	s_waitcnt vmcnt(6)
	v_cndmask_b32_e64 v74, 0, v74, s[4:5]
	s_cselect_b64 s[4:5], -1, 0
	s_and_b64 s[4:5], vcc, s[4:5]
	s_cmp_lt_i32 s46, s76
	ds_write2_b32 v12, v21, v20 offset1:65
	ds_write2_b32 v12, v19, v18 offset0:130 offset1:195
	v_add_u32_e32 v18, 0x400, v12
	s_waitcnt vmcnt(5)
	v_cndmask_b32_e64 v73, 0, v73, s[4:5]
	s_cselect_b64 s[4:5], -1, 0
	ds_write2_b32 v18, v17, v16 offset0:4 offset1:69
	ds_write2_b32 v18, v15, v8 offset0:134 offset1:199
	v_add_u32_e32 v8, 0x800, v12
	s_and_b64 s[4:5], vcc, s[4:5]
	ds_write2_b32 v8, v29, v28 offset0:8 offset1:73
	ds_write2_b32 v8, v27, v26 offset0:138 offset1:203
	v_add_u32_e32 v8, 0xc00, v12
	s_cmp_lt_i32 s47, s76
	ds_write2_b32 v8, v25, v24 offset0:12 offset1:77
	ds_write2_b32 v8, v23, v22 offset0:142 offset1:207
	v_add_u32_e32 v8, 0x1000, v12
	s_waitcnt vmcnt(4)
	v_cndmask_b32_e64 v72, 0, v72, s[4:5]
	s_cselect_b64 s[4:5], -1, 0
	ds_write2_b32 v8, v37, v36 offset0:16 offset1:81
	ds_write2_b32 v8, v35, v34 offset0:146 offset1:211
	v_add_u32_e32 v8, 0x1400, v12
	s_and_b64 s[4:5], vcc, s[4:5]
	ds_write2_b32 v8, v33, v32 offset0:20 offset1:85
	ds_write2_b32 v8, v31, v30 offset0:150 offset1:215
	v_add_u32_e32 v8, 0x1800, v12
	s_cmp_lt_i32 s48, s76
	ds_write2_b32 v8, v45, v44 offset0:24 offset1:89
	ds_write2_b32 v8, v43, v42 offset0:154 offset1:219
	v_add_u32_e32 v8, 0x1c00, v12
	s_waitcnt vmcnt(3)
	v_cndmask_b32_e64 v71, 0, v71, s[4:5]
	s_cselect_b64 s[4:5], -1, 0
	ds_write2_b32 v8, v41, v40 offset0:28 offset1:93
	ds_write2_b32 v8, v39, v38 offset0:158 offset1:223
	v_add_u32_e32 v8, 0x2000, v12
	s_and_b64 s[4:5], vcc, s[4:5]
	ds_write2_b32 v8, v53, v52 offset0:32 offset1:97
	ds_write2_b32 v8, v51, v50 offset0:162 offset1:227
	v_add_u32_e32 v8, 0x2400, v12
	s_cmp_lt_i32 s49, s76
	ds_write2_b32 v8, v49, v48 offset0:36 offset1:101
	ds_write2_b32 v8, v47, v46 offset0:166 offset1:231
	v_add_u32_e32 v8, 0x2800, v12
	s_waitcnt vmcnt(2)
	v_cndmask_b32_e64 v77, 0, v77, s[4:5]
	s_cselect_b64 s[4:5], -1, 0
	ds_write2_b32 v8, v61, v60 offset0:40 offset1:105
	ds_write2_b32 v8, v59, v58 offset0:170 offset1:235
	v_add_u32_e32 v8, 0x2c00, v12
	s_and_b64 s[4:5], vcc, s[4:5]
	ds_write2_b32 v8, v57, v56 offset0:44 offset1:109
	ds_write2_b32 v8, v55, v54 offset0:174 offset1:239
	v_add_u32_e32 v8, 0x3000, v12
	s_cmp_lt_i32 s44, s76
	ds_write2_b32 v8, v70, v69 offset0:48 offset1:113
	ds_write2_b32 v8, v68, v67 offset0:178 offset1:243
	v_add_u32_e32 v8, 0x3400, v12
	s_waitcnt vmcnt(1)
	v_cndmask_b32_e64 v76, 0, v76, s[4:5]
	s_cselect_b64 s[4:5], -1, 0
	ds_write2_b32 v8, v66, v64 offset0:52 offset1:117
	ds_write2_b32 v8, v63, v62 offset0:182 offset1:247
	v_add_u32_e32 v8, 0x3800, v12
	s_and_b64 vcc, vcc, s[4:5]
	ds_write2_b32 v8, v65, v74 offset0:56 offset1:121
	ds_write2_b32 v8, v73, v72 offset0:186 offset1:251
	v_add_u32_e32 v8, 0x3c00, v12
	s_waitcnt vmcnt(0)
	v_cndmask_b32_e32 v75, 0, v75, vcc
	ds_write2_b32 v8, v71, v77 offset0:60 offset1:125
	ds_write2_b32 v8, v76, v75 offset0:190 offset1:255
	s_waitcnt lgkmcnt(0)
	ds_read2_b32 v[16:17], v14 offset1:65
	v_add_u32_e32 v24, s59, v13
	v_mul_lo_u32 v22, s57, v24
	s_ashr_i32 s59, s58, 31
	v_readlane_b32 s76, v254, 31
	s_waitcnt lgkmcnt(0)
; __device__ __forceinline__ unsigned cvt_pk_bf16(float lo, float hi) { unsigned r; asm volatile("v_cvt_pk_bf16_f32 %0, %1, %2" : "=v"(r) : "v"(lo), "v"(hi)); return r; }
; #define LAS __attribute__((address_space(3)))
; __device__ __forceinline__ void conv_store(const ConvItem& ci, LAS float* scr, int lane, const float (&v)[64]) {
;     ...
; #pragma unroll
;     for (int j = 0; j < 8; ++j) { const int n = (lane >> 3) + 8 * j; const LAS float* s = scr + (8 * c) * 65 + n;
;         v4u o; o.x = cvt_pk_bf16(s[0 * 65] * s0[0], s[1 * 65] * s0[1]); o.y = cvt_pk_bf16(s[2 * 65] * s0[2], s[3 * 65] * s0[3]); o.z = cvt_pk_bf16(s[4 * 65] * s1[0], s[5 * 65] * s1[1]); o.w = cvt_pk_bf16(s[6 * 65] * s1[2], s[7 * 65] * s1[3]);
;         *(v4u*)(ci.dst + (size_t)(ci.drow0 + n) * ci.ldd + ci.k0 + 8 * c) = o; }
	v_mul_f32_e32 v8, v4, v16
	v_mul_f32_e32 v15, v5, v17
	v_cvt_pk_bf16_f32 v16, v8, v15
	ds_read2_b32 v[18:19], v14 offset0:130 offset1:195
	s_add_i32 s3, s3, s33
	s_add_i32 s66, s66, s67
	s_add_i32 s68, s68, s69
	s_add_i32 s70, s70, s71
	s_waitcnt lgkmcnt(0)
	v_mul_f32_e32 v15, v7, v19
	v_mul_f32_e32 v8, v6, v18
	v_cvt_pk_bf16_f32 v17, v8, v15
	v_add_u32_e32 v15, 0x400, v14
	ds_read2_b32 v[18:19], v15 offset0:4 offset1:69
	s_add_i32 s72, s72, s73
	s_add_i32 s74, s74, s75
	v_readlane_b32 s78, v254, 33
	v_readlane_b32 s79, v254, 34
	s_waitcnt lgkmcnt(0)
	v_mul_f32_e32 v8, v0, v18
	v_mul_f32_e32 v18, v1, v19
	v_cvt_pk_bf16_f32 v18, v8, v18
	ds_read2_b32 v[20:21], v15 offset0:134 offset1:199
	v_readlane_b32 s80, v255, 21
	v_readlane_b32 s77, v254, 32
	s_movk_i32 s78, 0x1580
	v_readlane_b32 s82, v255, 23
	s_waitcnt lgkmcnt(0)
	v_mul_f32_e32 v8, v2, v20
	v_mul_f32_e32 v19, v3, v21
	v_cvt_pk_bf16_f32 v19, v8, v19
	v_ashrrev_i32_e32 v8, 31, v24
	v_mul_lo_u32 v8, s56, v8
	v_mad_u64_u32 v[20:21], s[4:5], s56, v24, 0
	v_add3_u32 v21, v21, v8, v22
	ds_read2_b32 v[22:23], v14 offset0:8 offset1:73
	v_lshl_add_u64 v[20:21], v[20:21], 1, s[60:61]
	s_lshl_b64 s[4:5], s[58:59], 1
	v_lshl_add_u64 v[20:21], v[20:21], 0, s[4:5]
	v_lshlrev_b32_e32 v8, 1, v10
	v_lshl_add_u64 v[20:21], v[20:21], 0, v[8:9]
	global_store_dwordx4 v[20:21], v[16:19], off
	s_cmpk_lt_i32 s3, 16768
	v_readlane_b32 s83, v255, 24
	s_waitcnt lgkmcnt(0)
	v_mul_f32_e32 v16, v4, v22
	v_mul_f32_e32 v17, v5, v23
	v_cvt_pk_bf16_f32 v16, v16, v17
	ds_read2_b32 v[18:19], v14 offset0:138 offset1:203
	s_mov_b32 s79, 0x3f22f983
	s_mov_b32 s85, 0xbfc90fda
	s_brev_b32 s86, 1
	s_movk_i32 s87, 0x1f8
	s_waitcnt lgkmcnt(0)
	v_mul_f32_e32 v17, v6, v18
	v_mul_f32_e32 v18, v7, v19
	v_cvt_pk_bf16_f32 v17, v17, v18
	ds_read2_b32 v[18:19], v15 offset0:12 offset1:77
	s_mov_b64 s[88:89], 0x80
	s_mov_b64 s[92:93], 0x4000
	s_mov_b64 s[94:95], 0x4800
	v_readlane_b32 s81, v255, 22
	s_waitcnt lgkmcnt(0)
	v_mul_f32_e32 v18, v0, v18
	v_mul_f32_e32 v19, v1, v19
	v_cvt_pk_bf16_f32 v18, v18, v19
	ds_read2_b32 v[20:21], v15 offset0:142 offset1:207
	s_waitcnt lgkmcnt(0)
	v_mul_f32_e32 v19, v2, v20
	v_mul_f32_e32 v20, v3, v21
	v_cvt_pk_bf16_f32 v19, v19, v20
	v_add_u32_e32 v20, 8, v24
	v_ashrrev_i32_e32 v21, 31, v20
	v_mul_lo_u32 v22, s56, v21
	v_mul_lo_u32 v23, s57, v20
	v_mad_u64_u32 v[20:21], s[6:7], s56, v20, 0
	v_add3_u32 v21, v21, v22, v23
	ds_read2_b32 v[22:23], v14 offset0:16 offset1:81
	v_lshl_add_u64 v[20:21], v[20:21], 1, s[60:61]
	v_lshl_add_u64 v[20:21], v[20:21], 0, s[4:5]
	v_lshl_add_u64 v[20:21], v[20:21], 0, v[8:9]
	global_store_dwordx4 v[20:21], v[16:19], off
	s_waitcnt lgkmcnt(0)
	s_nop 0
	v_mul_f32_e32 v16, v4, v22
	v_mul_f32_e32 v17, v5, v23
	v_cvt_pk_bf16_f32 v16, v16, v17
	ds_read2_b32 v[18:19], v14 offset0:146 offset1:211
	s_waitcnt lgkmcnt(0)
	v_mul_f32_e32 v17, v6, v18
	v_mul_f32_e32 v18, v7, v19
	v_cvt_pk_bf16_f32 v17, v17, v18
	ds_read2_b32 v[18:19], v15 offset0:20 offset1:85
	s_waitcnt lgkmcnt(0)
	v_mul_f32_e32 v18, v0, v18
	v_mul_f32_e32 v19, v1, v19
	v_cvt_pk_bf16_f32 v18, v18, v19
	ds_read2_b32 v[20:21], v15 offset0:150 offset1:215
	s_waitcnt lgkmcnt(0)
	v_mul_f32_e32 v19, v2, v20
	v_mul_f32_e32 v20, v3, v21
	v_cvt_pk_bf16_f32 v19, v19, v20
	v_add_u32_e32 v20, 16, v24
	v_ashrrev_i32_e32 v21, 31, v20
	v_mul_lo_u32 v22, s56, v21
	v_mul_lo_u32 v23, s57, v20
	v_mad_u64_u32 v[20:21], s[6:7], s56, v20, 0
	v_add3_u32 v21, v21, v22, v23
	ds_read2_b32 v[22:23], v14 offset0:24 offset1:89
	v_lshl_add_u64 v[20:21], v[20:21], 1, s[60:61]
	v_lshl_add_u64 v[20:21], v[20:21], 0, s[4:5]
	v_lshl_add_u64 v[20:21], v[20:21], 0, v[8:9]
	global_store_dwordx4 v[20:21], v[16:19], off
	s_waitcnt lgkmcnt(0)
	s_nop 0
	v_mul_f32_e32 v16, v4, v22
	v_mul_f32_e32 v17, v5, v23
	v_cvt_pk_bf16_f32 v16, v16, v17
	ds_read2_b32 v[18:19], v14 offset0:154 offset1:219
	s_waitcnt lgkmcnt(0)
	v_mul_f32_e32 v17, v6, v18
	v_mul_f32_e32 v18, v7, v19
	v_cvt_pk_bf16_f32 v17, v17, v18
	ds_read2_b32 v[18:19], v15 offset0:28 offset1:93
	s_waitcnt lgkmcnt(0)
	v_mul_f32_e32 v18, v0, v18
	v_mul_f32_e32 v19, v1, v19
	v_cvt_pk_bf16_f32 v18, v18, v19
	ds_read2_b32 v[20:21], v15 offset0:158 offset1:223
	s_waitcnt lgkmcnt(0)
; __device__ __forceinline__ unsigned cvt_pk_bf16(float lo, float hi) { unsigned r; asm volatile("v_cvt_pk_bf16_f32 %0, %1, %2" : "=v"(r) : "v"(lo), "v"(hi)); return r; }
; #define LAS __attribute__((address_space(3)))
; #define LDS_WAIT() asm volatile("s_waitcnt lgkmcnt(0)" ::: "memory")
; __device__ __forceinline__ void conv_store(const ConvItem& ci, LAS float* scr, int lane, const float (&v)[64]) {
;     ...
; #pragma unroll
;     for (int j = 0; j < 8; ++j) { const int n = (lane >> 3) + 8 * j; const LAS float* s = scr + (8 * c) * 65 + n;
;         v4u o; o.x = cvt_pk_bf16(s[0 * 65] * s0[0], s[1 * 65] * s0[1]); o.y = cvt_pk_bf16(s[2 * 65] * s0[2], s[3 * 65] * s0[3]); o.z = cvt_pk_bf16(s[4 * 65] * s1[0], s[5 * 65] * s1[1]); o.w = cvt_pk_bf16(s[6 * 65] * s1[2], s[7 * 65] * s1[3]);
;         *(v4u*)(ci.dst + (size_t)(ci.drow0 + n) * ci.ldd + ci.k0 + 8 * c) = o; }
;     LDS_WAIT(); asm volatile("" ::: "memory");
; }
	v_mul_f32_e32 v19, v2, v20
	v_mul_f32_e32 v20, v3, v21
	v_cvt_pk_bf16_f32 v19, v19, v20
	v_add_u32_e32 v20, 24, v24
	v_ashrrev_i32_e32 v21, 31, v20
	v_mul_lo_u32 v22, s56, v21
	v_mul_lo_u32 v23, s57, v20
	v_mad_u64_u32 v[20:21], s[6:7], s56, v20, 0
	v_add3_u32 v21, v21, v22, v23
	ds_read2_b32 v[22:23], v14 offset0:32 offset1:97
	v_lshl_add_u64 v[20:21], v[20:21], 1, s[60:61]
	v_lshl_add_u64 v[20:21], v[20:21], 0, s[4:5]
	v_lshl_add_u64 v[20:21], v[20:21], 0, v[8:9]
	global_store_dwordx4 v[20:21], v[16:19], off
	s_waitcnt lgkmcnt(0)
	s_nop 0
	v_mul_f32_e32 v16, v4, v22
	v_mul_f32_e32 v17, v5, v23
	v_cvt_pk_bf16_f32 v16, v16, v17
	ds_read2_b32 v[18:19], v14 offset0:162 offset1:227
	s_waitcnt lgkmcnt(0)
	v_mul_f32_e32 v17, v6, v18
	v_mul_f32_e32 v18, v7, v19
	v_cvt_pk_bf16_f32 v17, v17, v18
	ds_read2_b32 v[18:19], v15 offset0:36 offset1:101
	s_waitcnt lgkmcnt(0)
	v_mul_f32_e32 v18, v0, v18
	v_mul_f32_e32 v19, v1, v19
	v_cvt_pk_bf16_f32 v18, v18, v19
	ds_read2_b32 v[20:21], v15 offset0:166 offset1:231
	s_waitcnt lgkmcnt(0)
	v_mul_f32_e32 v19, v2, v20
	v_mul_f32_e32 v20, v3, v21
	v_cvt_pk_bf16_f32 v19, v19, v20
	v_add_u32_e32 v20, 32, v24
	v_ashrrev_i32_e32 v21, 31, v20
	v_mul_lo_u32 v22, s56, v21
	v_mul_lo_u32 v23, s57, v20
	v_mad_u64_u32 v[20:21], s[6:7], s56, v20, 0
	v_add3_u32 v21, v21, v22, v23
	ds_read2_b32 v[22:23], v14 offset0:40 offset1:105
	v_lshl_add_u64 v[20:21], v[20:21], 1, s[60:61]
	v_lshl_add_u64 v[20:21], v[20:21], 0, s[4:5]
	v_lshl_add_u64 v[20:21], v[20:21], 0, v[8:9]
	global_store_dwordx4 v[20:21], v[16:19], off
	s_waitcnt lgkmcnt(0)
	s_nop 0
	v_mul_f32_e32 v16, v4, v22
	v_mul_f32_e32 v17, v5, v23
	v_cvt_pk_bf16_f32 v16, v16, v17
	ds_read2_b32 v[18:19], v14 offset0:170 offset1:235
	s_waitcnt lgkmcnt(0)
	v_mul_f32_e32 v17, v6, v18
	v_mul_f32_e32 v18, v7, v19
	v_cvt_pk_bf16_f32 v17, v17, v18
	ds_read2_b32 v[18:19], v15 offset0:44 offset1:109
	s_waitcnt lgkmcnt(0)
	v_mul_f32_e32 v18, v0, v18
	v_mul_f32_e32 v19, v1, v19
	v_cvt_pk_bf16_f32 v18, v18, v19
	ds_read2_b32 v[20:21], v15 offset0:174 offset1:239
	s_waitcnt lgkmcnt(0)
	v_mul_f32_e32 v19, v2, v20
	v_mul_f32_e32 v20, v3, v21
	v_cvt_pk_bf16_f32 v19, v19, v20
	v_add_u32_e32 v20, 40, v24
	v_ashrrev_i32_e32 v21, 31, v20
	v_mul_lo_u32 v22, s56, v21
	v_mul_lo_u32 v23, s57, v20
	v_mad_u64_u32 v[20:21], s[6:7], s56, v20, 0
	v_add3_u32 v21, v21, v22, v23
	ds_read2_b32 v[22:23], v14 offset0:48 offset1:113
	v_lshl_add_u64 v[20:21], v[20:21], 1, s[60:61]
	v_lshl_add_u64 v[20:21], v[20:21], 0, s[4:5]
	v_lshl_add_u64 v[20:21], v[20:21], 0, v[8:9]
	global_store_dwordx4 v[20:21], v[16:19], off
	s_waitcnt lgkmcnt(0)
	s_nop 0
	v_mul_f32_e32 v16, v4, v22
	v_mul_f32_e32 v17, v5, v23
	v_cvt_pk_bf16_f32 v16, v16, v17
	ds_read2_b32 v[18:19], v14 offset0:178 offset1:243
	s_waitcnt lgkmcnt(0)
	v_mul_f32_e32 v17, v6, v18
	v_mul_f32_e32 v18, v7, v19
	v_cvt_pk_bf16_f32 v17, v17, v18
	ds_read2_b32 v[18:19], v15 offset0:52 offset1:117
	s_waitcnt lgkmcnt(0)
	v_mul_f32_e32 v18, v0, v18
	v_mul_f32_e32 v19, v1, v19
	v_cvt_pk_bf16_f32 v18, v18, v19
	ds_read2_b32 v[20:21], v15 offset0:182 offset1:247
	s_waitcnt lgkmcnt(0)
	v_mul_f32_e32 v19, v2, v20
	v_mul_f32_e32 v20, v3, v21
	v_cvt_pk_bf16_f32 v19, v19, v20
	v_add_u32_e32 v20, 48, v24
	v_ashrrev_i32_e32 v21, 31, v20
	v_mul_lo_u32 v22, s56, v21
	v_mul_lo_u32 v23, s57, v20
	v_mad_u64_u32 v[20:21], s[6:7], s56, v20, 0
	v_add3_u32 v21, v21, v22, v23
	ds_read2_b32 v[22:23], v14 offset0:56 offset1:121
	v_lshl_add_u64 v[20:21], v[20:21], 1, s[60:61]
	v_lshl_add_u64 v[20:21], v[20:21], 0, s[4:5]
	v_lshl_add_u64 v[20:21], v[20:21], 0, v[8:9]
	global_store_dwordx4 v[20:21], v[16:19], off
	s_waitcnt lgkmcnt(0)
	v_mul_f32_e32 v4, v4, v22
	v_mul_f32_e32 v5, v5, v23
	v_cvt_pk_bf16_f32 v4, v4, v5
	ds_read2_b32 v[16:17], v14 offset0:186 offset1:251
	s_waitcnt lgkmcnt(0)
	v_mul_f32_e32 v5, v6, v16
	v_mul_f32_e32 v6, v7, v17
	v_cvt_pk_bf16_f32 v5, v5, v6
	ds_read2_b32 v[6:7], v15 offset0:60 offset1:125
	s_waitcnt lgkmcnt(0)
	v_mul_f32_e32 v0, v0, v6
	v_mul_f32_e32 v1, v1, v7
	v_cvt_pk_bf16_f32 v6, v0, v1
	ds_read2_b32 v[0:1], v15 offset0:190 offset1:255
	s_waitcnt lgkmcnt(0)
	v_mul_f32_e32 v0, v2, v0
	v_mul_f32_e32 v1, v3, v1
	v_cvt_pk_bf16_f32 v7, v0, v1
	v_add_u32_e32 v0, 56, v24
	v_ashrrev_i32_e32 v1, 31, v0
	v_mul_lo_u32 v2, s56, v1
	v_mul_lo_u32 v3, s57, v0
	v_mad_u64_u32 v[0:1], s[6:7], s56, v0, 0
	v_add3_u32 v1, v1, v2, v3
	v_lshl_add_u64 v[0:1], v[0:1], 1, s[60:61]
	v_lshl_add_u64 v[0:1], v[0:1], 0, s[4:5]
	v_lshl_add_u64 v[0:1], v[0:1], 0, v[8:9]
	global_store_dwordx4 v[0:1], v[4:7], off
	s_waitcnt lgkmcnt(0)
	s_cbranch_scc0 .Lcvp130_ret
